# one priority raise per MFMA segment: removed the drop-and-raise pair between the two 16-MFMA halves of every K-loop slot
# baseline (speedup 1.0000x reference)
; #define PG8_STAGE(bufoff, gbase, voff) do { _Pragma("unroll") for (int _i = 0; _i < 2; ++_i) \
;         __builtin_amdgcn_global_load_lds((const unsigned*)((const char*)(gbase) + (voff)[_i]), (PG8_LAS unsigned*)(lds + (bufoff) + ldsw + _i * 8192), 16, 0, 0); } while (0)
; #define PG8_LDA(dst, b, h) do { if constexpr (FP8) { _Pragma("unroll") for (int m = 0; m < 4; ++m) dst##8[m] = pg8_ld8(lds + PG8_SA(b, h) + aoff + m * 2048); } \
;         else { _Pragma("unroll") for (int m = 0; m < 4; ++m) _Pragma("unroll") for (int k = 0; k < 2; ++k) dst[m][k] = *(const PG8_LAS bf16x8*)(lds + PG8_SA(b, h) + aoff + m * 2048 + k * 1024); } } while (0)
; #define PG8_LDB(dst, b, h) do { if constexpr (FP8) { _Pragma("unroll") for (int n = 0; n < 2; ++n) dst##8[n] = pg8_ld8(lds + PG8_SB(b, h) + boff + n * 2048); } \
;         else { _Pragma("unroll") for (int n = 0; n < 2; ++n) _Pragma("unroll") for (int k = 0; k < 2; ++k) dst[n][k] = *(const PG8_LAS bf16x8*)(lds + PG8_SB(b, h) + boff + n * 2048 + k * 1024); } } while (0)
; #define PG8_WAIT_V(n) asm volatile("s_waitcnt vmcnt(" #n ")" ::: "memory")
; #define PG8_WAIT_L(n) asm volatile("s_waitcnt lgkmcnt(" #n ")" ::: "memory")
; #define PG8_BAR __builtin_amdgcn_s_barrier()
; #define PG8_SCHED __builtin_amdgcn_sched_barrier(0)
;     ...
;             PG8_LDB(B0, 0, 0); PG8_LDB(B1, 0, 1); PG8_SCHED; PG8_LDA(At, 0, 0); PG8_STAGE(PG8_SA(1, 1), a1 + hstep, voffA);
;             PG8_WAIT_V(8); PG8_WAIT_L(0); PG8_BAR; PG8_MMA(0, 0, At, B0); PG8_MMA(0, 1, At, B1); PG8_BAR; PG8_SCHED;
;             PG8_LDA(At, 0, 1); PG8_STAGE(PG8_SB(0, 0), b2, voffB); PG8_STAGE(PG8_SB(0, 1), b2 + hstep, voffB); PG8_STAGE(PG8_SA(0, 0), a2, voffA);
;             PG8_WAIT_V(8); PG8_WAIT_L(0); PG8_BAR; PG8_MMA(1, 0, At, B0); PG8_MMA(1, 1, At, B1); PG8_BAR; PG8_SCHED;
.LBB0_154:
	s_add_u32 s0, s20, 0xfffc0080
	s_addc_u32 s1, s21, -1
	s_add_i32 s43, 0, 0x10000
	s_cmp_eq_u32 s42, 12
	s_cselect_b32 s23, s5, s1
	s_cselect_b32 s22, s13, s0
	v_add_u32_e32 v80, s43, v156
	s_cselect_b32 s1, s11, s41
	s_cselect_b32 s0, s19, s40
	s_add_i32 s46, 0, 0x14000
	ds_read_b128 v[144:147], v80
	ds_read_b128 v[152:155], v80 offset:1024
	ds_read_b128 v[174:177], v80 offset:2048
	ds_read_b128 v[178:181], v80 offset:3072
	v_add_u32_e32 v80, s46, v156
	ds_read_b128 v[182:185], v80
	ds_read_b128 v[186:189], v80 offset:1024
	ds_read_b128 v[206:209], v80 offset:2048
	ds_read_b128 v[210:213], v80 offset:3072
	v_lshl_add_u64 v[148:149], s[20:21], 0, v[142:143]
	s_add_i32 m0, s29, 0xc000
	ds_read_b128 v[214:217], v158
	ds_read_b128 v[218:221], v158 offset:1024
	ds_read_b128 v[222:225], v158 offset:2048
	ds_read_b128 v[226:229], v158 offset:3072
	ds_read_b128 v[230:233], v158 offset:4096
	ds_read_b128 v[234:237], v158 offset:5120
	ds_read_b128 v[238:241], v158 offset:6144
	ds_read_b128 v[242:245], v158 offset:7168
	global_load_lds_dwordx4 v[148:149], off
	v_lshl_add_u64 v[148:149], s[20:21], 0, v[140:141]
	s_add_i32 m0, s29, 0xe000
	s_nop 0
	global_load_lds_dwordx4 v[148:149], off
	s_waitcnt vmcnt(8)
	s_waitcnt lgkmcnt(0)
	s_barrier
	s_setprio 1
	s_waitcnt lgkmcnt(0)
	v_mfma_f32_16x16x32_f16 v[126:129], v[144:147], v[214:217], v[126:129]
	v_mfma_f32_16x16x32_f16 v[122:125], v[174:177], v[214:217], v[122:125]
	v_mfma_f32_16x16x32_f16 v[114:117], v[144:147], v[222:225], v[114:117]
	v_mfma_f32_16x16x32_f16 v[106:109], v[174:177], v[222:225], v[106:109]
	v_mfma_f32_16x16x32_f16 v[98:101], v[144:147], v[230:233], v[98:101]
	v_mfma_f32_16x16x32_f16 v[90:93], v[174:177], v[230:233], v[90:93]
	v_mfma_f32_16x16x32_f16 v[82:85], v[144:147], v[238:241], v[82:85]
	v_mfma_f32_16x16x32_f16 v[72:75], v[174:177], v[238:241], v[72:75]
	v_mfma_f32_16x16x32_f16 v[126:129], v[152:155], v[218:221], v[126:129]
	v_mfma_f32_16x16x32_f16 v[122:125], v[178:181], v[218:221], v[122:125]
	v_mfma_f32_16x16x32_f16 v[114:117], v[152:155], v[226:229], v[114:117]
	v_mfma_f32_16x16x32_f16 v[106:109], v[178:181], v[226:229], v[106:109]
	v_mfma_f32_16x16x32_f16 v[98:101], v[152:155], v[234:237], v[98:101]
	v_mfma_f32_16x16x32_f16 v[90:93], v[178:181], v[234:237], v[90:93]
	v_mfma_f32_16x16x32_f16 v[82:85], v[152:155], v[242:245], v[82:85]
	v_mfma_f32_16x16x32_f16 v[72:75], v[178:181], v[242:245], v[72:75]
	v_mfma_f32_16x16x32_f16 v[118:121], v[182:185], v[214:217], v[118:121]
	v_mfma_f32_16x16x32_f16 v[110:113], v[206:209], v[214:217], v[110:113]
	v_mfma_f32_16x16x32_f16 v[102:105], v[182:185], v[222:225], v[102:105]
	v_mfma_f32_16x16x32_f16 v[94:97], v[206:209], v[222:225], v[94:97]
	v_mfma_f32_16x16x32_f16 v[86:89], v[182:185], v[230:233], v[86:89]
	v_mfma_f32_16x16x32_f16 v[76:79], v[206:209], v[230:233], v[76:79]
	v_mfma_f32_16x16x32_f16 v[68:71], v[182:185], v[238:241], v[68:71]
	v_mfma_f32_16x16x32_f16 v[64:67], v[206:209], v[238:241], v[64:67]
	v_mfma_f32_16x16x32_f16 v[118:121], v[186:189], v[218:221], v[118:121]
	v_mfma_f32_16x16x32_f16 v[110:113], v[210:213], v[218:221], v[110:113]
	v_mfma_f32_16x16x32_f16 v[102:105], v[186:189], v[226:229], v[102:105]
	v_mfma_f32_16x16x32_f16 v[94:97], v[210:213], v[226:229], v[94:97]
	v_mfma_f32_16x16x32_f16 v[86:89], v[186:189], v[234:237], v[86:89]
	v_mfma_f32_16x16x32_f16 v[76:79], v[210:213], v[234:237], v[76:79]
	v_mfma_f32_16x16x32_f16 v[68:71], v[186:189], v[242:245], v[68:71]
	v_mfma_f32_16x16x32_f16 v[64:67], v[210:213], v[242:245], v[64:67]
	s_setprio 0
	s_barrier
	s_add_i32 s43, s43, s25
	v_lshl_add_u64 v[148:149], s[0:1], 0, v[134:135]
	s_mov_b32 m0, s43
	ds_read_b128 v[214:217], v158 offset:16384
	ds_read_b128 v[218:221], v158 offset:17408
	ds_read_b128 v[222:225], v158 offset:18432
	ds_read_b128 v[226:229], v158 offset:19456
	ds_read_b128 v[230:233], v158 offset:20480
	ds_read_b128 v[234:237], v158 offset:21504
	ds_read_b128 v[238:241], v158 offset:22528
	ds_read_b128 v[242:245], v158 offset:23552
	global_load_lds_dwordx4 v[148:149], off
	s_add_i32 m0, s43, 0x2000
	s_add_u32 s44, s0, 0x40000
	v_lshl_add_u64 v[160:161], s[0:1], 0, v[130:131]
	s_addc_u32 s45, s1, 0
	s_add_i32 s43, s46, s25
	global_load_lds_dwordx4 v[160:161], off
	v_lshl_add_u64 v[190:191], s[44:45], 0, v[134:135]
	s_mov_b32 m0, s43
	v_lshl_add_u64 v[246:247], s[22:23], 0, v[132:133]
	global_load_lds_dwordx4 v[190:191], off
	v_lshl_add_u64 v[190:191], s[44:45], 0, v[130:131]
	s_add_i32 m0, s43, 0x2000
	s_nop 0
	global_load_lds_dwordx4 v[190:191], off
	v_lshl_add_u64 v[190:191], s[22:23], 0, v[136:137]
	s_mov_b32 m0, s29
	s_nop 0
	global_load_lds_dwordx4 v[190:191], off
	s_mov_b32 m0, s30
	s_nop 0
	global_load_lds_dwordx4 v[246:247], off
	s_waitcnt vmcnt(8)
	s_waitcnt lgkmcnt(0)
	s_barrier
; #define PG8_STAGE(bufoff, gbase, voff) do { _Pragma("unroll") for (int _i = 0; _i < 2; ++_i) \
;         __builtin_amdgcn_global_load_lds((const unsigned*)((const char*)(gbase) + (voff)[_i]), (PG8_LAS unsigned*)(lds + (bufoff) + ldsw + _i * 8192), 16, 0, 0); } while (0)
; #define PG8_LDA(dst, b, h) do { if constexpr (FP8) { _Pragma("unroll") for (int m = 0; m < 4; ++m) dst##8[m] = pg8_ld8(lds + PG8_SA(b, h) + aoff + m * 2048); } \
;         else { _Pragma("unroll") for (int m = 0; m < 4; ++m) _Pragma("unroll") for (int k = 0; k < 2; ++k) dst[m][k] = *(const PG8_LAS bf16x8*)(lds + PG8_SA(b, h) + aoff + m * 2048 + k * 1024); } } while (0)
; #define PG8_LDB(dst, b, h) do { if constexpr (FP8) { _Pragma("unroll") for (int n = 0; n < 2; ++n) dst##8[n] = pg8_ld8(lds + PG8_SB(b, h) + boff + n * 2048); } \
;         else { _Pragma("unroll") for (int n = 0; n < 2; ++n) _Pragma("unroll") for (int k = 0; k < 2; ++k) dst[n][k] = *(const PG8_LAS bf16x8*)(lds + PG8_SB(b, h) + boff + n * 2048 + k * 1024); } } while (0)
; #define PG8_WAIT_V(n) asm volatile("s_waitcnt vmcnt(" #n ")" ::: "memory")
; #define PG8_WAIT_L(n) asm volatile("s_waitcnt lgkmcnt(" #n ")" ::: "memory")
; #define PG8_BAR __builtin_amdgcn_s_barrier()
; #define PG8_SCHED __builtin_amdgcn_sched_barrier(0)
;     ...
;             PG8_WAIT_V(8); PG8_WAIT_L(0); PG8_BAR; PG8_MMA(0, 0, At, B0); PG8_MMA(0, 1, At, B1); PG8_BAR; PG8_SCHED;
;             PG8_LDA(At, 0, 1); PG8_STAGE(PG8_SB(0, 0), b2, voffB); PG8_STAGE(PG8_SB(0, 1), b2 + hstep, voffB); PG8_STAGE(PG8_SA(0, 0), a2, voffA);
;             PG8_WAIT_V(8); PG8_WAIT_L(0); PG8_BAR; PG8_MMA(1, 0, At, B0); PG8_MMA(1, 1, At, B1); PG8_BAR; PG8_SCHED;
;             PG8_LDB(B0, 1, 0); PG8_LDB(B1, 1, 1); PG8_SCHED; PG8_LDA(At, 1, 0); PG8_STAGE(PG8_SA(0, 1), a2 + hstep, voffA);
;             PG8_WAIT_V(8); PG8_WAIT_L(0); PG8_BAR; PG8_MMA(0, 0, At, B0); PG8_MMA(0, 1, At, B1); PG8_BAR; PG8_SCHED;
	s_setprio 1
	s_waitcnt lgkmcnt(0)
	v_mfma_f32_16x16x32_f16 v[60:63], v[144:147], v[214:217], v[60:63]
	v_mfma_f32_16x16x32_f16 v[56:59], v[174:177], v[214:217], v[56:59]
	v_mfma_f32_16x16x32_f16 v[52:55], v[144:147], v[222:225], v[52:55]
	v_mfma_f32_16x16x32_f16 v[44:47], v[174:177], v[222:225], v[44:47]
	v_mfma_f32_16x16x32_f16 v[36:39], v[144:147], v[230:233], v[36:39]
	v_mfma_f32_16x16x32_f16 v[28:31], v[174:177], v[230:233], v[28:31]
	v_mfma_f32_16x16x32_f16 v[20:23], v[144:147], v[238:241], v[20:23]
	v_mfma_f32_16x16x32_f16 v[12:15], v[174:177], v[238:241], v[12:15]
	v_mfma_f32_16x16x32_f16 v[60:63], v[152:155], v[218:221], v[60:63]
	v_mfma_f32_16x16x32_f16 v[56:59], v[178:181], v[218:221], v[56:59]
	v_mfma_f32_16x16x32_f16 v[52:55], v[152:155], v[226:229], v[52:55]
	v_mfma_f32_16x16x32_f16 v[44:47], v[178:181], v[226:229], v[44:47]
	v_mfma_f32_16x16x32_f16 v[36:39], v[152:155], v[234:237], v[36:39]
	v_mfma_f32_16x16x32_f16 v[28:31], v[178:181], v[234:237], v[28:31]
	v_mfma_f32_16x16x32_f16 v[20:23], v[152:155], v[242:245], v[20:23]
	v_mfma_f32_16x16x32_f16 v[12:15], v[178:181], v[242:245], v[12:15]
	v_mfma_f32_16x16x32_f16 v[48:51], v[182:185], v[214:217], v[48:51]
	v_mfma_f32_16x16x32_f16 v[40:43], v[206:209], v[214:217], v[40:43]
	v_mfma_f32_16x16x32_f16 v[32:35], v[182:185], v[222:225], v[32:35]
	v_mfma_f32_16x16x32_f16 v[24:27], v[206:209], v[222:225], v[24:27]
	v_mfma_f32_16x16x32_f16 v[16:19], v[182:185], v[230:233], v[16:19]
	v_mfma_f32_16x16x32_f16 v[8:11], v[206:209], v[230:233], v[8:11]
	v_mfma_f32_16x16x32_f16 v[4:7], v[182:185], v[238:241], v[4:7]
	v_mfma_f32_16x16x32_f16 v[0:3], v[206:209], v[238:241], v[0:3]
	v_mfma_f32_16x16x32_f16 v[48:51], v[186:189], v[218:221], v[48:51]
	v_mfma_f32_16x16x32_f16 v[40:43], v[210:213], v[218:221], v[40:43]
	v_mfma_f32_16x16x32_f16 v[32:35], v[186:189], v[226:229], v[32:35]
	v_mfma_f32_16x16x32_f16 v[24:27], v[210:213], v[226:229], v[24:27]
	v_mfma_f32_16x16x32_f16 v[16:19], v[186:189], v[234:237], v[16:19]
	v_mfma_f32_16x16x32_f16 v[8:11], v[210:213], v[234:237], v[8:11]
	v_mfma_f32_16x16x32_f16 v[4:7], v[186:189], v[242:245], v[4:7]
	v_mfma_f32_16x16x32_f16 v[0:3], v[210:213], v[242:245], v[0:3]
	s_setprio 0
	s_barrier
	s_add_i32 s43, 0, 0x18000
	v_add_u32_e32 v80, s43, v156
	s_add_i32 s44, 0, 0x1c000
	ds_read_b128 v[144:147], v80
	ds_read_b128 v[152:155], v80 offset:1024
	ds_read_b128 v[174:177], v80 offset:2048
	ds_read_b128 v[178:181], v80 offset:3072
	v_add_u32_e32 v80, s44, v156
	ds_read_b128 v[182:185], v80
	ds_read_b128 v[186:189], v80 offset:1024
	ds_read_b128 v[206:209], v80 offset:2048
	ds_read_b128 v[210:213], v80 offset:3072
	s_add_u32 s22, s22, 0x40000
	s_addc_u32 s23, s23, 0
	s_mov_b32 m0, s31
	v_lshl_add_u64 v[248:249], s[22:23], 0, v[136:137]
	ds_read_b128 v[214:217], v158 offset:32768
	ds_read_b128 v[218:221], v158 offset:33792
	ds_read_b128 v[222:225], v158 offset:34816
	ds_read_b128 v[226:229], v158 offset:35840
	ds_read_b128 v[230:233], v158 offset:36864
	ds_read_b128 v[234:237], v158 offset:37888
	ds_read_b128 v[238:241], v158 offset:38912
	ds_read_b128 v[242:245], v158 offset:39936
	global_load_lds_dwordx4 v[248:249], off
	v_lshl_add_u64 v[248:249], s[22:23], 0, v[132:133]
	s_mov_b32 m0, s34
	s_nop 0
	global_load_lds_dwordx4 v[248:249], off
	s_waitcnt vmcnt(8)
	s_waitcnt lgkmcnt(0)
	s_barrier
	s_setprio 1
	s_waitcnt lgkmcnt(0)
	v_mfma_f32_16x16x32_f16 v[126:129], v[144:147], v[214:217], v[126:129]
	v_mfma_f32_16x16x32_f16 v[122:125], v[174:177], v[214:217], v[122:125]
	v_mfma_f32_16x16x32_f16 v[114:117], v[144:147], v[222:225], v[114:117]
	v_mfma_f32_16x16x32_f16 v[106:109], v[174:177], v[222:225], v[106:109]
	v_mfma_f32_16x16x32_f16 v[98:101], v[144:147], v[230:233], v[98:101]
	v_mfma_f32_16x16x32_f16 v[90:93], v[174:177], v[230:233], v[90:93]
	v_mfma_f32_16x16x32_f16 v[82:85], v[144:147], v[238:241], v[82:85]
	v_mfma_f32_16x16x32_f16 v[72:75], v[174:177], v[238:241], v[72:75]
	v_mfma_f32_16x16x32_f16 v[126:129], v[152:155], v[218:221], v[126:129]
	v_mfma_f32_16x16x32_f16 v[122:125], v[178:181], v[218:221], v[122:125]
	v_mfma_f32_16x16x32_f16 v[114:117], v[152:155], v[226:229], v[114:117]
	v_mfma_f32_16x16x32_f16 v[106:109], v[178:181], v[226:229], v[106:109]
	v_mfma_f32_16x16x32_f16 v[98:101], v[152:155], v[234:237], v[98:101]
	v_mfma_f32_16x16x32_f16 v[90:93], v[178:181], v[234:237], v[90:93]
	v_mfma_f32_16x16x32_f16 v[82:85], v[152:155], v[242:245], v[82:85]
	v_mfma_f32_16x16x32_f16 v[72:75], v[178:181], v[242:245], v[72:75]
	v_mfma_f32_16x16x32_f16 v[118:121], v[182:185], v[214:217], v[118:121]
	v_mfma_f32_16x16x32_f16 v[110:113], v[206:209], v[214:217], v[110:113]
	v_mfma_f32_16x16x32_f16 v[102:105], v[182:185], v[222:225], v[102:105]
	v_mfma_f32_16x16x32_f16 v[94:97], v[206:209], v[222:225], v[94:97]
	v_mfma_f32_16x16x32_f16 v[86:89], v[182:185], v[230:233], v[86:89]
	v_mfma_f32_16x16x32_f16 v[76:79], v[206:209], v[230:233], v[76:79]
	v_mfma_f32_16x16x32_f16 v[68:71], v[182:185], v[238:241], v[68:71]
	v_mfma_f32_16x16x32_f16 v[64:67], v[206:209], v[238:241], v[64:67]
	v_mfma_f32_16x16x32_f16 v[118:121], v[186:189], v[218:221], v[118:121]
	v_mfma_f32_16x16x32_f16 v[110:113], v[210:213], v[218:221], v[110:113]
	v_mfma_f32_16x16x32_f16 v[102:105], v[186:189], v[226:229], v[102:105]
	v_mfma_f32_16x16x32_f16 v[94:97], v[210:213], v[226:229], v[94:97]
	v_mfma_f32_16x16x32_f16 v[86:89], v[186:189], v[234:237], v[86:89]
	v_mfma_f32_16x16x32_f16 v[76:79], v[210:213], v[234:237], v[76:79]
	v_mfma_f32_16x16x32_f16 v[68:71], v[186:189], v[242:245], v[68:71]
	v_mfma_f32_16x16x32_f16 v[64:67], v[210:213], v[242:245], v[64:67]
	s_setprio 0
	s_barrier
; #define PG8_STAGE(bufoff, gbase, voff) do { _Pragma("unroll") for (int _i = 0; _i < 2; ++_i) \
;         __builtin_amdgcn_global_load_lds((const unsigned*)((const char*)(gbase) + (voff)[_i]), (PG8_LAS unsigned*)(lds + (bufoff) + ldsw + _i * 8192), 16, 0, 0); } while (0)
; #define PG8_LDA(dst, b, h) do { if constexpr (FP8) { _Pragma("unroll") for (int m = 0; m < 4; ++m) dst##8[m] = pg8_ld8(lds + PG8_SA(b, h) + aoff + m * 2048); } \
;         else { _Pragma("unroll") for (int m = 0; m < 4; ++m) _Pragma("unroll") for (int k = 0; k < 2; ++k) dst[m][k] = *(const PG8_LAS bf16x8*)(lds + PG8_SA(b, h) + aoff + m * 2048 + k * 1024); } } while (0)
; #define PG8_WAIT_V(n) asm volatile("s_waitcnt vmcnt(" #n ")" ::: "memory")
; #define PG8_WAIT_L(n) asm volatile("s_waitcnt lgkmcnt(" #n ")" ::: "memory")
; #define PG8_BAR __builtin_amdgcn_s_barrier()
; #define PG8_SCHED __builtin_amdgcn_sched_barrier(0)
;     ...
;             PG8_LDA(At, 1, 1); PG8_STAGE(PG8_SB(1, 0), b3, voffB); PG8_STAGE(PG8_SB(1, 1), b3 + hstep, voffB); PG8_STAGE(PG8_SA(1, 0), a3, voffA);
;             PG8_WAIT_V(8); PG8_WAIT_L(0); PG8_BAR; PG8_MMA(1, 0, At, B0); PG8_MMA(1, 1, At, B1); PG8_BAR; PG8_SCHED;
;     ...
;         if constexpr (ALIGN_EPI) { if (wr == 0) PG8_BAR; }
	s_add_i32 s22, s43, s25
	v_lshl_add_u64 v[148:149], v[148:149], 0, s[86:87]
	s_mov_b32 m0, s22
	ds_read_b128 v[214:217], v158 offset:49152
	ds_read_b128 v[218:221], v158 offset:50176
	ds_read_b128 v[222:225], v158 offset:51200
	ds_read_b128 v[226:229], v158 offset:52224
	ds_read_b128 v[230:233], v158 offset:53248
	ds_read_b128 v[234:237], v158 offset:54272
	ds_read_b128 v[238:241], v158 offset:55296
	ds_read_b128 v[242:245], v158 offset:56320
	global_load_lds_dwordx4 v[148:149], off
	s_add_i32 m0, s22, 0x2000
	s_add_u32 s0, s0, 0x40080
	v_lshl_add_u64 v[148:149], v[160:161], 0, s[86:87]
	s_addc_u32 s1, s1, 0
	s_add_i32 s22, s44, s25
	global_load_lds_dwordx4 v[148:149], off
	v_lshl_add_u64 v[148:149], s[0:1], 0, v[134:135]
	s_mov_b32 m0, s22
	s_nop 0
	global_load_lds_dwordx4 v[148:149], off
	v_lshl_add_u64 v[148:149], s[0:1], 0, v[130:131]
	s_add_i32 m0, s22, 0x2000
	s_nop 0
	global_load_lds_dwordx4 v[148:149], off
	v_lshl_add_u64 v[148:149], v[190:191], 0, s[86:87]
	s_mov_b32 m0, s37
	s_nop 0
	global_load_lds_dwordx4 v[148:149], off
	v_lshl_add_u64 v[148:149], v[246:247], 0, s[86:87]
	s_mov_b32 m0, s38
	s_nop 0
	global_load_lds_dwordx4 v[148:149], off
	s_waitcnt vmcnt(8)
	s_waitcnt lgkmcnt(0)
	s_barrier
	s_setprio 1
	s_waitcnt lgkmcnt(0)
	v_mfma_f32_16x16x32_f16 v[60:63], v[144:147], v[214:217], v[60:63]
	v_mfma_f32_16x16x32_f16 v[56:59], v[174:177], v[214:217], v[56:59]
	v_mfma_f32_16x16x32_f16 v[52:55], v[144:147], v[222:225], v[52:55]
	v_mfma_f32_16x16x32_f16 v[44:47], v[174:177], v[222:225], v[44:47]
	v_mfma_f32_16x16x32_f16 v[36:39], v[144:147], v[230:233], v[36:39]
	v_mfma_f32_16x16x32_f16 v[28:31], v[174:177], v[230:233], v[28:31]
	v_mfma_f32_16x16x32_f16 v[20:23], v[144:147], v[238:241], v[20:23]
	v_mfma_f32_16x16x32_f16 v[12:15], v[174:177], v[238:241], v[12:15]
	v_mfma_f32_16x16x32_f16 v[60:63], v[152:155], v[218:221], v[60:63]
	v_mfma_f32_16x16x32_f16 v[56:59], v[178:181], v[218:221], v[56:59]
	v_mfma_f32_16x16x32_f16 v[52:55], v[152:155], v[226:229], v[52:55]
	v_mfma_f32_16x16x32_f16 v[44:47], v[178:181], v[226:229], v[44:47]
	v_mfma_f32_16x16x32_f16 v[36:39], v[152:155], v[234:237], v[36:39]
	v_mfma_f32_16x16x32_f16 v[28:31], v[178:181], v[234:237], v[28:31]
	v_mfma_f32_16x16x32_f16 v[20:23], v[152:155], v[242:245], v[20:23]
	v_mfma_f32_16x16x32_f16 v[12:15], v[178:181], v[242:245], v[12:15]
	v_mfma_f32_16x16x32_f16 v[48:51], v[182:185], v[214:217], v[48:51]
	v_mfma_f32_16x16x32_f16 v[40:43], v[206:209], v[214:217], v[40:43]
	v_mfma_f32_16x16x32_f16 v[32:35], v[182:185], v[222:225], v[32:35]
	v_mfma_f32_16x16x32_f16 v[24:27], v[206:209], v[222:225], v[24:27]
	v_mfma_f32_16x16x32_f16 v[16:19], v[182:185], v[230:233], v[16:19]
	v_mfma_f32_16x16x32_f16 v[8:11], v[206:209], v[230:233], v[8:11]
	v_mfma_f32_16x16x32_f16 v[4:7], v[182:185], v[238:241], v[4:7]
	v_mfma_f32_16x16x32_f16 v[0:3], v[206:209], v[238:241], v[0:3]
	v_mfma_f32_16x16x32_f16 v[48:51], v[186:189], v[218:221], v[48:51]
	v_mfma_f32_16x16x32_f16 v[40:43], v[210:213], v[218:221], v[40:43]
	v_mfma_f32_16x16x32_f16 v[32:35], v[186:189], v[226:229], v[32:35]
	v_mfma_f32_16x16x32_f16 v[24:27], v[210:213], v[226:229], v[24:27]
	v_mfma_f32_16x16x32_f16 v[16:19], v[186:189], v[234:237], v[16:19]
	v_mfma_f32_16x16x32_f16 v[8:11], v[210:213], v[234:237], v[8:11]
	v_mfma_f32_16x16x32_f16 v[4:7], v[186:189], v[242:245], v[4:7]
	v_mfma_f32_16x16x32_f16 v[0:3], v[210:213], v[242:245], v[0:3]
	s_setprio 0
	s_barrier
	s_add_i32 s42, s42, 2
	s_add_u32 s40, s40, 0x100
	s_addc_u32 s41, s41, 0
	s_add_u32 s20, s20, 0x100
	s_addc_u32 s21, s21, 0
	s_cmp_gt_u32 s42, 13
	s_cbranch_scc0 .LBB0_154
	s_and_b64 vcc, exec, s[8:9]
	s_cbranch_vccz .LBB0_157
	s_barrier

; #define PG8_STAGE(bufoff, gbase, voff) do { _Pragma("unroll") for (int _i = 0; _i < 2; ++_i) \
;         __builtin_amdgcn_global_load_lds((const unsigned*)((const char*)(gbase) + (voff)[_i]), (PG8_LAS unsigned*)(lds + (bufoff) + ldsw + _i * 8192), 16, 0, 0); } while (0)
; #define PG8_LDA(dst, b, h) do { if constexpr (FP8) { _Pragma("unroll") for (int m = 0; m < 4; ++m) dst##8[m] = pg8_ld8(lds + PG8_SA(b, h) + aoff + m * 2048); } \
;         else { _Pragma("unroll") for (int m = 0; m < 4; ++m) _Pragma("unroll") for (int k = 0; k < 2; ++k) dst[m][k] = *(const PG8_LAS bf16x8*)(lds + PG8_SA(b, h) + aoff + m * 2048 + k * 1024); } } while (0)
; #define PG8_LDB(dst, b, h) do { if constexpr (FP8) { _Pragma("unroll") for (int n = 0; n < 2; ++n) dst##8[n] = pg8_ld8(lds + PG8_SB(b, h) + boff + n * 2048); } \
;         else { _Pragma("unroll") for (int n = 0; n < 2; ++n) _Pragma("unroll") for (int k = 0; k < 2; ++k) dst[n][k] = *(const PG8_LAS bf16x8*)(lds + PG8_SB(b, h) + boff + n * 2048 + k * 1024); } } while (0)
; #define PG8_WAIT_V(n) asm volatile("s_waitcnt vmcnt(" #n ")" ::: "memory")
; #define PG8_WAIT_L(n) asm volatile("s_waitcnt lgkmcnt(" #n ")" ::: "memory")
; #define PG8_BAR __builtin_amdgcn_s_barrier()
; #define PG8_SCHED __builtin_amdgcn_sched_barrier(0)
;     ...
;             const bool last = (t == nt - 2);
;             const char* a1 = cA + (size_t)(t + 1) * kstep;
;             const char* a2 = last ? nA : cA + (size_t)(t + 2) * kstep; const char* b2 = last ? nB : cB + (size_t)(t + 2) * kstep;
;             const char* a3 = a2 + kstep; const char* b3 = b2 + kstep;
;             if (last && has_next) S.a_ready(nxt);
;             if constexpr (SP2) {
;             PG8_LDB(B0, 0, 0); PG8_LDB(B1, 0, 1); PG8_SCHED; PG8_LDA(At, 0, 0); PG8_STAGE(PG8_SA(1, 1), a1 + hstep, voffA);
;             PG8_WAIT_V(8); PG8_WAIT_L(0); PG8_BAR; PG8_MMA(0, 0, At, B0); PG8_MMA(0, 1, At, B1); PG8_BAR; PG8_SCHED;
;             PG8_LDA(At, 0, 1); PG8_STAGE(PG8_SB(0, 0), b2, voffB); PG8_STAGE(PG8_SB(0, 1), b2 + hstep, voffB); PG8_STAGE(PG8_SA(0, 0), a2, voffA);
.LBB0_467:
	s_add_u32 s0, s16, s22
	s_addc_u32 s1, s17, s23
	s_add_u32 s0, s0, 0x100
	s_addc_u32 s1, s1, 0
	s_add_u32 s50, s47, s22
	s_addc_u32 s51, s48, s23
	s_add_i32 s52, 0, 0x10000
	s_cmpk_eq_i32 s22, 0x700
	s_cselect_b32 s25, s11, s1
	s_cselect_b32 s24, s44, s0
	v_add_u32_e32 v80, s52, v205
	s_cselect_b32 s1, s45, s51
	s_cselect_b32 s0, s46, s50
	s_add_i32 s53, 0, 0x14000
	ds_read_b128 v[148:151], v80
	ds_read_b128 v[152:155], v80 offset:1024
	ds_read_b128 v[156:159], v80 offset:2048
	ds_read_b128 v[174:177], v80 offset:3072
	v_add_u32_e32 v80, s53, v205
	ds_read_b128 v[178:181], v80
	ds_read_b128 v[182:185], v80 offset:1024
	ds_read_b128 v[186:189], v80 offset:2048
	ds_read_b128 v[208:211], v80 offset:3072
	v_lshl_add_u64 v[82:83], v[146:147], 0, s[22:23]
	s_add_i32 m0, s31, 0xc000
	ds_read_b128 v[212:215], v206
	ds_read_b128 v[216:219], v206 offset:1024
	ds_read_b128 v[220:223], v206 offset:2048
	ds_read_b128 v[224:227], v206 offset:3072
	ds_read_b128 v[228:231], v206 offset:4096
	ds_read_b128 v[232:235], v206 offset:5120
	ds_read_b128 v[236:239], v206 offset:6144
	ds_read_b128 v[240:243], v206 offset:7168
	global_load_lds_dwordx4 v[82:83], off
	v_lshl_add_u64 v[82:83], v[144:145], 0, s[22:23]
	s_add_i32 m0, s31, 0xe000
	s_nop 0
	global_load_lds_dwordx4 v[82:83], off
	s_waitcnt vmcnt(8)
	s_waitcnt lgkmcnt(0)
	s_barrier
	s_setprio 1
	s_waitcnt lgkmcnt(0)
	v_mfma_f32_16x16x32_bf16 v[128:131], v[148:151], v[212:215], v[128:131]
	v_mfma_f32_16x16x32_bf16 v[124:127], v[156:159], v[212:215], v[124:127]
	v_mfma_f32_16x16x32_bf16 v[112:115], v[148:151], v[220:223], v[112:115]
	v_mfma_f32_16x16x32_bf16 v[108:111], v[156:159], v[220:223], v[108:111]
	v_mfma_f32_16x16x32_bf16 v[96:99], v[148:151], v[228:231], v[96:99]
	v_mfma_f32_16x16x32_bf16 v[92:95], v[156:159], v[228:231], v[92:95]
	v_mfma_f32_16x16x32_bf16 v[76:79], v[148:151], v[236:239], v[76:79]
	v_mfma_f32_16x16x32_bf16 v[72:75], v[156:159], v[236:239], v[72:75]
	v_mfma_f32_16x16x32_bf16 v[128:131], v[152:155], v[216:219], v[128:131]
	v_mfma_f32_16x16x32_bf16 v[124:127], v[174:177], v[216:219], v[124:127]
	v_mfma_f32_16x16x32_bf16 v[112:115], v[152:155], v[224:227], v[112:115]
	v_mfma_f32_16x16x32_bf16 v[108:111], v[174:177], v[224:227], v[108:111]
	v_mfma_f32_16x16x32_bf16 v[96:99], v[152:155], v[232:235], v[96:99]
	v_mfma_f32_16x16x32_bf16 v[92:95], v[174:177], v[232:235], v[92:95]
	v_mfma_f32_16x16x32_bf16 v[76:79], v[152:155], v[240:243], v[76:79]
	v_mfma_f32_16x16x32_bf16 v[72:75], v[174:177], v[240:243], v[72:75]
	v_mfma_f32_16x16x32_bf16 v[120:123], v[178:181], v[212:215], v[120:123]
	v_mfma_f32_16x16x32_bf16 v[116:119], v[186:189], v[212:215], v[116:119]
	v_mfma_f32_16x16x32_bf16 v[104:107], v[178:181], v[220:223], v[104:107]
	v_mfma_f32_16x16x32_bf16 v[100:103], v[186:189], v[220:223], v[100:103]
	v_mfma_f32_16x16x32_bf16 v[88:91], v[178:181], v[228:231], v[88:91]
	v_mfma_f32_16x16x32_bf16 v[82:85], v[186:189], v[228:231], v[84:87]
	v_mfma_f32_16x16x32_bf16 v[68:71], v[178:181], v[236:239], v[68:71]
	v_mfma_f32_16x16x32_bf16 v[64:67], v[186:189], v[236:239], v[64:67]
	v_mfma_f32_16x16x32_bf16 v[120:123], v[182:185], v[216:219], v[120:123]
	v_mfma_f32_16x16x32_bf16 v[116:119], v[208:211], v[216:219], v[116:119]
	v_mfma_f32_16x16x32_bf16 v[104:107], v[182:185], v[224:227], v[104:107]
	v_mfma_f32_16x16x32_bf16 v[100:103], v[208:211], v[224:227], v[100:103]
	v_mfma_f32_16x16x32_bf16 v[88:91], v[182:185], v[232:235], v[88:91]
	v_mfma_f32_16x16x32_bf16 v[82:85], v[208:211], v[232:235], v[82:85]
	v_mfma_f32_16x16x32_bf16 v[68:71], v[182:185], v[240:243], v[68:71]
	v_mfma_f32_16x16x32_bf16 v[64:67], v[208:211], v[240:243], v[64:67]
	s_setprio 0
	s_barrier
	s_add_i32 s50, s52, s30
	v_lshl_add_u64 v[160:161], s[0:1], 0, v[134:135]
	s_mov_b32 m0, s50
	ds_read_b128 v[212:215], v206 offset:16384
	ds_read_b128 v[216:219], v206 offset:17408
	ds_read_b128 v[220:223], v206 offset:18432
	ds_read_b128 v[224:227], v206 offset:19456
	ds_read_b128 v[228:231], v206 offset:20480
	ds_read_b128 v[232:235], v206 offset:21504
	ds_read_b128 v[236:239], v206 offset:22528
	ds_read_b128 v[240:243], v206 offset:23552
	global_load_lds_dwordx4 v[160:161], off
	s_add_i32 m0, s50, 0x2000
	s_add_u32 s50, s0, 0x40000
	v_lshl_add_u64 v[190:191], s[0:1], 0, v[138:139]
	s_addc_u32 s51, s1, 0
	s_add_i32 s52, s53, s30
	global_load_lds_dwordx4 v[190:191], off
	v_lshl_add_u64 v[86:87], s[50:51], 0, v[134:135]
	s_mov_b32 m0, s52
	v_lshl_add_u64 v[244:245], s[24:25], 0, v[132:133]
	global_load_lds_dwordx4 v[86:87], off
	v_lshl_add_u64 v[86:87], s[50:51], 0, v[138:139]
	s_add_i32 m0, s52, 0x2000
	v_lshl_add_u64 v[246:247], s[24:25], 0, v[136:137]
	global_load_lds_dwordx4 v[86:87], off
	s_mov_b32 m0, s31
	s_nop 0
	global_load_lds_dwordx4 v[244:245], off
	s_mov_b32 m0, s34
	s_nop 0
	global_load_lds_dwordx4 v[246:247], off
	s_waitcnt vmcnt(8)
	s_waitcnt lgkmcnt(0)
	s_barrier
; #define PG8_STAGE(bufoff, gbase, voff) do { _Pragma("unroll") for (int _i = 0; _i < 2; ++_i) \
;         __builtin_amdgcn_global_load_lds((const unsigned*)((const char*)(gbase) + (voff)[_i]), (PG8_LAS unsigned*)(lds + (bufoff) + ldsw + _i * 8192), 16, 0, 0); } while (0)
; #define PG8_LDA(dst, b, h) do { if constexpr (FP8) { _Pragma("unroll") for (int m = 0; m < 4; ++m) dst##8[m] = pg8_ld8(lds + PG8_SA(b, h) + aoff + m * 2048); } \
;         else { _Pragma("unroll") for (int m = 0; m < 4; ++m) _Pragma("unroll") for (int k = 0; k < 2; ++k) dst[m][k] = *(const PG8_LAS bf16x8*)(lds + PG8_SA(b, h) + aoff + m * 2048 + k * 1024); } } while (0)
; #define PG8_LDB(dst, b, h) do { if constexpr (FP8) { _Pragma("unroll") for (int n = 0; n < 2; ++n) dst##8[n] = pg8_ld8(lds + PG8_SB(b, h) + boff + n * 2048); } \
;         else { _Pragma("unroll") for (int n = 0; n < 2; ++n) _Pragma("unroll") for (int k = 0; k < 2; ++k) dst[n][k] = *(const PG8_LAS bf16x8*)(lds + PG8_SB(b, h) + boff + n * 2048 + k * 1024); } } while (0)
; #define PG8_WAIT_V(n) asm volatile("s_waitcnt vmcnt(" #n ")" ::: "memory")
; #define PG8_WAIT_L(n) asm volatile("s_waitcnt lgkmcnt(" #n ")" ::: "memory")
; #define PG8_BAR __builtin_amdgcn_s_barrier()
; #define PG8_SCHED __builtin_amdgcn_sched_barrier(0)
;     ...
;             PG8_WAIT_V(8); PG8_WAIT_L(0); PG8_BAR; PG8_MMA(0, 0, At, B0); PG8_MMA(0, 1, At, B1); PG8_BAR; PG8_SCHED;
;             PG8_LDA(At, 0, 1); PG8_STAGE(PG8_SB(0, 0), b2, voffB); PG8_STAGE(PG8_SB(0, 1), b2 + hstep, voffB); PG8_STAGE(PG8_SA(0, 0), a2, voffA);
;             PG8_WAIT_V(8); PG8_WAIT_L(0); PG8_BAR; PG8_MMA(1, 0, At, B0); PG8_MMA(1, 1, At, B1); PG8_BAR; PG8_SCHED;
;             PG8_LDB(B0, 1, 0); PG8_LDB(B1, 1, 1); PG8_SCHED; PG8_LDA(At, 1, 0); PG8_STAGE(PG8_SA(0, 1), a2 + hstep, voffA);
;             PG8_WAIT_V(8); PG8_WAIT_L(0); PG8_BAR; PG8_MMA(0, 0, At, B0); PG8_MMA(0, 1, At, B1); PG8_BAR; PG8_SCHED;
	s_setprio 1
	s_waitcnt lgkmcnt(0)
	v_mfma_f32_16x16x32_bf16 v[60:63], v[148:151], v[212:215], v[60:63]
	v_mfma_f32_16x16x32_bf16 v[56:59], v[156:159], v[212:215], v[56:59]
	v_mfma_f32_16x16x32_bf16 v[44:47], v[148:151], v[220:223], v[44:47]
	v_mfma_f32_16x16x32_bf16 v[40:43], v[156:159], v[220:223], v[40:43]
	v_mfma_f32_16x16x32_bf16 v[28:31], v[148:151], v[228:231], v[28:31]
	v_mfma_f32_16x16x32_bf16 v[24:27], v[156:159], v[228:231], v[24:27]
	v_mfma_f32_16x16x32_bf16 v[12:15], v[148:151], v[236:239], v[12:15]
	v_mfma_f32_16x16x32_bf16 v[8:11], v[156:159], v[236:239], v[8:11]
	v_mfma_f32_16x16x32_bf16 v[60:63], v[152:155], v[216:219], v[60:63]
	v_mfma_f32_16x16x32_bf16 v[56:59], v[174:177], v[216:219], v[56:59]
	v_mfma_f32_16x16x32_bf16 v[44:47], v[152:155], v[224:227], v[44:47]
	v_mfma_f32_16x16x32_bf16 v[40:43], v[174:177], v[224:227], v[40:43]
	v_mfma_f32_16x16x32_bf16 v[28:31], v[152:155], v[232:235], v[28:31]
	v_mfma_f32_16x16x32_bf16 v[24:27], v[174:177], v[232:235], v[24:27]
	v_mfma_f32_16x16x32_bf16 v[12:15], v[152:155], v[240:243], v[12:15]
	v_mfma_f32_16x16x32_bf16 v[8:11], v[174:177], v[240:243], v[8:11]
	v_mfma_f32_16x16x32_bf16 v[52:55], v[178:181], v[212:215], v[52:55]
	v_mfma_f32_16x16x32_bf16 v[48:51], v[186:189], v[212:215], v[48:51]
	v_mfma_f32_16x16x32_bf16 v[36:39], v[178:181], v[220:223], v[36:39]
	v_mfma_f32_16x16x32_bf16 v[32:35], v[186:189], v[220:223], v[32:35]
	v_mfma_f32_16x16x32_bf16 v[20:23], v[178:181], v[228:231], v[20:23]
	v_mfma_f32_16x16x32_bf16 v[16:19], v[186:189], v[228:231], v[16:19]
	v_mfma_f32_16x16x32_bf16 v[4:7], v[178:181], v[236:239], v[4:7]
	v_mfma_f32_16x16x32_bf16 v[0:3], v[186:189], v[236:239], v[0:3]
	v_mfma_f32_16x16x32_bf16 v[52:55], v[182:185], v[216:219], v[52:55]
	v_mfma_f32_16x16x32_bf16 v[48:51], v[208:211], v[216:219], v[48:51]
	v_mfma_f32_16x16x32_bf16 v[36:39], v[182:185], v[224:227], v[36:39]
	v_mfma_f32_16x16x32_bf16 v[32:35], v[208:211], v[224:227], v[32:35]
	v_mfma_f32_16x16x32_bf16 v[20:23], v[182:185], v[232:235], v[20:23]
	v_mfma_f32_16x16x32_bf16 v[16:19], v[208:211], v[232:235], v[16:19]
	v_mfma_f32_16x16x32_bf16 v[4:7], v[182:185], v[240:243], v[4:7]
	v_mfma_f32_16x16x32_bf16 v[0:3], v[208:211], v[240:243], v[0:3]
	s_setprio 0
	s_barrier
	s_add_i32 s50, 0, 0x18000
	v_add_u32_e32 v80, s50, v205
	s_add_i32 s51, 0, 0x1c000
	ds_read_b128 v[148:151], v80
	ds_read_b128 v[152:155], v80 offset:1024
	ds_read_b128 v[156:159], v80 offset:2048
	ds_read_b128 v[174:177], v80 offset:3072
	v_add_u32_e32 v80, s51, v205
	ds_read_b128 v[178:181], v80
	ds_read_b128 v[182:185], v80 offset:1024
	ds_read_b128 v[186:189], v80 offset:2048
	ds_read_b128 v[208:211], v80 offset:3072
	s_add_u32 s24, s24, 0x40000
	s_addc_u32 s25, s25, 0
	s_mov_b32 m0, s35
	v_lshl_add_u64 v[86:87], s[24:25], 0, v[132:133]
	ds_read_b128 v[212:215], v206 offset:32768
	ds_read_b128 v[216:219], v206 offset:33792
	ds_read_b128 v[220:223], v206 offset:34816
	ds_read_b128 v[224:227], v206 offset:35840
	ds_read_b128 v[228:231], v206 offset:36864
	ds_read_b128 v[232:235], v206 offset:37888
	ds_read_b128 v[236:239], v206 offset:38912
	ds_read_b128 v[240:243], v206 offset:39936
	global_load_lds_dwordx4 v[86:87], off
	v_lshl_add_u64 v[86:87], s[24:25], 0, v[136:137]
	s_mov_b32 m0, s36
	s_nop 0
	global_load_lds_dwordx4 v[86:87], off
	s_waitcnt vmcnt(8)
	s_waitcnt lgkmcnt(0)
	s_barrier
	s_setprio 1
	s_waitcnt lgkmcnt(0)
	v_mfma_f32_16x16x32_bf16 v[128:131], v[148:151], v[212:215], v[128:131]
	v_mfma_f32_16x16x32_bf16 v[124:127], v[156:159], v[212:215], v[124:127]
	v_mfma_f32_16x16x32_bf16 v[112:115], v[148:151], v[220:223], v[112:115]
	v_mfma_f32_16x16x32_bf16 v[108:111], v[156:159], v[220:223], v[108:111]
	v_mfma_f32_16x16x32_bf16 v[96:99], v[148:151], v[228:231], v[96:99]
	v_mfma_f32_16x16x32_bf16 v[92:95], v[156:159], v[228:231], v[92:95]
	v_mfma_f32_16x16x32_bf16 v[76:79], v[148:151], v[236:239], v[76:79]
	v_mfma_f32_16x16x32_bf16 v[72:75], v[156:159], v[236:239], v[72:75]
	v_mfma_f32_16x16x32_bf16 v[128:131], v[152:155], v[216:219], v[128:131]
	v_mfma_f32_16x16x32_bf16 v[124:127], v[174:177], v[216:219], v[124:127]
	v_mfma_f32_16x16x32_bf16 v[112:115], v[152:155], v[224:227], v[112:115]
	v_mfma_f32_16x16x32_bf16 v[108:111], v[174:177], v[224:227], v[108:111]
	v_mfma_f32_16x16x32_bf16 v[96:99], v[152:155], v[232:235], v[96:99]
	v_mfma_f32_16x16x32_bf16 v[92:95], v[174:177], v[232:235], v[92:95]
	v_mfma_f32_16x16x32_bf16 v[76:79], v[152:155], v[240:243], v[76:79]
	v_mfma_f32_16x16x32_bf16 v[72:75], v[174:177], v[240:243], v[72:75]
	v_mfma_f32_16x16x32_bf16 v[120:123], v[178:181], v[212:215], v[120:123]
	v_mfma_f32_16x16x32_bf16 v[116:119], v[186:189], v[212:215], v[116:119]
	v_mfma_f32_16x16x32_bf16 v[104:107], v[178:181], v[220:223], v[104:107]
	v_mfma_f32_16x16x32_bf16 v[100:103], v[186:189], v[220:223], v[100:103]
	v_mfma_f32_16x16x32_bf16 v[86:89], v[178:181], v[228:231], v[88:91]
	v_mfma_f32_16x16x32_bf16 v[82:85], v[186:189], v[228:231], v[82:85]
	v_mfma_f32_16x16x32_bf16 v[68:71], v[178:181], v[236:239], v[68:71]
	v_mfma_f32_16x16x32_bf16 v[64:67], v[186:189], v[236:239], v[64:67]
	v_mfma_f32_16x16x32_bf16 v[120:123], v[182:185], v[216:219], v[120:123]
	v_mfma_f32_16x16x32_bf16 v[116:119], v[208:211], v[216:219], v[116:119]
	v_mfma_f32_16x16x32_bf16 v[104:107], v[182:185], v[224:227], v[104:107]
	v_mfma_f32_16x16x32_bf16 v[100:103], v[208:211], v[224:227], v[100:103]
	v_mfma_f32_16x16x32_bf16 v[88:91], v[182:185], v[232:235], v[86:89]
	v_mfma_f32_16x16x32_bf16 v[84:87], v[208:211], v[232:235], v[82:85]
	v_mfma_f32_16x16x32_bf16 v[68:71], v[182:185], v[240:243], v[68:71]
	v_mfma_f32_16x16x32_bf16 v[64:67], v[208:211], v[240:243], v[64:67]
	s_setprio 0
	s_barrier
; #define PG8_STAGE(bufoff, gbase, voff) do { _Pragma("unroll") for (int _i = 0; _i < 2; ++_i) \
;         __builtin_amdgcn_global_load_lds((const unsigned*)((const char*)(gbase) + (voff)[_i]), (PG8_LAS unsigned*)(lds + (bufoff) + ldsw + _i * 8192), 16, 0, 0); } while (0)
; #define PG8_LDA(dst, b, h) do { if constexpr (FP8) { _Pragma("unroll") for (int m = 0; m < 4; ++m) dst##8[m] = pg8_ld8(lds + PG8_SA(b, h) + aoff + m * 2048); } \
;         else { _Pragma("unroll") for (int m = 0; m < 4; ++m) _Pragma("unroll") for (int k = 0; k < 2; ++k) dst[m][k] = *(const PG8_LAS bf16x8*)(lds + PG8_SA(b, h) + aoff + m * 2048 + k * 1024); } } while (0)
; #define PG8_WAIT_V(n) asm volatile("s_waitcnt vmcnt(" #n ")" ::: "memory")
; #define PG8_WAIT_L(n) asm volatile("s_waitcnt lgkmcnt(" #n ")" ::: "memory")
; #define PG8_BAR __builtin_amdgcn_s_barrier()
; #define PG8_SCHED __builtin_amdgcn_sched_barrier(0)
;     ...
;         for (int t = 0; t < nt; t += 2) {
;     ...
;             PG8_LDA(At, 1, 1); PG8_STAGE(PG8_SB(1, 0), b3, voffB); PG8_STAGE(PG8_SB(1, 1), b3 + hstep, voffB); PG8_STAGE(PG8_SA(1, 0), a3, voffA);
;             PG8_WAIT_V(8); PG8_WAIT_L(0); PG8_BAR; PG8_MMA(1, 0, At, B0); PG8_MMA(1, 1, At, B1); PG8_BAR; PG8_SCHED;
	s_add_i32 s24, s50, s30
	v_lshl_add_u64 v[82:83], v[160:161], 0, s[86:87]
	s_mov_b32 m0, s24
	ds_read_b128 v[212:215], v206 offset:49152
	ds_read_b128 v[216:219], v206 offset:50176
	ds_read_b128 v[220:223], v206 offset:51200
	ds_read_b128 v[224:227], v206 offset:52224
	ds_read_b128 v[228:231], v206 offset:53248
	ds_read_b128 v[232:235], v206 offset:54272
	ds_read_b128 v[236:239], v206 offset:55296
	ds_read_b128 v[240:243], v206 offset:56320
	global_load_lds_dwordx4 v[82:83], off
	s_add_i32 m0, s24, 0x2000
	s_add_u32 s0, s0, 0x40080
	v_lshl_add_u64 v[82:83], v[190:191], 0, s[86:87]
	s_addc_u32 s1, s1, 0
	s_add_i32 s24, s51, s30
	global_load_lds_dwordx4 v[82:83], off
	v_lshl_add_u64 v[82:83], s[0:1], 0, v[134:135]
	s_mov_b32 m0, s24
	s_nop 0
	global_load_lds_dwordx4 v[82:83], off
	v_lshl_add_u64 v[82:83], s[0:1], 0, v[138:139]
	s_add_i32 m0, s24, 0x2000
	s_nop 0
	global_load_lds_dwordx4 v[82:83], off
	v_lshl_add_u64 v[82:83], v[244:245], 0, s[86:87]
	s_mov_b32 m0, s41
	s_nop 0
	global_load_lds_dwordx4 v[82:83], off
	v_lshl_add_u64 v[82:83], v[246:247], 0, s[86:87]
	s_mov_b32 m0, s42
	s_nop 0
	global_load_lds_dwordx4 v[82:83], off
	s_waitcnt vmcnt(8)
	s_waitcnt lgkmcnt(0)
	s_barrier
	s_setprio 1
	s_waitcnt lgkmcnt(0)
	v_mfma_f32_16x16x32_bf16 v[60:63], v[148:151], v[212:215], v[60:63]
	v_mfma_f32_16x16x32_bf16 v[56:59], v[156:159], v[212:215], v[56:59]
	v_mfma_f32_16x16x32_bf16 v[44:47], v[148:151], v[220:223], v[44:47]
	v_mfma_f32_16x16x32_bf16 v[40:43], v[156:159], v[220:223], v[40:43]
	v_mfma_f32_16x16x32_bf16 v[28:31], v[148:151], v[228:231], v[28:31]
	v_mfma_f32_16x16x32_bf16 v[24:27], v[156:159], v[228:231], v[24:27]
	v_mfma_f32_16x16x32_bf16 v[12:15], v[148:151], v[236:239], v[12:15]
	v_mfma_f32_16x16x32_bf16 v[8:11], v[156:159], v[236:239], v[8:11]
	v_mfma_f32_16x16x32_bf16 v[60:63], v[152:155], v[216:219], v[60:63]
	v_mfma_f32_16x16x32_bf16 v[56:59], v[174:177], v[216:219], v[56:59]
	v_mfma_f32_16x16x32_bf16 v[44:47], v[152:155], v[224:227], v[44:47]
	v_mfma_f32_16x16x32_bf16 v[40:43], v[174:177], v[224:227], v[40:43]
	v_mfma_f32_16x16x32_bf16 v[28:31], v[152:155], v[232:235], v[28:31]
	v_mfma_f32_16x16x32_bf16 v[24:27], v[174:177], v[232:235], v[24:27]
	v_mfma_f32_16x16x32_bf16 v[12:15], v[152:155], v[240:243], v[12:15]
	v_mfma_f32_16x16x32_bf16 v[8:11], v[174:177], v[240:243], v[8:11]
	v_mfma_f32_16x16x32_bf16 v[52:55], v[178:181], v[212:215], v[52:55]
	v_mfma_f32_16x16x32_bf16 v[48:51], v[186:189], v[212:215], v[48:51]
	v_mfma_f32_16x16x32_bf16 v[36:39], v[178:181], v[220:223], v[36:39]
	v_mfma_f32_16x16x32_bf16 v[32:35], v[186:189], v[220:223], v[32:35]
	v_mfma_f32_16x16x32_bf16 v[20:23], v[178:181], v[228:231], v[20:23]
	v_mfma_f32_16x16x32_bf16 v[16:19], v[186:189], v[228:231], v[16:19]
	v_mfma_f32_16x16x32_bf16 v[4:7], v[178:181], v[236:239], v[4:7]
	v_mfma_f32_16x16x32_bf16 v[0:3], v[186:189], v[236:239], v[0:3]
	v_mfma_f32_16x16x32_bf16 v[52:55], v[182:185], v[216:219], v[52:55]
	v_mfma_f32_16x16x32_bf16 v[48:51], v[208:211], v[216:219], v[48:51]
	v_mfma_f32_16x16x32_bf16 v[36:39], v[182:185], v[224:227], v[36:39]
	v_mfma_f32_16x16x32_bf16 v[32:35], v[208:211], v[224:227], v[32:35]
	v_mfma_f32_16x16x32_bf16 v[20:23], v[182:185], v[232:235], v[20:23]
	v_mfma_f32_16x16x32_bf16 v[16:19], v[208:211], v[232:235], v[16:19]
	v_mfma_f32_16x16x32_bf16 v[4:7], v[182:185], v[240:243], v[4:7]
	v_mfma_f32_16x16x32_bf16 v[0:3], v[208:211], v[240:243], v[0:3]
	s_setprio 0
	s_barrier
	s_add_i32 s49, s49, 2
	s_add_u32 s22, s22, 0x100
	s_addc_u32 s23, s23, 0
	s_cmp_gt_u32 s49, 13
	s_cbranch_scc1 .LBB0_470

; #define PG8_STAGE(bufoff, gbase, voff) do { _Pragma("unroll") for (int _i = 0; _i < 2; ++_i) \
;         __builtin_amdgcn_global_load_lds((const unsigned*)((const char*)(gbase) + (voff)[_i]), (PG8_LAS unsigned*)(lds + (bufoff) + ldsw + _i * 8192), 16, 0, 0); } while (0)
; #define PG8_LDA(dst, b, h) do { if constexpr (FP8) { _Pragma("unroll") for (int m = 0; m < 4; ++m) dst##8[m] = pg8_ld8(lds + PG8_SA(b, h) + aoff + m * 2048); } \
;         else { _Pragma("unroll") for (int m = 0; m < 4; ++m) _Pragma("unroll") for (int k = 0; k < 2; ++k) dst[m][k] = *(const PG8_LAS bf16x8*)(lds + PG8_SA(b, h) + aoff + m * 2048 + k * 1024); } } while (0)
; #define PG8_LDB(dst, b, h) do { if constexpr (FP8) { _Pragma("unroll") for (int n = 0; n < 2; ++n) dst##8[n] = pg8_ld8(lds + PG8_SB(b, h) + boff + n * 2048); } \
;         else { _Pragma("unroll") for (int n = 0; n < 2; ++n) _Pragma("unroll") for (int k = 0; k < 2; ++k) dst[n][k] = *(const PG8_LAS bf16x8*)(lds + PG8_SB(b, h) + boff + n * 2048 + k * 1024); } } while (0)
; #define PG8_WAIT_V(n) asm volatile("s_waitcnt vmcnt(" #n ")" ::: "memory")
; #define PG8_WAIT_L(n) asm volatile("s_waitcnt lgkmcnt(" #n ")" ::: "memory")
; #define PG8_BAR __builtin_amdgcn_s_barrier()
; #define PG8_SCHED __builtin_amdgcn_sched_barrier(0)
;     ...
;             const bool last = (t == nt - 2);
;             const char* a1 = cA + (size_t)(t + 1) * kstep;
;             const char* a2 = last ? nA : cA + (size_t)(t + 2) * kstep; const char* b2 = last ? nB : cB + (size_t)(t + 2) * kstep;
;             const char* a3 = a2 + kstep; const char* b3 = b2 + kstep;
;             if (last && has_next) S.a_ready(nxt);
;             if constexpr (SP2) {
;             PG8_LDB(B0, 0, 0); PG8_LDB(B1, 0, 1); PG8_SCHED; PG8_LDA(At, 0, 0); PG8_STAGE(PG8_SA(1, 1), a1 + hstep, voffA);
;             PG8_WAIT_V(8); PG8_WAIT_L(0); PG8_BAR; PG8_MMA(0, 0, At, B0); PG8_MMA(0, 1, At, B1); PG8_BAR; PG8_SCHED;
;             PG8_LDA(At, 0, 1); PG8_STAGE(PG8_SB(0, 0), b2, voffB); PG8_STAGE(PG8_SB(0, 1), b2 + hstep, voffB); PG8_STAGE(PG8_SA(0, 0), a2, voffA);
.LBB0_552:
	s_add_u32 s0, s22, 0xfffc0080
	s_addc_u32 s1, s23, -1
	s_add_i32 s46, 0, 0x10000
	s_cmp_eq_u32 s45, 12
	s_cselect_b32 s25, s13, s1
	s_cselect_b32 s24, s41, s0
	s_cselect_b32 s1, s11, s44
	s_cselect_b32 s0, s42, s43
	s_add_i32 s48, 0, 0x14000
	v_add_u32_e32 v152, s46, v156
	v_add_u32_e32 v170, s48, v156
	ds_read_b128 v[130:133], v152
	ds_read_b128 v[134:137], v152 offset:1024
	ds_read_b128 v[148:151], v152 offset:2048
	ds_read_b128 v[152:155], v152 offset:3072
	ds_read_b128 v[158:161], v170
	ds_read_b128 v[174:177], v170 offset:1024
	ds_read_b128 v[178:181], v170 offset:2048
	ds_read_b128 v[182:185], v170 offset:3072
	v_lshl_add_u64 v[190:191], s[22:23], 0, v[146:147]
	s_add_i32 m0, s19, 0xc000
	ds_read_b128 v[186:189], v157
	ds_read_b128 v[206:209], v157 offset:1024
	ds_read_b128 v[210:213], v157 offset:2048
	ds_read_b128 v[214:217], v157 offset:3072
	ds_read_b128 v[218:221], v157 offset:4096
	ds_read_b128 v[222:225], v157 offset:5120
	ds_read_b128 v[226:229], v157 offset:6144
	ds_read_b128 v[230:233], v157 offset:7168
	global_load_lds_dwordx4 v[190:191], off
	v_lshl_add_u64 v[190:191], s[22:23], 0, v[144:145]
	s_add_i32 m0, s19, 0xe000
	s_nop 0
	global_load_lds_dwordx4 v[190:191], off
	s_waitcnt vmcnt(8)
	s_waitcnt lgkmcnt(0)
	s_barrier
	s_setprio 1
	s_waitcnt lgkmcnt(0)
	v_mfma_f32_16x16x32_bf16 v[126:129], v[130:133], v[186:189], v[126:129]
	v_mfma_f32_16x16x32_bf16 v[122:125], v[148:151], v[186:189], v[122:125]
	v_mfma_f32_16x16x32_bf16 v[110:113], v[130:133], v[210:213], v[110:113]
	v_mfma_f32_16x16x32_bf16 v[106:109], v[148:151], v[210:213], v[106:109]
	v_mfma_f32_16x16x32_bf16 v[94:97], v[130:133], v[218:221], v[94:97]
	v_mfma_f32_16x16x32_bf16 v[90:93], v[148:151], v[218:221], v[90:93]
	v_mfma_f32_16x16x32_bf16 v[76:79], v[130:133], v[226:229], v[76:79]
	v_mfma_f32_16x16x32_bf16 v[72:75], v[148:151], v[226:229], v[72:75]
	v_mfma_f32_16x16x32_bf16 v[126:129], v[134:137], v[206:209], v[126:129]
	v_mfma_f32_16x16x32_bf16 v[122:125], v[152:155], v[206:209], v[122:125]
	v_mfma_f32_16x16x32_bf16 v[110:113], v[134:137], v[214:217], v[110:113]
	v_mfma_f32_16x16x32_bf16 v[106:109], v[152:155], v[214:217], v[106:109]
	v_mfma_f32_16x16x32_bf16 v[94:97], v[134:137], v[222:225], v[94:97]
	v_mfma_f32_16x16x32_bf16 v[90:93], v[152:155], v[222:225], v[90:93]
	v_mfma_f32_16x16x32_bf16 v[76:79], v[134:137], v[230:233], v[76:79]
	v_mfma_f32_16x16x32_bf16 v[72:75], v[152:155], v[230:233], v[72:75]
	v_mfma_f32_16x16x32_bf16 v[118:121], v[158:161], v[186:189], v[118:121]
	v_mfma_f32_16x16x32_bf16 v[114:117], v[178:181], v[186:189], v[114:117]
	v_mfma_f32_16x16x32_bf16 v[102:105], v[158:161], v[210:213], v[102:105]
	v_mfma_f32_16x16x32_bf16 v[98:101], v[178:181], v[210:213], v[98:101]
	v_mfma_f32_16x16x32_bf16 v[86:89], v[158:161], v[218:221], v[86:89]
	v_mfma_f32_16x16x32_bf16 v[82:85], v[178:181], v[218:221], v[82:85]
	v_mfma_f32_16x16x32_bf16 v[68:71], v[158:161], v[226:229], v[68:71]
	v_mfma_f32_16x16x32_bf16 v[64:67], v[178:181], v[226:229], v[64:67]
	v_mfma_f32_16x16x32_bf16 v[118:121], v[174:177], v[206:209], v[118:121]
	v_mfma_f32_16x16x32_bf16 v[114:117], v[182:185], v[206:209], v[114:117]
	v_mfma_f32_16x16x32_bf16 v[102:105], v[174:177], v[214:217], v[102:105]
	v_mfma_f32_16x16x32_bf16 v[98:101], v[182:185], v[214:217], v[98:101]
	v_mfma_f32_16x16x32_bf16 v[86:89], v[174:177], v[222:225], v[86:89]
	v_mfma_f32_16x16x32_bf16 v[82:85], v[182:185], v[222:225], v[82:85]
	v_mfma_f32_16x16x32_bf16 v[68:71], v[174:177], v[230:233], v[68:71]
	v_mfma_f32_16x16x32_bf16 v[64:67], v[182:185], v[230:233], v[64:67]
	s_setprio 0
	s_barrier
	s_add_i32 s46, s46, s29
	v_lshl_add_u64 v[190:191], s[0:1], 0, v[80:81]
	s_mov_b32 m0, s46
	ds_read_b128 v[186:189], v157 offset:16384
	ds_read_b128 v[206:209], v157 offset:17408
	ds_read_b128 v[210:213], v157 offset:18432
	ds_read_b128 v[214:217], v157 offset:19456
	ds_read_b128 v[218:221], v157 offset:20480
	ds_read_b128 v[222:225], v157 offset:21504
	ds_read_b128 v[226:229], v157 offset:22528
	ds_read_b128 v[230:233], v157 offset:23552
	global_load_lds_dwordx4 v[190:191], off
	s_add_i32 m0, s46, 0x2000
	s_add_u32 s46, s0, 0x40000
	v_lshl_add_u64 v[234:235], s[0:1], 0, v[142:143]
	s_addc_u32 s47, s1, 0
	s_add_i32 s48, s48, s29
	global_load_lds_dwordx4 v[234:235], off
	v_lshl_add_u64 v[236:237], s[46:47], 0, v[80:81]
	s_mov_b32 m0, s48
	v_lshl_add_u64 v[238:239], s[24:25], 0, v[140:141]
	global_load_lds_dwordx4 v[236:237], off
	v_lshl_add_u64 v[236:237], s[46:47], 0, v[142:143]
	s_add_i32 m0, s48, 0x2000
	s_nop 0
	global_load_lds_dwordx4 v[236:237], off
	v_lshl_add_u64 v[236:237], s[24:25], 0, v[138:139]
	s_mov_b32 m0, s19
	s_nop 0
	global_load_lds_dwordx4 v[236:237], off
	s_mov_b32 m0, s21
	s_nop 0
	global_load_lds_dwordx4 v[238:239], off
	s_waitcnt vmcnt(8)
	s_waitcnt lgkmcnt(0)
	s_barrier
; #define PG8_STAGE(bufoff, gbase, voff) do { _Pragma("unroll") for (int _i = 0; _i < 2; ++_i) \
;         __builtin_amdgcn_global_load_lds((const unsigned*)((const char*)(gbase) + (voff)[_i]), (PG8_LAS unsigned*)(lds + (bufoff) + ldsw + _i * 8192), 16, 0, 0); } while (0)
; #define PG8_LDA(dst, b, h) do { if constexpr (FP8) { _Pragma("unroll") for (int m = 0; m < 4; ++m) dst##8[m] = pg8_ld8(lds + PG8_SA(b, h) + aoff + m * 2048); } \
;         else { _Pragma("unroll") for (int m = 0; m < 4; ++m) _Pragma("unroll") for (int k = 0; k < 2; ++k) dst[m][k] = *(const PG8_LAS bf16x8*)(lds + PG8_SA(b, h) + aoff + m * 2048 + k * 1024); } } while (0)
; #define PG8_LDB(dst, b, h) do { if constexpr (FP8) { _Pragma("unroll") for (int n = 0; n < 2; ++n) dst##8[n] = pg8_ld8(lds + PG8_SB(b, h) + boff + n * 2048); } \
;         else { _Pragma("unroll") for (int n = 0; n < 2; ++n) _Pragma("unroll") for (int k = 0; k < 2; ++k) dst[n][k] = *(const PG8_LAS bf16x8*)(lds + PG8_SB(b, h) + boff + n * 2048 + k * 1024); } } while (0)
; #define PG8_WAIT_V(n) asm volatile("s_waitcnt vmcnt(" #n ")" ::: "memory")
; #define PG8_WAIT_L(n) asm volatile("s_waitcnt lgkmcnt(" #n ")" ::: "memory")
; #define PG8_BAR __builtin_amdgcn_s_barrier()
; #define PG8_SCHED __builtin_amdgcn_sched_barrier(0)
;     ...
;             PG8_WAIT_V(8); PG8_WAIT_L(0); PG8_BAR; PG8_MMA(0, 0, At, B0); PG8_MMA(0, 1, At, B1); PG8_BAR; PG8_SCHED;
;             PG8_LDA(At, 0, 1); PG8_STAGE(PG8_SB(0, 0), b2, voffB); PG8_STAGE(PG8_SB(0, 1), b2 + hstep, voffB); PG8_STAGE(PG8_SA(0, 0), a2, voffA);
;             PG8_WAIT_V(8); PG8_WAIT_L(0); PG8_BAR; PG8_MMA(1, 0, At, B0); PG8_MMA(1, 1, At, B1); PG8_BAR; PG8_SCHED;
;             PG8_LDB(B0, 1, 0); PG8_LDB(B1, 1, 1); PG8_SCHED; PG8_LDA(At, 1, 0); PG8_STAGE(PG8_SA(0, 1), a2 + hstep, voffA);
;             PG8_WAIT_V(8); PG8_WAIT_L(0); PG8_BAR; PG8_MMA(0, 0, At, B0); PG8_MMA(0, 1, At, B1); PG8_BAR; PG8_SCHED;
	s_setprio 1
	s_waitcnt lgkmcnt(0)
	v_mfma_f32_16x16x32_bf16 v[60:63], v[130:133], v[186:189], v[60:63]
	v_mfma_f32_16x16x32_bf16 v[56:59], v[148:151], v[186:189], v[56:59]
	v_mfma_f32_16x16x32_bf16 v[44:47], v[130:133], v[210:213], v[44:47]
	v_mfma_f32_16x16x32_bf16 v[40:43], v[148:151], v[210:213], v[40:43]
	v_mfma_f32_16x16x32_bf16 v[28:31], v[130:133], v[218:221], v[28:31]
	v_mfma_f32_16x16x32_bf16 v[24:27], v[148:151], v[218:221], v[24:27]
	v_mfma_f32_16x16x32_bf16 v[12:15], v[130:133], v[226:229], v[12:15]
	v_mfma_f32_16x16x32_bf16 v[8:11], v[148:151], v[226:229], v[8:11]
	v_mfma_f32_16x16x32_bf16 v[60:63], v[134:137], v[206:209], v[60:63]
	v_mfma_f32_16x16x32_bf16 v[56:59], v[152:155], v[206:209], v[56:59]
	v_mfma_f32_16x16x32_bf16 v[44:47], v[134:137], v[214:217], v[44:47]
	v_mfma_f32_16x16x32_bf16 v[40:43], v[152:155], v[214:217], v[40:43]
	v_mfma_f32_16x16x32_bf16 v[28:31], v[134:137], v[222:225], v[28:31]
	v_mfma_f32_16x16x32_bf16 v[24:27], v[152:155], v[222:225], v[24:27]
	v_mfma_f32_16x16x32_bf16 v[12:15], v[134:137], v[230:233], v[12:15]
	v_mfma_f32_16x16x32_bf16 v[8:11], v[152:155], v[230:233], v[8:11]
	v_mfma_f32_16x16x32_bf16 v[52:55], v[158:161], v[186:189], v[52:55]
	v_mfma_f32_16x16x32_bf16 v[48:51], v[178:181], v[186:189], v[48:51]
	v_mfma_f32_16x16x32_bf16 v[36:39], v[158:161], v[210:213], v[36:39]
	v_mfma_f32_16x16x32_bf16 v[32:35], v[178:181], v[210:213], v[32:35]
	v_mfma_f32_16x16x32_bf16 v[20:23], v[158:161], v[218:221], v[20:23]
	v_mfma_f32_16x16x32_bf16 v[16:19], v[178:181], v[218:221], v[16:19]
	v_mfma_f32_16x16x32_bf16 v[4:7], v[158:161], v[226:229], v[4:7]
	v_mfma_f32_16x16x32_bf16 v[0:3], v[178:181], v[226:229], v[0:3]
	v_mfma_f32_16x16x32_bf16 v[52:55], v[174:177], v[206:209], v[52:55]
	v_mfma_f32_16x16x32_bf16 v[48:51], v[182:185], v[206:209], v[48:51]
	v_mfma_f32_16x16x32_bf16 v[36:39], v[174:177], v[214:217], v[36:39]
	v_mfma_f32_16x16x32_bf16 v[32:35], v[182:185], v[214:217], v[32:35]
	v_mfma_f32_16x16x32_bf16 v[20:23], v[174:177], v[222:225], v[20:23]
	v_mfma_f32_16x16x32_bf16 v[16:19], v[182:185], v[222:225], v[16:19]
	v_mfma_f32_16x16x32_bf16 v[4:7], v[174:177], v[230:233], v[4:7]
	v_mfma_f32_16x16x32_bf16 v[0:3], v[182:185], v[230:233], v[0:3]
	s_setprio 0
	s_barrier
	s_add_i32 s46, 0, 0x18000
	s_add_i32 s47, 0, 0x1c000
	v_add_u32_e32 v152, s46, v156
	v_add_u32_e32 v170, s47, v156
	ds_read_b128 v[130:133], v152
	ds_read_b128 v[134:137], v152 offset:1024
	ds_read_b128 v[148:151], v152 offset:2048
	ds_read_b128 v[152:155], v152 offset:3072
	ds_read_b128 v[158:161], v170
	ds_read_b128 v[174:177], v170 offset:1024
	ds_read_b128 v[178:181], v170 offset:2048
	ds_read_b128 v[182:185], v170 offset:3072
	s_add_u32 s24, s24, 0x40000
	s_addc_u32 s25, s25, 0
	s_mov_b32 m0, s30
	v_lshl_add_u64 v[240:241], s[24:25], 0, v[138:139]
	ds_read_b128 v[186:189], v157 offset:32768
	ds_read_b128 v[206:209], v157 offset:33792
	ds_read_b128 v[210:213], v157 offset:34816
	ds_read_b128 v[214:217], v157 offset:35840
	ds_read_b128 v[218:221], v157 offset:36864
	ds_read_b128 v[222:225], v157 offset:37888
	ds_read_b128 v[226:229], v157 offset:38912
	ds_read_b128 v[230:233], v157 offset:39936
	global_load_lds_dwordx4 v[240:241], off
	v_lshl_add_u64 v[240:241], s[24:25], 0, v[140:141]
	s_mov_b32 m0, s31
	s_nop 0
	global_load_lds_dwordx4 v[240:241], off
	s_waitcnt vmcnt(8)
	s_waitcnt lgkmcnt(0)
	s_barrier
	s_setprio 1
	s_waitcnt lgkmcnt(0)
	v_mfma_f32_16x16x32_bf16 v[126:129], v[130:133], v[186:189], v[126:129]
	v_mfma_f32_16x16x32_bf16 v[122:125], v[148:151], v[186:189], v[122:125]
	v_mfma_f32_16x16x32_bf16 v[110:113], v[130:133], v[210:213], v[110:113]
	v_mfma_f32_16x16x32_bf16 v[106:109], v[148:151], v[210:213], v[106:109]
	v_mfma_f32_16x16x32_bf16 v[94:97], v[130:133], v[218:221], v[94:97]
	v_mfma_f32_16x16x32_bf16 v[90:93], v[148:151], v[218:221], v[90:93]
	v_mfma_f32_16x16x32_bf16 v[76:79], v[130:133], v[226:229], v[76:79]
	v_mfma_f32_16x16x32_bf16 v[72:75], v[148:151], v[226:229], v[72:75]
	v_mfma_f32_16x16x32_bf16 v[126:129], v[134:137], v[206:209], v[126:129]
	v_mfma_f32_16x16x32_bf16 v[122:125], v[152:155], v[206:209], v[122:125]
	v_mfma_f32_16x16x32_bf16 v[110:113], v[134:137], v[214:217], v[110:113]
	v_mfma_f32_16x16x32_bf16 v[106:109], v[152:155], v[214:217], v[106:109]
	v_mfma_f32_16x16x32_bf16 v[94:97], v[134:137], v[222:225], v[94:97]
	v_mfma_f32_16x16x32_bf16 v[90:93], v[152:155], v[222:225], v[90:93]
	v_mfma_f32_16x16x32_bf16 v[76:79], v[134:137], v[230:233], v[76:79]
	v_mfma_f32_16x16x32_bf16 v[72:75], v[152:155], v[230:233], v[72:75]
	v_mfma_f32_16x16x32_bf16 v[118:121], v[158:161], v[186:189], v[118:121]
	v_mfma_f32_16x16x32_bf16 v[114:117], v[178:181], v[186:189], v[114:117]
	v_mfma_f32_16x16x32_bf16 v[102:105], v[158:161], v[210:213], v[102:105]
	v_mfma_f32_16x16x32_bf16 v[98:101], v[178:181], v[210:213], v[98:101]
	v_mfma_f32_16x16x32_bf16 v[86:89], v[158:161], v[218:221], v[86:89]
	v_mfma_f32_16x16x32_bf16 v[82:85], v[178:181], v[218:221], v[82:85]
	v_mfma_f32_16x16x32_bf16 v[68:71], v[158:161], v[226:229], v[68:71]
	v_mfma_f32_16x16x32_bf16 v[64:67], v[178:181], v[226:229], v[64:67]
	v_mfma_f32_16x16x32_bf16 v[118:121], v[174:177], v[206:209], v[118:121]
	v_mfma_f32_16x16x32_bf16 v[114:117], v[182:185], v[206:209], v[114:117]
	v_mfma_f32_16x16x32_bf16 v[102:105], v[174:177], v[214:217], v[102:105]
	v_mfma_f32_16x16x32_bf16 v[98:101], v[182:185], v[214:217], v[98:101]
	v_mfma_f32_16x16x32_bf16 v[86:89], v[174:177], v[222:225], v[86:89]
	v_mfma_f32_16x16x32_bf16 v[82:85], v[182:185], v[222:225], v[82:85]
	v_mfma_f32_16x16x32_bf16 v[68:71], v[174:177], v[230:233], v[68:71]
	v_mfma_f32_16x16x32_bf16 v[64:67], v[182:185], v[230:233], v[64:67]
	s_setprio 0
	s_barrier
; #define PG8_STAGE(bufoff, gbase, voff) do { _Pragma("unroll") for (int _i = 0; _i < 2; ++_i) \
;         __builtin_amdgcn_global_load_lds((const unsigned*)((const char*)(gbase) + (voff)[_i]), (PG8_LAS unsigned*)(lds + (bufoff) + ldsw + _i * 8192), 16, 0, 0); } while (0)
; #define PG8_LDA(dst, b, h) do { if constexpr (FP8) { _Pragma("unroll") for (int m = 0; m < 4; ++m) dst##8[m] = pg8_ld8(lds + PG8_SA(b, h) + aoff + m * 2048); } \
;         else { _Pragma("unroll") for (int m = 0; m < 4; ++m) _Pragma("unroll") for (int k = 0; k < 2; ++k) dst[m][k] = *(const PG8_LAS bf16x8*)(lds + PG8_SA(b, h) + aoff + m * 2048 + k * 1024); } } while (0)
; #define PG8_WAIT_V(n) asm volatile("s_waitcnt vmcnt(" #n ")" ::: "memory")
; #define PG8_WAIT_L(n) asm volatile("s_waitcnt lgkmcnt(" #n ")" ::: "memory")
; #define PG8_BAR __builtin_amdgcn_s_barrier()
; #define PG8_SCHED __builtin_amdgcn_sched_barrier(0)
;     ...
;             PG8_LDA(At, 1, 1); PG8_STAGE(PG8_SB(1, 0), b3, voffB); PG8_STAGE(PG8_SB(1, 1), b3 + hstep, voffB); PG8_STAGE(PG8_SA(1, 0), a3, voffA);
;             PG8_WAIT_V(8); PG8_WAIT_L(0); PG8_BAR; PG8_MMA(1, 0, At, B0); PG8_MMA(1, 1, At, B1); PG8_BAR; PG8_SCHED;
;     ...
;         if constexpr (ALIGN_EPI) { if (wr == 0) PG8_BAR; }
	s_add_i32 s24, s46, s29
	v_lshl_add_u64 v[190:191], v[190:191], 0, s[86:87]
	s_mov_b32 m0, s24
	ds_read_b128 v[186:189], v157 offset:49152
	ds_read_b128 v[206:209], v157 offset:50176
	ds_read_b128 v[210:213], v157 offset:51200
	ds_read_b128 v[214:217], v157 offset:52224
	ds_read_b128 v[218:221], v157 offset:53248
	ds_read_b128 v[222:225], v157 offset:54272
	ds_read_b128 v[226:229], v157 offset:55296
	ds_read_b128 v[230:233], v157 offset:56320
	global_load_lds_dwordx4 v[190:191], off
	s_add_i32 m0, s24, 0x2000
	s_add_u32 s0, s0, 0x40080
	v_lshl_add_u64 v[190:191], v[234:235], 0, s[86:87]
	s_addc_u32 s1, s1, 0
	s_add_i32 s24, s47, s29
	global_load_lds_dwordx4 v[190:191], off
	v_lshl_add_u64 v[190:191], s[0:1], 0, v[80:81]
	s_mov_b32 m0, s24
	s_nop 0
	global_load_lds_dwordx4 v[190:191], off
	v_lshl_add_u64 v[190:191], s[0:1], 0, v[142:143]
	s_add_i32 m0, s24, 0x2000
	s_nop 0
	global_load_lds_dwordx4 v[190:191], off
	v_lshl_add_u64 v[190:191], v[236:237], 0, s[86:87]
	s_mov_b32 m0, s37
	s_nop 0
	global_load_lds_dwordx4 v[190:191], off
	v_lshl_add_u64 v[190:191], v[238:239], 0, s[86:87]
	s_mov_b32 m0, s38
	s_nop 0
	global_load_lds_dwordx4 v[190:191], off
	s_waitcnt vmcnt(8)
	s_waitcnt lgkmcnt(0)
	s_barrier
	s_setprio 1
	s_waitcnt lgkmcnt(0)
	v_mfma_f32_16x16x32_bf16 v[60:63], v[130:133], v[186:189], v[60:63]
	v_mfma_f32_16x16x32_bf16 v[56:59], v[148:151], v[186:189], v[56:59]
	v_mfma_f32_16x16x32_bf16 v[44:47], v[130:133], v[210:213], v[44:47]
	v_mfma_f32_16x16x32_bf16 v[40:43], v[148:151], v[210:213], v[40:43]
	v_mfma_f32_16x16x32_bf16 v[28:31], v[130:133], v[218:221], v[28:31]
	v_mfma_f32_16x16x32_bf16 v[24:27], v[148:151], v[218:221], v[24:27]
	v_mfma_f32_16x16x32_bf16 v[12:15], v[130:133], v[226:229], v[12:15]
	v_mfma_f32_16x16x32_bf16 v[8:11], v[148:151], v[226:229], v[8:11]
	v_mfma_f32_16x16x32_bf16 v[60:63], v[134:137], v[206:209], v[60:63]
	v_mfma_f32_16x16x32_bf16 v[56:59], v[152:155], v[206:209], v[56:59]
	v_mfma_f32_16x16x32_bf16 v[44:47], v[134:137], v[214:217], v[44:47]
	v_mfma_f32_16x16x32_bf16 v[40:43], v[152:155], v[214:217], v[40:43]
	v_mfma_f32_16x16x32_bf16 v[28:31], v[134:137], v[222:225], v[28:31]
	v_mfma_f32_16x16x32_bf16 v[24:27], v[152:155], v[222:225], v[24:27]
	v_mfma_f32_16x16x32_bf16 v[12:15], v[134:137], v[230:233], v[12:15]
	v_mfma_f32_16x16x32_bf16 v[8:11], v[152:155], v[230:233], v[8:11]
	v_mfma_f32_16x16x32_bf16 v[52:55], v[158:161], v[186:189], v[52:55]
	v_mfma_f32_16x16x32_bf16 v[48:51], v[178:181], v[186:189], v[48:51]
	v_mfma_f32_16x16x32_bf16 v[36:39], v[158:161], v[210:213], v[36:39]
	v_mfma_f32_16x16x32_bf16 v[32:35], v[178:181], v[210:213], v[32:35]
	v_mfma_f32_16x16x32_bf16 v[20:23], v[158:161], v[218:221], v[20:23]
	v_mfma_f32_16x16x32_bf16 v[16:19], v[178:181], v[218:221], v[16:19]
	v_mfma_f32_16x16x32_bf16 v[4:7], v[158:161], v[226:229], v[4:7]
	v_mfma_f32_16x16x32_bf16 v[0:3], v[178:181], v[226:229], v[0:3]
	v_mfma_f32_16x16x32_bf16 v[52:55], v[174:177], v[206:209], v[52:55]
	v_mfma_f32_16x16x32_bf16 v[48:51], v[182:185], v[206:209], v[48:51]
	v_mfma_f32_16x16x32_bf16 v[36:39], v[174:177], v[214:217], v[36:39]
	v_mfma_f32_16x16x32_bf16 v[32:35], v[182:185], v[214:217], v[32:35]
	v_mfma_f32_16x16x32_bf16 v[20:23], v[174:177], v[222:225], v[20:23]
	v_mfma_f32_16x16x32_bf16 v[16:19], v[182:185], v[222:225], v[16:19]
	v_mfma_f32_16x16x32_bf16 v[4:7], v[174:177], v[230:233], v[4:7]
	v_mfma_f32_16x16x32_bf16 v[0:3], v[182:185], v[230:233], v[0:3]
	s_setprio 0
	s_barrier
	s_add_i32 s45, s45, 2
	s_add_u32 s43, s43, 0x100
	s_addc_u32 s44, s44, 0
	s_add_u32 s22, s22, 0x100
	s_addc_u32 s23, s23, 0
	s_cmp_gt_u32 s45, 13
	s_cbranch_scc0 .LBB0_552
	s_and_b64 vcc, exec, s[8:9]
	s_cbranch_vccz .LBB0_555
	s_barrier

; #define PG8_STAGE(bufoff, gbase, voff) do { _Pragma("unroll") for (int _i = 0; _i < 2; ++_i) \
;         __builtin_amdgcn_global_load_lds((const unsigned*)((const char*)(gbase) + (voff)[_i]), (PG8_LAS unsigned*)(lds + (bufoff) + ldsw + _i * 8192), 16, 0, 0); } while (0)
; #define PG8_LDA(dst, b, h) do { if constexpr (FP8) { _Pragma("unroll") for (int m = 0; m < 4; ++m) dst##8[m] = pg8_ld8(lds + PG8_SA(b, h) + aoff + m * 2048); } \
;         else { _Pragma("unroll") for (int m = 0; m < 4; ++m) _Pragma("unroll") for (int k = 0; k < 2; ++k) dst[m][k] = *(const PG8_LAS bf16x8*)(lds + PG8_SA(b, h) + aoff + m * 2048 + k * 1024); } } while (0)
; #define PG8_LDB(dst, b, h) do { if constexpr (FP8) { _Pragma("unroll") for (int n = 0; n < 2; ++n) dst##8[n] = pg8_ld8(lds + PG8_SB(b, h) + boff + n * 2048); } \
;         else { _Pragma("unroll") for (int n = 0; n < 2; ++n) _Pragma("unroll") for (int k = 0; k < 2; ++k) dst[n][k] = *(const PG8_LAS bf16x8*)(lds + PG8_SB(b, h) + boff + n * 2048 + k * 1024); } } while (0)
; #define PG8_WAIT_V(n) asm volatile("s_waitcnt vmcnt(" #n ")" ::: "memory")
; #define PG8_WAIT_L(n) asm volatile("s_waitcnt lgkmcnt(" #n ")" ::: "memory")
; #define PG8_BAR __builtin_amdgcn_s_barrier()
; #define PG8_SCHED __builtin_amdgcn_sched_barrier(0)
;     ...
;             const bool last = (t == nt - 2);
;             const char* a1 = cA + (size_t)(t + 1) * kstep;
;             const char* a2 = last ? nA : cA + (size_t)(t + 2) * kstep; const char* b2 = last ? nB : cB + (size_t)(t + 2) * kstep;
;             const char* a3 = a2 + kstep; const char* b3 = b2 + kstep;
;             if (last && has_next) S.a_ready(nxt);
;             if constexpr (SP2) {
;             PG8_LDB(B0, 0, 0); PG8_LDB(B1, 0, 1); PG8_SCHED; PG8_LDA(At, 0, 0); PG8_STAGE(PG8_SA(1, 1), a1 + hstep, voffA);
;             PG8_WAIT_V(8); PG8_WAIT_L(0); PG8_BAR; PG8_MMA(0, 0, At, B0); PG8_MMA(0, 1, At, B1); PG8_BAR; PG8_SCHED;
;             PG8_LDA(At, 0, 1); PG8_STAGE(PG8_SB(0, 0), b2, voffB); PG8_STAGE(PG8_SB(0, 1), b2 + hstep, voffB); PG8_STAGE(PG8_SA(0, 0), a2, voffA);
;             PG8_WAIT_V(8); PG8_WAIT_L(0); PG8_BAR; PG8_MMA(1, 0, At, B0); PG8_MMA(1, 1, At, B1); PG8_BAR; PG8_SCHED;
.LBB0_918:
	s_add_u32 s0, s24, 0xfffe0080
	s_addc_u32 s1, s25, -1
	s_add_i32 s45, 0, 0x10000
	s_cmp_eq_u32 s44, 4
	s_cselect_b32 s27, s13, s1
	s_cselect_b32 s26, s40, s0
	s_cselect_b32 s1, s15, s43
	s_cselect_b32 s0, s41, s42
	s_add_i32 s46, 0, 0x14000
	v_add_u32_e32 v0, s45, v190
	v_add_u32_e32 v12, s46, v190
	ds_read_b128 v[16:19], v0
	ds_read_b128 v[20:23], v0 offset:1024
	ds_read_b128 v[24:27], v0 offset:2048
	ds_read_b128 v[28:31], v0 offset:3072
	ds_read_b128 v[0:3], v12
	ds_read_b128 v[4:7], v12 offset:1024
	ds_read_b128 v[8:11], v12 offset:2048
	ds_read_b128 v[12:15], v12 offset:3072
	v_lshl_add_u64 v[230:231], s[24:25], 0, v[178:179]
	s_add_i32 m0, s21, 0xc000
	ds_read_b128 v[180:183], v205
	ds_read_b128 v[184:187], v205 offset:1024
	ds_read_b128 v[206:209], v205 offset:2048
	ds_read_b128 v[210:213], v205 offset:3072
	ds_read_b128 v[214:217], v205 offset:4096
	ds_read_b128 v[218:221], v205 offset:5120
	ds_read_b128 v[222:225], v205 offset:6144
	ds_read_b128 v[226:229], v205 offset:7168
	global_load_lds_dwordx4 v[230:231], off
	v_lshl_add_u64 v[230:231], s[24:25], 0, v[176:177]
	s_add_i32 m0, s21, 0xe000
	s_nop 0
	global_load_lds_dwordx4 v[230:231], off
	s_waitcnt vmcnt(8)
	s_waitcnt lgkmcnt(0)
	s_barrier
	s_setprio 1
	s_waitcnt lgkmcnt(0)
	v_mfma_scale_f32_16x16x128_f8f6f4 v[158:161], v[16:23], v[180:187], v[158:161], v189, v189 op_sel_hi:[0,0,0]
	v_mfma_scale_f32_16x16x128_f8f6f4 v[154:157], v[24:31], v[180:187], v[154:157], v189, v189 op_sel_hi:[0,0,0]
	v_mfma_scale_f32_16x16x128_f8f6f4 v[150:153], v[16:23], v[206:213], v[150:153], v189, v189 op_sel_hi:[0,0,0]
	v_mfma_scale_f32_16x16x128_f8f6f4 v[146:149], v[24:31], v[206:213], v[146:149], v189, v189 op_sel_hi:[0,0,0]
	v_mfma_scale_f32_16x16x128_f8f6f4 v[142:145], v[16:23], v[214:221], v[142:145], v189, v189 op_sel_hi:[0,0,0]
	v_mfma_scale_f32_16x16x128_f8f6f4 v[138:141], v[24:31], v[214:221], v[138:141], v189, v189 op_sel_hi:[0,0,0]
	v_mfma_scale_f32_16x16x128_f8f6f4 v[134:137], v[16:23], v[222:229], v[134:137], v189, v189 op_sel_hi:[0,0,0]
	v_mfma_scale_f32_16x16x128_f8f6f4 v[130:133], v[24:31], v[222:229], v[130:133], v189, v189 op_sel_hi:[0,0,0]
	v_mfma_scale_f32_16x16x128_f8f6f4 v[126:129], v[0:7], v[180:187], v[126:129], v189, v189 op_sel_hi:[0,0,0]
	v_mfma_scale_f32_16x16x128_f8f6f4 v[122:125], v[8:15], v[180:187], v[122:125], v189, v189 op_sel_hi:[0,0,0]
	v_mfma_scale_f32_16x16x128_f8f6f4 v[118:121], v[0:7], v[206:213], v[118:121], v189, v189 op_sel_hi:[0,0,0]
	v_mfma_scale_f32_16x16x128_f8f6f4 v[114:117], v[8:15], v[206:213], v[114:117], v189, v189 op_sel_hi:[0,0,0]
	v_mfma_scale_f32_16x16x128_f8f6f4 v[110:113], v[0:7], v[214:221], v[110:113], v189, v189 op_sel_hi:[0,0,0]
	v_mfma_scale_f32_16x16x128_f8f6f4 v[106:109], v[8:15], v[214:221], v[106:109], v189, v189 op_sel_hi:[0,0,0]
	v_mfma_scale_f32_16x16x128_f8f6f4 v[102:105], v[0:7], v[222:229], v[102:105], v189, v189 op_sel_hi:[0,0,0]
	v_mfma_scale_f32_16x16x128_f8f6f4 v[98:101], v[8:15], v[222:229], v[98:101], v189, v189 op_sel_hi:[0,0,0]
	s_setprio 0
	s_barrier
	s_add_i32 s45, s45, s29
	v_lshl_add_u64 v[180:181], s[0:1], 0, v[80:81]
	s_mov_b32 m0, s45
	ds_read_b128 v[206:209], v205 offset:16384
	ds_read_b128 v[210:213], v205 offset:17408
	ds_read_b128 v[214:217], v205 offset:18432
	ds_read_b128 v[218:221], v205 offset:19456
	ds_read_b128 v[222:225], v205 offset:20480
	ds_read_b128 v[226:229], v205 offset:21504
	ds_read_b128 v[230:233], v205 offset:22528
	ds_read_b128 v[234:237], v205 offset:23552
	global_load_lds_dwordx4 v[180:181], off
	s_add_i32 m0, s45, 0x2000
	s_add_u32 s48, s0, 0x20000
	v_lshl_add_u64 v[182:183], s[0:1], 0, v[174:175]
	s_addc_u32 s49, s1, 0
	s_add_i32 s45, s46, s29
	global_load_lds_dwordx4 v[182:183], off
	v_lshl_add_u64 v[184:185], s[48:49], 0, v[80:81]
	s_mov_b32 m0, s45
	v_lshl_add_u64 v[186:187], s[26:27], 0, v[174:175]
	global_load_lds_dwordx4 v[184:185], off
	v_lshl_add_u64 v[184:185], s[48:49], 0, v[174:175]
	s_add_i32 m0, s45, 0x2000
	s_nop 0
	global_load_lds_dwordx4 v[184:185], off
	v_lshl_add_u64 v[184:185], s[26:27], 0, v[80:81]
	s_mov_b32 m0, s21
	s_nop 0
	global_load_lds_dwordx4 v[184:185], off
	s_mov_b32 m0, s23
	s_nop 0
	global_load_lds_dwordx4 v[186:187], off
	s_waitcnt vmcnt(8)
	s_waitcnt lgkmcnt(0)
	s_barrier
	s_setprio 1
	s_waitcnt lgkmcnt(0)
	v_mfma_scale_f32_16x16x128_f8f6f4 v[94:97], v[16:23], v[206:213], v[94:97], v189, v189 op_sel_hi:[0,0,0]
	v_mfma_scale_f32_16x16x128_f8f6f4 v[90:93], v[24:31], v[206:213], v[90:93], v189, v189 op_sel_hi:[0,0,0]
	v_mfma_scale_f32_16x16x128_f8f6f4 v[86:89], v[16:23], v[214:221], v[86:89], v189, v189 op_sel_hi:[0,0,0]
	v_mfma_scale_f32_16x16x128_f8f6f4 v[82:85], v[24:31], v[214:221], v[82:85], v189, v189 op_sel_hi:[0,0,0]
	v_mfma_scale_f32_16x16x128_f8f6f4 v[76:79], v[16:23], v[222:229], v[76:79], v189, v189 op_sel_hi:[0,0,0]
	v_mfma_scale_f32_16x16x128_f8f6f4 v[72:75], v[24:31], v[222:229], v[72:75], v189, v189 op_sel_hi:[0,0,0]
	v_mfma_scale_f32_16x16x128_f8f6f4 v[68:71], v[16:23], v[230:237], v[68:71], v189, v189 op_sel_hi:[0,0,0]
	v_mfma_scale_f32_16x16x128_f8f6f4 v[64:67], v[24:31], v[230:237], v[64:67], v189, v189 op_sel_hi:[0,0,0]
	v_mfma_scale_f32_16x16x128_f8f6f4 v[60:63], v[0:7], v[206:213], v[60:63], v189, v189 op_sel_hi:[0,0,0]
	v_mfma_scale_f32_16x16x128_f8f6f4 v[56:59], v[8:15], v[206:213], v[56:59], v189, v189 op_sel_hi:[0,0,0]
	v_mfma_scale_f32_16x16x128_f8f6f4 v[52:55], v[0:7], v[214:221], v[52:55], v189, v189 op_sel_hi:[0,0,0]
	v_mfma_scale_f32_16x16x128_f8f6f4 v[48:51], v[8:15], v[214:221], v[48:51], v189, v189 op_sel_hi:[0,0,0]
	v_mfma_scale_f32_16x16x128_f8f6f4 v[44:47], v[0:7], v[222:229], v[44:47], v189, v189 op_sel_hi:[0,0,0]
	v_mfma_scale_f32_16x16x128_f8f6f4 v[40:43], v[8:15], v[222:229], v[40:43], v189, v189 op_sel_hi:[0,0,0]
	v_mfma_scale_f32_16x16x128_f8f6f4 v[36:39], v[0:7], v[230:237], v[36:39], v189, v189 op_sel_hi:[0,0,0]
	v_mfma_scale_f32_16x16x128_f8f6f4 v[32:35], v[8:15], v[230:237], v[32:35], v189, v189 op_sel_hi:[0,0,0]
	s_setprio 0
	s_barrier
; #define PG8_STAGE(bufoff, gbase, voff) do { _Pragma("unroll") for (int _i = 0; _i < 2; ++_i) \
;         __builtin_amdgcn_global_load_lds((const unsigned*)((const char*)(gbase) + (voff)[_i]), (PG8_LAS unsigned*)(lds + (bufoff) + ldsw + _i * 8192), 16, 0, 0); } while (0)
; #define PG8_LDA(dst, b, h) do { if constexpr (FP8) { _Pragma("unroll") for (int m = 0; m < 4; ++m) dst##8[m] = pg8_ld8(lds + PG8_SA(b, h) + aoff + m * 2048); } \
;         else { _Pragma("unroll") for (int m = 0; m < 4; ++m) _Pragma("unroll") for (int k = 0; k < 2; ++k) dst[m][k] = *(const PG8_LAS bf16x8*)(lds + PG8_SA(b, h) + aoff + m * 2048 + k * 1024); } } while (0)
; #define PG8_LDB(dst, b, h) do { if constexpr (FP8) { _Pragma("unroll") for (int n = 0; n < 2; ++n) dst##8[n] = pg8_ld8(lds + PG8_SB(b, h) + boff + n * 2048); } \
;         else { _Pragma("unroll") for (int n = 0; n < 2; ++n) _Pragma("unroll") for (int k = 0; k < 2; ++k) dst[n][k] = *(const PG8_LAS bf16x8*)(lds + PG8_SB(b, h) + boff + n * 2048 + k * 1024); } } while (0)
; #define PG8_WAIT_V(n) asm volatile("s_waitcnt vmcnt(" #n ")" ::: "memory")
; #define PG8_WAIT_L(n) asm volatile("s_waitcnt lgkmcnt(" #n ")" ::: "memory")
; #define PG8_BAR __builtin_amdgcn_s_barrier()
; #define PG8_SCHED __builtin_amdgcn_sched_barrier(0)
;     ...
;             PG8_LDB(B0, 1, 0); PG8_LDB(B1, 1, 1); PG8_SCHED; PG8_LDA(At, 1, 0); PG8_STAGE(PG8_SA(0, 1), a2 + hstep, voffA);
;             PG8_WAIT_V(8); PG8_WAIT_L(0); PG8_BAR; PG8_MMA(0, 0, At, B0); PG8_MMA(0, 1, At, B1); PG8_BAR; PG8_SCHED;
;             PG8_LDA(At, 1, 1); PG8_STAGE(PG8_SB(1, 0), b3, voffB); PG8_STAGE(PG8_SB(1, 1), b3 + hstep, voffB); PG8_STAGE(PG8_SA(1, 0), a3, voffA);
;             PG8_WAIT_V(8); PG8_WAIT_L(0); PG8_BAR; PG8_MMA(1, 0, At, B0); PG8_MMA(1, 1, At, B1); PG8_BAR; PG8_SCHED;
;     ...
;         if constexpr (FP8) asm volatile("s_nop 15\n\ts_nop 15" ::: "memory");
;         if constexpr (ALIGN_EPI) { if (wr == 0) PG8_BAR; }
	s_add_i32 s45, 0, 0x18000
	s_add_i32 s46, 0, 0x1c000
	v_add_u32_e32 v12, s45, v190
	v_add_u32_e32 v28, s46, v190
	ds_read_b128 v[0:3], v12
	ds_read_b128 v[4:7], v12 offset:1024
	ds_read_b128 v[8:11], v12 offset:2048
	ds_read_b128 v[12:15], v12 offset:3072
	ds_read_b128 v[16:19], v28
	ds_read_b128 v[20:23], v28 offset:1024
	ds_read_b128 v[24:27], v28 offset:2048
	ds_read_b128 v[28:31], v28 offset:3072
	s_add_u32 s26, s26, 0x20000
	s_addc_u32 s27, s27, 0
	s_mov_b32 m0, s34
	v_lshl_add_u64 v[238:239], s[26:27], 0, v[80:81]
	ds_read_b128 v[206:209], v205 offset:32768
	ds_read_b128 v[210:213], v205 offset:33792
	ds_read_b128 v[214:217], v205 offset:34816
	ds_read_b128 v[218:221], v205 offset:35840
	ds_read_b128 v[222:225], v205 offset:36864
	ds_read_b128 v[226:229], v205 offset:37888
	ds_read_b128 v[230:233], v205 offset:38912
	ds_read_b128 v[234:237], v205 offset:39936
	global_load_lds_dwordx4 v[238:239], off
	v_lshl_add_u64 v[238:239], s[26:27], 0, v[174:175]
	s_mov_b32 m0, s35
	s_nop 0
	global_load_lds_dwordx4 v[238:239], off
	s_waitcnt vmcnt(8)
	s_waitcnt lgkmcnt(0)
	s_barrier
	s_setprio 1
	s_waitcnt lgkmcnt(0)
	v_mfma_scale_f32_16x16x128_f8f6f4 v[158:161], v[0:7], v[206:213], v[158:161], v189, v189 op_sel_hi:[0,0,0]
	v_mfma_scale_f32_16x16x128_f8f6f4 v[154:157], v[8:15], v[206:213], v[154:157], v189, v189 op_sel_hi:[0,0,0]
	v_mfma_scale_f32_16x16x128_f8f6f4 v[150:153], v[0:7], v[214:221], v[150:153], v189, v189 op_sel_hi:[0,0,0]
	v_mfma_scale_f32_16x16x128_f8f6f4 v[146:149], v[8:15], v[214:221], v[146:149], v189, v189 op_sel_hi:[0,0,0]
	v_mfma_scale_f32_16x16x128_f8f6f4 v[142:145], v[0:7], v[222:229], v[142:145], v189, v189 op_sel_hi:[0,0,0]
	v_mfma_scale_f32_16x16x128_f8f6f4 v[138:141], v[8:15], v[222:229], v[138:141], v189, v189 op_sel_hi:[0,0,0]
	v_mfma_scale_f32_16x16x128_f8f6f4 v[134:137], v[0:7], v[230:237], v[134:137], v189, v189 op_sel_hi:[0,0,0]
	v_mfma_scale_f32_16x16x128_f8f6f4 v[130:133], v[8:15], v[230:237], v[130:133], v189, v189 op_sel_hi:[0,0,0]
	v_mfma_scale_f32_16x16x128_f8f6f4 v[126:129], v[16:23], v[206:213], v[126:129], v189, v189 op_sel_hi:[0,0,0]
	v_mfma_scale_f32_16x16x128_f8f6f4 v[122:125], v[24:31], v[206:213], v[122:125], v189, v189 op_sel_hi:[0,0,0]
	v_mfma_scale_f32_16x16x128_f8f6f4 v[118:121], v[16:23], v[214:221], v[118:121], v189, v189 op_sel_hi:[0,0,0]
	v_mfma_scale_f32_16x16x128_f8f6f4 v[114:117], v[24:31], v[214:221], v[114:117], v189, v189 op_sel_hi:[0,0,0]
	v_mfma_scale_f32_16x16x128_f8f6f4 v[110:113], v[16:23], v[222:229], v[110:113], v189, v189 op_sel_hi:[0,0,0]
	v_mfma_scale_f32_16x16x128_f8f6f4 v[106:109], v[24:31], v[222:229], v[106:109], v189, v189 op_sel_hi:[0,0,0]
	v_mfma_scale_f32_16x16x128_f8f6f4 v[102:105], v[16:23], v[230:237], v[102:105], v189, v189 op_sel_hi:[0,0,0]
	v_mfma_scale_f32_16x16x128_f8f6f4 v[98:101], v[24:31], v[230:237], v[98:101], v189, v189 op_sel_hi:[0,0,0]
	s_setprio 0
	s_barrier
	s_add_i32 s26, s45, s29
	v_lshl_add_u64 v[180:181], v[180:181], 0, s[86:87]
	s_mov_b32 m0, s26
	ds_read_b128 v[206:209], v205 offset:49152
	ds_read_b128 v[210:213], v205 offset:50176
	ds_read_b128 v[214:217], v205 offset:51200
	ds_read_b128 v[218:221], v205 offset:52224
	ds_read_b128 v[222:225], v205 offset:53248
	ds_read_b128 v[226:229], v205 offset:54272
	ds_read_b128 v[230:233], v205 offset:55296
	ds_read_b128 v[234:237], v205 offset:56320
	global_load_lds_dwordx4 v[180:181], off
	s_add_i32 m0, s26, 0x2000
	s_add_u32 s0, s0, 0x20080
	v_lshl_add_u64 v[180:181], v[182:183], 0, s[86:87]
	s_addc_u32 s1, s1, 0
	s_add_i32 s26, s46, s29
	global_load_lds_dwordx4 v[180:181], off
	v_lshl_add_u64 v[180:181], s[0:1], 0, v[80:81]
	s_mov_b32 m0, s26
	s_nop 0
	global_load_lds_dwordx4 v[180:181], off
	v_lshl_add_u64 v[180:181], s[0:1], 0, v[174:175]
	s_add_i32 m0, s26, 0x2000
	s_nop 0
	global_load_lds_dwordx4 v[180:181], off
	v_lshl_add_u64 v[180:181], v[184:185], 0, s[86:87]
	s_mov_b32 m0, s36
	s_nop 0
	global_load_lds_dwordx4 v[180:181], off
	v_lshl_add_u64 v[180:181], v[186:187], 0, s[86:87]
	s_mov_b32 m0, s37
	s_nop 0
	global_load_lds_dwordx4 v[180:181], off
	s_waitcnt vmcnt(8)
	s_waitcnt lgkmcnt(0)
	s_barrier
	s_setprio 1
	s_waitcnt lgkmcnt(0)
	v_mfma_scale_f32_16x16x128_f8f6f4 v[94:97], v[0:7], v[206:213], v[94:97], v189, v189 op_sel_hi:[0,0,0]
	v_mfma_scale_f32_16x16x128_f8f6f4 v[90:93], v[8:15], v[206:213], v[90:93], v189, v189 op_sel_hi:[0,0,0]
	v_mfma_scale_f32_16x16x128_f8f6f4 v[86:89], v[0:7], v[214:221], v[86:89], v189, v189 op_sel_hi:[0,0,0]
	v_mfma_scale_f32_16x16x128_f8f6f4 v[82:85], v[8:15], v[214:221], v[82:85], v189, v189 op_sel_hi:[0,0,0]
	v_mfma_scale_f32_16x16x128_f8f6f4 v[76:79], v[0:7], v[222:229], v[76:79], v189, v189 op_sel_hi:[0,0,0]
	v_mfma_scale_f32_16x16x128_f8f6f4 v[72:75], v[8:15], v[222:229], v[72:75], v189, v189 op_sel_hi:[0,0,0]
	v_mfma_scale_f32_16x16x128_f8f6f4 v[68:71], v[0:7], v[230:237], v[68:71], v189, v189 op_sel_hi:[0,0,0]
	v_mfma_scale_f32_16x16x128_f8f6f4 v[64:67], v[8:15], v[230:237], v[64:67], v189, v189 op_sel_hi:[0,0,0]
	v_mfma_scale_f32_16x16x128_f8f6f4 v[60:63], v[16:23], v[206:213], v[60:63], v189, v189 op_sel_hi:[0,0,0]
	v_mfma_scale_f32_16x16x128_f8f6f4 v[56:59], v[24:31], v[206:213], v[56:59], v189, v189 op_sel_hi:[0,0,0]
	v_mfma_scale_f32_16x16x128_f8f6f4 v[52:55], v[16:23], v[214:221], v[52:55], v189, v189 op_sel_hi:[0,0,0]
	v_mfma_scale_f32_16x16x128_f8f6f4 v[48:51], v[24:31], v[214:221], v[48:51], v189, v189 op_sel_hi:[0,0,0]
	v_mfma_scale_f32_16x16x128_f8f6f4 v[44:47], v[16:23], v[222:229], v[44:47], v189, v189 op_sel_hi:[0,0,0]
	v_mfma_scale_f32_16x16x128_f8f6f4 v[40:43], v[24:31], v[222:229], v[40:43], v189, v189 op_sel_hi:[0,0,0]
	v_mfma_scale_f32_16x16x128_f8f6f4 v[36:39], v[16:23], v[230:237], v[36:39], v189, v189 op_sel_hi:[0,0,0]
	v_mfma_scale_f32_16x16x128_f8f6f4 v[32:35], v[24:31], v[230:237], v[32:35], v189, v189 op_sel_hi:[0,0,0]
	s_setprio 0
	s_barrier
	s_add_i32 s44, s44, 2
	s_add_u32 s42, s42, 0x100
	s_addc_u32 s43, s43, 0
	s_add_u32 s24, s24, 0x100
	s_addc_u32 s25, s25, 0
	s_cmp_gt_u32 s44, 5
	s_cbranch_scc0 .LBB0_918
	s_nop 15
	s_nop 15
	s_and_b64 vcc, exec, s[8:9]
	s_cbranch_vccz .LBB0_921
	s_barrier

; #define PG8_STAGE(bufoff, gbase, voff) do { _Pragma("unroll") for (int _i = 0; _i < 2; ++_i) \
;         __builtin_amdgcn_global_load_lds((const unsigned*)((const char*)(gbase) + (voff)[_i]), (PG8_LAS unsigned*)(lds + (bufoff) + ldsw + _i * 8192), 16, 0, 0); } while (0)
; #define PG8_LDA(dst, b, h) do { if constexpr (FP8) { _Pragma("unroll") for (int m = 0; m < 4; ++m) dst##8[m] = pg8_ld8(lds + PG8_SA(b, h) + aoff + m * 2048); } \
;         else { _Pragma("unroll") for (int m = 0; m < 4; ++m) _Pragma("unroll") for (int k = 0; k < 2; ++k) dst[m][k] = *(const PG8_LAS bf16x8*)(lds + PG8_SA(b, h) + aoff + m * 2048 + k * 1024); } } while (0)
; #define PG8_LDB(dst, b, h) do { if constexpr (FP8) { _Pragma("unroll") for (int n = 0; n < 2; ++n) dst##8[n] = pg8_ld8(lds + PG8_SB(b, h) + boff + n * 2048); } \
;         else { _Pragma("unroll") for (int n = 0; n < 2; ++n) _Pragma("unroll") for (int k = 0; k < 2; ++k) dst[n][k] = *(const PG8_LAS bf16x8*)(lds + PG8_SB(b, h) + boff + n * 2048 + k * 1024); } } while (0)
; #define PG8_WAIT_V(n) asm volatile("s_waitcnt vmcnt(" #n ")" ::: "memory")
; #define PG8_WAIT_L(n) asm volatile("s_waitcnt lgkmcnt(" #n ")" ::: "memory")
; #define PG8_BAR __builtin_amdgcn_s_barrier()
; #define PG8_SCHED __builtin_amdgcn_sched_barrier(0)
;     ...
;             const bool last = (t == nt - 2);
;             const char* a1 = cA + (size_t)(t + 1) * kstep;
;             const char* a2 = last ? nA : cA + (size_t)(t + 2) * kstep; const char* b2 = last ? nB : cB + (size_t)(t + 2) * kstep;
;             const char* a3 = a2 + kstep; const char* b3 = b2 + kstep;
;             if (last && has_next) S.a_ready(nxt);
;             if constexpr (SP2) {
;             PG8_LDB(B0, 0, 0); PG8_LDB(B1, 0, 1); PG8_SCHED; PG8_LDA(At, 0, 0); PG8_STAGE(PG8_SA(1, 1), a1 + hstep, voffA);
;             PG8_WAIT_V(8); PG8_WAIT_L(0); PG8_BAR; PG8_MMA(0, 0, At, B0); PG8_MMA(0, 1, At, B1); PG8_BAR; PG8_SCHED;
;             PG8_LDA(At, 0, 1); PG8_STAGE(PG8_SB(0, 0), b2, voffB); PG8_STAGE(PG8_SB(0, 1), b2 + hstep, voffB); PG8_STAGE(PG8_SA(0, 0), a2, voffA);
.LBB0_946:
	s_add_i32 s47, s0, 2
	s_add_u32 s48, s20, 0x80
	s_addc_u32 s1, s21, 0
	s_add_i32 s50, 0, 0x10000
	s_cmp_eq_u32 s41, s0
	s_cselect_b32 s1, s17, s1
	s_cselect_b32 s0, s16, s48
	s_cselect_b32 s49, s19, s46
	s_cselect_b32 s48, s18, s45
	s_add_i32 s51, 0, 0x14000
	v_add_u32_e32 v154, s50, v140
	v_add_u32_e32 v170, s51, v140
	ds_read_b128 v[142:145], v154
	ds_read_b128 v[146:149], v154 offset:1024
	ds_read_b128 v[150:153], v154 offset:2048
	ds_read_b128 v[154:157], v154 offset:3072
	ds_read_b128 v[158:161], v170
	ds_read_b128 v[174:177], v170 offset:1024
	ds_read_b128 v[178:181], v170 offset:2048
	ds_read_b128 v[182:185], v170 offset:3072
	v_lshl_add_u64 v[190:191], s[20:21], 0, v[138:139]
	s_add_i32 m0, s28, 0xc000
	ds_read_b128 v[186:189], v141
	ds_read_b128 v[206:209], v141 offset:1024
	ds_read_b128 v[210:213], v141 offset:2048
	ds_read_b128 v[214:217], v141 offset:3072
	ds_read_b128 v[218:221], v141 offset:4096
	ds_read_b128 v[222:225], v141 offset:5120
	ds_read_b128 v[226:229], v141 offset:6144
	ds_read_b128 v[230:233], v141 offset:7168
	global_load_lds_dwordx4 v[190:191], off
	v_lshl_add_u64 v[190:191], s[20:21], 0, v[136:137]
	s_add_i32 m0, s28, 0xe000
	s_nop 0
	global_load_lds_dwordx4 v[190:191], off
	s_waitcnt vmcnt(8)
	s_waitcnt lgkmcnt(0)
	s_barrier
	s_setprio 1
	s_waitcnt lgkmcnt(0)
	v_mfma_f32_16x16x32_bf16 v[122:125], v[142:145], v[186:189], v[122:125]
	v_mfma_f32_16x16x32_bf16 v[126:129], v[150:153], v[186:189], v[126:129]
	v_mfma_f32_16x16x32_bf16 v[110:113], v[142:145], v[210:213], v[110:113]
	v_mfma_f32_16x16x32_bf16 v[106:109], v[150:153], v[210:213], v[106:109]
	v_mfma_f32_16x16x32_bf16 v[94:97], v[142:145], v[218:221], v[94:97]
	v_mfma_f32_16x16x32_bf16 v[90:93], v[150:153], v[218:221], v[90:93]
	v_mfma_f32_16x16x32_bf16 v[76:79], v[142:145], v[226:229], v[76:79]
	v_mfma_f32_16x16x32_bf16 v[72:75], v[150:153], v[226:229], v[72:75]
	v_mfma_f32_16x16x32_bf16 v[122:125], v[146:149], v[206:209], v[122:125]
	v_mfma_f32_16x16x32_bf16 v[126:129], v[154:157], v[206:209], v[126:129]
	v_mfma_f32_16x16x32_bf16 v[110:113], v[146:149], v[214:217], v[110:113]
	v_mfma_f32_16x16x32_bf16 v[106:109], v[154:157], v[214:217], v[106:109]
	v_mfma_f32_16x16x32_bf16 v[94:97], v[146:149], v[222:225], v[94:97]
	v_mfma_f32_16x16x32_bf16 v[90:93], v[154:157], v[222:225], v[90:93]
	v_mfma_f32_16x16x32_bf16 v[76:79], v[146:149], v[230:233], v[76:79]
	v_mfma_f32_16x16x32_bf16 v[72:75], v[154:157], v[230:233], v[72:75]
	v_mfma_f32_16x16x32_bf16 v[118:121], v[158:161], v[186:189], v[118:121]
	v_mfma_f32_16x16x32_bf16 v[114:117], v[178:181], v[186:189], v[114:117]
	v_mfma_f32_16x16x32_bf16 v[102:105], v[158:161], v[210:213], v[102:105]
	v_mfma_f32_16x16x32_bf16 v[98:101], v[178:181], v[210:213], v[98:101]
	v_mfma_f32_16x16x32_bf16 v[86:89], v[158:161], v[218:221], v[86:89]
	v_mfma_f32_16x16x32_bf16 v[82:85], v[178:181], v[218:221], v[82:85]
	v_mfma_f32_16x16x32_bf16 v[68:71], v[158:161], v[226:229], v[68:71]
	v_mfma_f32_16x16x32_bf16 v[64:67], v[178:181], v[226:229], v[64:67]
	v_mfma_f32_16x16x32_bf16 v[118:121], v[174:177], v[206:209], v[118:121]
	v_mfma_f32_16x16x32_bf16 v[114:117], v[182:185], v[206:209], v[114:117]
	v_mfma_f32_16x16x32_bf16 v[102:105], v[174:177], v[214:217], v[102:105]
	v_mfma_f32_16x16x32_bf16 v[98:101], v[182:185], v[214:217], v[98:101]
	v_mfma_f32_16x16x32_bf16 v[86:89], v[174:177], v[222:225], v[86:89]
	v_mfma_f32_16x16x32_bf16 v[82:85], v[182:185], v[222:225], v[82:85]
	v_mfma_f32_16x16x32_bf16 v[68:71], v[174:177], v[230:233], v[68:71]
	v_mfma_f32_16x16x32_bf16 v[64:67], v[182:185], v[230:233], v[64:67]
	s_setprio 0
	s_barrier
	s_add_i32 s50, s50, s27
	v_lshl_add_u64 v[190:191], s[48:49], 0, v[80:81]
	s_mov_b32 m0, s50
	ds_read_b128 v[186:189], v141 offset:16384
	ds_read_b128 v[206:209], v141 offset:17408
	ds_read_b128 v[210:213], v141 offset:18432
	ds_read_b128 v[214:217], v141 offset:19456
	ds_read_b128 v[218:221], v141 offset:20480
	ds_read_b128 v[222:225], v141 offset:21504
	ds_read_b128 v[226:229], v141 offset:22528
	ds_read_b128 v[230:233], v141 offset:23552
	global_load_lds_dwordx4 v[190:191], off
	s_add_i32 m0, s50, 0x2000
	v_lshl_add_u64 v[234:235], s[48:49], 0, v[130:131]
	s_add_u32 s48, s48, s6
	s_addc_u32 s49, s49, s7
	s_add_i32 s50, s51, s27
	global_load_lds_dwordx4 v[234:235], off
	v_lshl_add_u64 v[236:237], s[48:49], 0, v[80:81]
	s_mov_b32 m0, s50
	v_lshl_add_u64 v[238:239], s[48:49], 0, v[130:131]
	global_load_lds_dwordx4 v[236:237], off
	s_add_i32 m0, s50, 0x2000
	v_lshl_add_u64 v[240:241], s[0:1], 0, v[134:135]
	global_load_lds_dwordx4 v[238:239], off
	s_mov_b32 m0, s28
	v_lshl_add_u64 v[242:243], s[0:1], 0, v[132:133]
	global_load_lds_dwordx4 v[240:241], off
	s_mov_b32 m0, s29
	s_nop 0
	global_load_lds_dwordx4 v[242:243], off
	s_waitcnt vmcnt(8)
	s_waitcnt lgkmcnt(0)
	s_barrier
; #define PG8_STAGE(bufoff, gbase, voff) do { _Pragma("unroll") for (int _i = 0; _i < 2; ++_i) \
;         __builtin_amdgcn_global_load_lds((const unsigned*)((const char*)(gbase) + (voff)[_i]), (PG8_LAS unsigned*)(lds + (bufoff) + ldsw + _i * 8192), 16, 0, 0); } while (0)
; #define PG8_LDA(dst, b, h) do { if constexpr (FP8) { _Pragma("unroll") for (int m = 0; m < 4; ++m) dst##8[m] = pg8_ld8(lds + PG8_SA(b, h) + aoff + m * 2048); } \
;         else { _Pragma("unroll") for (int m = 0; m < 4; ++m) _Pragma("unroll") for (int k = 0; k < 2; ++k) dst[m][k] = *(const PG8_LAS bf16x8*)(lds + PG8_SA(b, h) + aoff + m * 2048 + k * 1024); } } while (0)
; #define PG8_LDB(dst, b, h) do { if constexpr (FP8) { _Pragma("unroll") for (int n = 0; n < 2; ++n) dst##8[n] = pg8_ld8(lds + PG8_SB(b, h) + boff + n * 2048); } \
;         else { _Pragma("unroll") for (int n = 0; n < 2; ++n) _Pragma("unroll") for (int k = 0; k < 2; ++k) dst[n][k] = *(const PG8_LAS bf16x8*)(lds + PG8_SB(b, h) + boff + n * 2048 + k * 1024); } } while (0)
; #define PG8_WAIT_V(n) asm volatile("s_waitcnt vmcnt(" #n ")" ::: "memory")
; #define PG8_WAIT_L(n) asm volatile("s_waitcnt lgkmcnt(" #n ")" ::: "memory")
; #define PG8_BAR __builtin_amdgcn_s_barrier()
; #define PG8_SCHED __builtin_amdgcn_sched_barrier(0)
;     ...
;             PG8_WAIT_V(8); PG8_WAIT_L(0); PG8_BAR; PG8_MMA(0, 0, At, B0); PG8_MMA(0, 1, At, B1); PG8_BAR; PG8_SCHED;
;             PG8_LDA(At, 0, 1); PG8_STAGE(PG8_SB(0, 0), b2, voffB); PG8_STAGE(PG8_SB(0, 1), b2 + hstep, voffB); PG8_STAGE(PG8_SA(0, 0), a2, voffA);
;             PG8_WAIT_V(8); PG8_WAIT_L(0); PG8_BAR; PG8_MMA(1, 0, At, B0); PG8_MMA(1, 1, At, B1); PG8_BAR; PG8_SCHED;
;             PG8_LDB(B0, 1, 0); PG8_LDB(B1, 1, 1); PG8_SCHED; PG8_LDA(At, 1, 0); PG8_STAGE(PG8_SA(0, 1), a2 + hstep, voffA);
;             PG8_WAIT_V(8); PG8_WAIT_L(0); PG8_BAR; PG8_MMA(0, 0, At, B0); PG8_MMA(0, 1, At, B1); PG8_BAR; PG8_SCHED;
	s_setprio 1
	s_waitcnt lgkmcnt(0)
	v_mfma_f32_16x16x32_bf16 v[60:63], v[142:145], v[186:189], v[60:63]
	v_mfma_f32_16x16x32_bf16 v[56:59], v[150:153], v[186:189], v[56:59]
	v_mfma_f32_16x16x32_bf16 v[44:47], v[142:145], v[210:213], v[44:47]
	v_mfma_f32_16x16x32_bf16 v[40:43], v[150:153], v[210:213], v[40:43]
	v_mfma_f32_16x16x32_bf16 v[28:31], v[142:145], v[218:221], v[28:31]
	v_mfma_f32_16x16x32_bf16 v[24:27], v[150:153], v[218:221], v[24:27]
	v_mfma_f32_16x16x32_bf16 v[12:15], v[142:145], v[226:229], v[12:15]
	v_mfma_f32_16x16x32_bf16 v[8:11], v[150:153], v[226:229], v[8:11]
	v_mfma_f32_16x16x32_bf16 v[60:63], v[146:149], v[206:209], v[60:63]
	v_mfma_f32_16x16x32_bf16 v[56:59], v[154:157], v[206:209], v[56:59]
	v_mfma_f32_16x16x32_bf16 v[44:47], v[146:149], v[214:217], v[44:47]
	v_mfma_f32_16x16x32_bf16 v[40:43], v[154:157], v[214:217], v[40:43]
	v_mfma_f32_16x16x32_bf16 v[28:31], v[146:149], v[222:225], v[28:31]
	v_mfma_f32_16x16x32_bf16 v[24:27], v[154:157], v[222:225], v[24:27]
	v_mfma_f32_16x16x32_bf16 v[12:15], v[146:149], v[230:233], v[12:15]
	v_mfma_f32_16x16x32_bf16 v[8:11], v[154:157], v[230:233], v[8:11]
	v_mfma_f32_16x16x32_bf16 v[52:55], v[158:161], v[186:189], v[52:55]
	v_mfma_f32_16x16x32_bf16 v[48:51], v[178:181], v[186:189], v[48:51]
	v_mfma_f32_16x16x32_bf16 v[36:39], v[158:161], v[210:213], v[36:39]
	v_mfma_f32_16x16x32_bf16 v[32:35], v[178:181], v[210:213], v[32:35]
	v_mfma_f32_16x16x32_bf16 v[20:23], v[158:161], v[218:221], v[20:23]
	v_mfma_f32_16x16x32_bf16 v[16:19], v[178:181], v[218:221], v[16:19]
	v_mfma_f32_16x16x32_bf16 v[4:7], v[158:161], v[226:229], v[4:7]
	v_mfma_f32_16x16x32_bf16 v[0:3], v[178:181], v[226:229], v[0:3]
	v_mfma_f32_16x16x32_bf16 v[52:55], v[174:177], v[206:209], v[52:55]
	v_mfma_f32_16x16x32_bf16 v[48:51], v[182:185], v[206:209], v[48:51]
	v_mfma_f32_16x16x32_bf16 v[36:39], v[174:177], v[214:217], v[36:39]
	v_mfma_f32_16x16x32_bf16 v[32:35], v[182:185], v[214:217], v[32:35]
	v_mfma_f32_16x16x32_bf16 v[20:23], v[174:177], v[222:225], v[20:23]
	v_mfma_f32_16x16x32_bf16 v[16:19], v[182:185], v[222:225], v[16:19]
	v_mfma_f32_16x16x32_bf16 v[4:7], v[174:177], v[230:233], v[4:7]
	v_mfma_f32_16x16x32_bf16 v[0:3], v[182:185], v[230:233], v[0:3]
	s_setprio 0
	s_barrier
	s_add_i32 s48, 0, 0x18000
	s_add_i32 s49, 0, 0x1c000
	v_add_u32_e32 v154, s48, v140
	v_add_u32_e32 v170, s49, v140
	ds_read_b128 v[142:145], v154
	ds_read_b128 v[146:149], v154 offset:1024
	ds_read_b128 v[150:153], v154 offset:2048
	ds_read_b128 v[154:157], v154 offset:3072
	ds_read_b128 v[158:161], v170
	ds_read_b128 v[174:177], v170 offset:1024
	ds_read_b128 v[178:181], v170 offset:2048
	ds_read_b128 v[182:185], v170 offset:3072
	s_add_u32 s0, s0, s6
	s_addc_u32 s1, s1, s7
	s_mov_b32 m0, s30
	v_lshl_add_u64 v[244:245], s[0:1], 0, v[134:135]
	ds_read_b128 v[186:189], v141 offset:32768
	ds_read_b128 v[206:209], v141 offset:33792
	ds_read_b128 v[210:213], v141 offset:34816
	ds_read_b128 v[214:217], v141 offset:35840
	ds_read_b128 v[218:221], v141 offset:36864
	ds_read_b128 v[222:225], v141 offset:37888
	ds_read_b128 v[226:229], v141 offset:38912
	ds_read_b128 v[230:233], v141 offset:39936
	global_load_lds_dwordx4 v[244:245], off
	v_lshl_add_u64 v[244:245], s[0:1], 0, v[132:133]
	s_mov_b32 m0, s31
	s_nop 0
	global_load_lds_dwordx4 v[244:245], off
	s_waitcnt vmcnt(8)
	s_waitcnt lgkmcnt(0)
	s_barrier
	s_setprio 1
	s_waitcnt lgkmcnt(0)
	v_mfma_f32_16x16x32_bf16 v[122:125], v[142:145], v[186:189], v[122:125]
	v_mfma_f32_16x16x32_bf16 v[126:129], v[150:153], v[186:189], v[126:129]
	v_mfma_f32_16x16x32_bf16 v[110:113], v[142:145], v[210:213], v[110:113]
	v_mfma_f32_16x16x32_bf16 v[106:109], v[150:153], v[210:213], v[106:109]
	v_mfma_f32_16x16x32_bf16 v[94:97], v[142:145], v[218:221], v[94:97]
	v_mfma_f32_16x16x32_bf16 v[90:93], v[150:153], v[218:221], v[90:93]
	v_mfma_f32_16x16x32_bf16 v[76:79], v[142:145], v[226:229], v[76:79]
	v_mfma_f32_16x16x32_bf16 v[72:75], v[150:153], v[226:229], v[72:75]
	v_mfma_f32_16x16x32_bf16 v[122:125], v[146:149], v[206:209], v[122:125]
	v_mfma_f32_16x16x32_bf16 v[126:129], v[154:157], v[206:209], v[126:129]
	v_mfma_f32_16x16x32_bf16 v[110:113], v[146:149], v[214:217], v[110:113]
	v_mfma_f32_16x16x32_bf16 v[106:109], v[154:157], v[214:217], v[106:109]
	v_mfma_f32_16x16x32_bf16 v[94:97], v[146:149], v[222:225], v[94:97]
	v_mfma_f32_16x16x32_bf16 v[90:93], v[154:157], v[222:225], v[90:93]
	v_mfma_f32_16x16x32_bf16 v[76:79], v[146:149], v[230:233], v[76:79]
	v_mfma_f32_16x16x32_bf16 v[72:75], v[154:157], v[230:233], v[72:75]
	v_mfma_f32_16x16x32_bf16 v[118:121], v[158:161], v[186:189], v[118:121]
	v_mfma_f32_16x16x32_bf16 v[114:117], v[178:181], v[186:189], v[114:117]
	v_mfma_f32_16x16x32_bf16 v[102:105], v[158:161], v[210:213], v[102:105]
	v_mfma_f32_16x16x32_bf16 v[98:101], v[178:181], v[210:213], v[98:101]
	v_mfma_f32_16x16x32_bf16 v[86:89], v[158:161], v[218:221], v[86:89]
	v_mfma_f32_16x16x32_bf16 v[82:85], v[178:181], v[218:221], v[82:85]
	v_mfma_f32_16x16x32_bf16 v[68:71], v[158:161], v[226:229], v[68:71]
	v_mfma_f32_16x16x32_bf16 v[64:67], v[178:181], v[226:229], v[64:67]
	v_mfma_f32_16x16x32_bf16 v[118:121], v[174:177], v[206:209], v[118:121]
	v_mfma_f32_16x16x32_bf16 v[114:117], v[182:185], v[206:209], v[114:117]
	v_mfma_f32_16x16x32_bf16 v[102:105], v[174:177], v[214:217], v[102:105]
	v_mfma_f32_16x16x32_bf16 v[98:101], v[182:185], v[214:217], v[98:101]
	v_mfma_f32_16x16x32_bf16 v[86:89], v[174:177], v[222:225], v[86:89]
	v_mfma_f32_16x16x32_bf16 v[82:85], v[182:185], v[222:225], v[82:85]
	v_mfma_f32_16x16x32_bf16 v[68:71], v[174:177], v[230:233], v[68:71]
	v_mfma_f32_16x16x32_bf16 v[64:67], v[182:185], v[230:233], v[64:67]
	s_setprio 0
	s_barrier
; #define PG8_STAGE(bufoff, gbase, voff) do { _Pragma("unroll") for (int _i = 0; _i < 2; ++_i) \
;         __builtin_amdgcn_global_load_lds((const unsigned*)((const char*)(gbase) + (voff)[_i]), (PG8_LAS unsigned*)(lds + (bufoff) + ldsw + _i * 8192), 16, 0, 0); } while (0)
; #define PG8_LDA(dst, b, h) do { if constexpr (FP8) { _Pragma("unroll") for (int m = 0; m < 4; ++m) dst##8[m] = pg8_ld8(lds + PG8_SA(b, h) + aoff + m * 2048); } \
;         else { _Pragma("unroll") for (int m = 0; m < 4; ++m) _Pragma("unroll") for (int k = 0; k < 2; ++k) dst[m][k] = *(const PG8_LAS bf16x8*)(lds + PG8_SA(b, h) + aoff + m * 2048 + k * 1024); } } while (0)
; #define PG8_WAIT_V(n) asm volatile("s_waitcnt vmcnt(" #n ")" ::: "memory")
; #define PG8_WAIT_L(n) asm volatile("s_waitcnt lgkmcnt(" #n ")" ::: "memory")
; #define PG8_BAR __builtin_amdgcn_s_barrier()
; #define PG8_SCHED __builtin_amdgcn_sched_barrier(0)
;     ...
;         for (int t = 0; t < nt; t += 2) {
;     ...
;             PG8_LDA(At, 1, 1); PG8_STAGE(PG8_SB(1, 0), b3, voffB); PG8_STAGE(PG8_SB(1, 1), b3 + hstep, voffB); PG8_STAGE(PG8_SA(1, 0), a3, voffA);
;             PG8_WAIT_V(8); PG8_WAIT_L(0); PG8_BAR; PG8_MMA(1, 0, At, B0); PG8_MMA(1, 1, At, B1); PG8_BAR; PG8_SCHED;
	s_add_i32 s0, s48, s27
	v_lshl_add_u64 v[190:191], v[190:191], 0, s[86:87]
	s_mov_b32 m0, s0
	ds_read_b128 v[186:189], v141 offset:49152
	ds_read_b128 v[206:209], v141 offset:50176
	ds_read_b128 v[210:213], v141 offset:51200
	ds_read_b128 v[214:217], v141 offset:52224
	ds_read_b128 v[218:221], v141 offset:53248
	ds_read_b128 v[222:225], v141 offset:54272
	ds_read_b128 v[226:229], v141 offset:55296
	ds_read_b128 v[230:233], v141 offset:56320
	global_load_lds_dwordx4 v[190:191], off
	v_lshl_add_u64 v[190:191], v[234:235], 0, s[86:87]
	s_add_i32 m0, s0, 0x2000
	s_add_i32 s0, s49, s27
	global_load_lds_dwordx4 v[190:191], off
	v_lshl_add_u64 v[190:191], v[236:237], 0, s[86:87]
	s_mov_b32 m0, s0
	s_nop 0
	global_load_lds_dwordx4 v[190:191], off
	v_lshl_add_u64 v[190:191], v[238:239], 0, s[86:87]
	s_add_i32 m0, s0, 0x2000
	s_nop 0
	global_load_lds_dwordx4 v[190:191], off
	v_lshl_add_u64 v[190:191], v[240:241], 0, s[86:87]
	s_mov_b32 m0, s39
	s_nop 0
	global_load_lds_dwordx4 v[190:191], off
	v_lshl_add_u64 v[190:191], v[242:243], 0, s[86:87]
	s_mov_b32 m0, s40
	s_nop 0
	global_load_lds_dwordx4 v[190:191], off
	s_waitcnt vmcnt(8)
	s_waitcnt lgkmcnt(0)
	s_barrier
	s_setprio 1
	s_waitcnt lgkmcnt(0)
	v_mfma_f32_16x16x32_bf16 v[60:63], v[142:145], v[186:189], v[60:63]
	v_mfma_f32_16x16x32_bf16 v[56:59], v[150:153], v[186:189], v[56:59]
	v_mfma_f32_16x16x32_bf16 v[44:47], v[142:145], v[210:213], v[44:47]
	v_mfma_f32_16x16x32_bf16 v[40:43], v[150:153], v[210:213], v[40:43]
	v_mfma_f32_16x16x32_bf16 v[28:31], v[142:145], v[218:221], v[28:31]
	v_mfma_f32_16x16x32_bf16 v[24:27], v[150:153], v[218:221], v[24:27]
	v_mfma_f32_16x16x32_bf16 v[12:15], v[142:145], v[226:229], v[12:15]
	v_mfma_f32_16x16x32_bf16 v[8:11], v[150:153], v[226:229], v[8:11]
	v_mfma_f32_16x16x32_bf16 v[60:63], v[146:149], v[206:209], v[60:63]
	v_mfma_f32_16x16x32_bf16 v[56:59], v[154:157], v[206:209], v[56:59]
	v_mfma_f32_16x16x32_bf16 v[44:47], v[146:149], v[214:217], v[44:47]
	v_mfma_f32_16x16x32_bf16 v[40:43], v[154:157], v[214:217], v[40:43]
	v_mfma_f32_16x16x32_bf16 v[28:31], v[146:149], v[222:225], v[28:31]
	v_mfma_f32_16x16x32_bf16 v[24:27], v[154:157], v[222:225], v[24:27]
	v_mfma_f32_16x16x32_bf16 v[12:15], v[146:149], v[230:233], v[12:15]
	v_mfma_f32_16x16x32_bf16 v[8:11], v[154:157], v[230:233], v[8:11]
	v_mfma_f32_16x16x32_bf16 v[52:55], v[158:161], v[186:189], v[52:55]
	v_mfma_f32_16x16x32_bf16 v[48:51], v[178:181], v[186:189], v[48:51]
	v_mfma_f32_16x16x32_bf16 v[36:39], v[158:161], v[210:213], v[36:39]
	v_mfma_f32_16x16x32_bf16 v[32:35], v[178:181], v[210:213], v[32:35]
	v_mfma_f32_16x16x32_bf16 v[20:23], v[158:161], v[218:221], v[20:23]
	v_mfma_f32_16x16x32_bf16 v[16:19], v[178:181], v[218:221], v[16:19]
	v_mfma_f32_16x16x32_bf16 v[4:7], v[158:161], v[226:229], v[4:7]
	v_mfma_f32_16x16x32_bf16 v[0:3], v[178:181], v[226:229], v[0:3]
	v_mfma_f32_16x16x32_bf16 v[52:55], v[174:177], v[206:209], v[52:55]
	v_mfma_f32_16x16x32_bf16 v[48:51], v[182:185], v[206:209], v[48:51]
	v_mfma_f32_16x16x32_bf16 v[36:39], v[174:177], v[214:217], v[36:39]
	v_mfma_f32_16x16x32_bf16 v[32:35], v[182:185], v[214:217], v[32:35]
	v_mfma_f32_16x16x32_bf16 v[20:23], v[174:177], v[222:225], v[20:23]
	v_mfma_f32_16x16x32_bf16 v[16:19], v[182:185], v[222:225], v[16:19]
	v_mfma_f32_16x16x32_bf16 v[4:7], v[174:177], v[230:233], v[4:7]
	v_mfma_f32_16x16x32_bf16 v[0:3], v[182:185], v[230:233], v[0:3]
	s_setprio 0
	s_barrier
	s_add_u32 s45, s45, 0x100
	s_addc_u32 s46, s46, 0
	s_add_u32 s20, s20, 0x100
	s_addc_u32 s21, s21, 0
	s_cmp_ge_i32 s47, s34
	s_mov_b32 s0, s47
	s_cbranch_scc0 .LBB0_946

; #define PG8_STAGE(bufoff, gbase, voff) do { _Pragma("unroll") for (int _i = 0; _i < 2; ++_i) \
;         __builtin_amdgcn_global_load_lds((const unsigned*)((const char*)(gbase) + (voff)[_i]), (PG8_LAS unsigned*)(lds + (bufoff) + ldsw + _i * 8192), 16, 0, 0); } while (0)
; #define PG8_LDA(dst, b, h) do { if constexpr (FP8) { _Pragma("unroll") for (int m = 0; m < 4; ++m) dst##8[m] = pg8_ld8(lds + PG8_SA(b, h) + aoff + m * 2048); } \
;         else { _Pragma("unroll") for (int m = 0; m < 4; ++m) _Pragma("unroll") for (int k = 0; k < 2; ++k) dst[m][k] = *(const PG8_LAS bf16x8*)(lds + PG8_SA(b, h) + aoff + m * 2048 + k * 1024); } } while (0)
; #define PG8_LDB(dst, b, h) do { if constexpr (FP8) { _Pragma("unroll") for (int n = 0; n < 2; ++n) dst##8[n] = pg8_ld8(lds + PG8_SB(b, h) + boff + n * 2048); } \
;         else { _Pragma("unroll") for (int n = 0; n < 2; ++n) _Pragma("unroll") for (int k = 0; k < 2; ++k) dst[n][k] = *(const PG8_LAS bf16x8*)(lds + PG8_SB(b, h) + boff + n * 2048 + k * 1024); } } while (0)
; #define PG8_WAIT_V(n) asm volatile("s_waitcnt vmcnt(" #n ")" ::: "memory")
; #define PG8_WAIT_L(n) asm volatile("s_waitcnt lgkmcnt(" #n ")" ::: "memory")
; #define PG8_BAR __builtin_amdgcn_s_barrier()
; #define PG8_SCHED __builtin_amdgcn_sched_barrier(0)
;     ...
;             const bool last = (t == nt - 2);
;             const char* a1 = cA + (size_t)(t + 1) * kstep;
;             const char* a2 = last ? nA : cA + (size_t)(t + 2) * kstep; const char* b2 = last ? nB : cB + (size_t)(t + 2) * kstep;
;             const char* a3 = a2 + kstep; const char* b3 = b2 + kstep;
;             if (last && has_next) S.a_ready(nxt);
;             if constexpr (SP2) {
;             PG8_LDB(B0, 0, 0); PG8_LDB(B1, 0, 1); PG8_SCHED; PG8_LDA(At, 0, 0); PG8_STAGE(PG8_SA(1, 1), a1 + hstep, voffA);
;             PG8_WAIT_V(8); PG8_WAIT_L(0); PG8_BAR; PG8_MMA(0, 0, At, B0); PG8_MMA(0, 1, At, B1); PG8_BAR; PG8_SCHED;
;             PG8_LDA(At, 0, 1); PG8_STAGE(PG8_SB(0, 0), b2, voffB); PG8_STAGE(PG8_SB(0, 1), b2 + hstep, voffB); PG8_STAGE(PG8_SA(0, 0), a2, voffA);
.LBB0_966:
	s_add_u32 s0, s20, 0xfffc0080
	s_addc_u32 s1, s21, -1
	s_add_i32 s43, 0, 0x10000
	s_cmp_eq_u32 s42, 12
	s_cselect_b32 s23, s13, s1
	s_cselect_b32 s22, s38, s0
	v_add_u32_e32 v145, s43, v141
	s_cselect_b32 s1, s11, s41
	s_cselect_b32 s0, s39, s40
	s_add_i32 s46, 0, 0x14000
	ds_read_b128 v[136:139], v145
	ds_read_b128 v[146:149], v145 offset:1024
	ds_read_b128 v[150:153], v145 offset:2048
	ds_read_b128 v[154:157], v145 offset:3072
	v_add_u32_e32 v145, s46, v141
	ds_read_b128 v[158:161], v145
	ds_read_b128 v[174:177], v145 offset:1024
	ds_read_b128 v[178:181], v145 offset:2048
	ds_read_b128 v[182:185], v145 offset:3072
	v_lshl_add_u64 v[190:191], s[20:21], 0, v[134:135]
	s_add_i32 m0, s19, 0xc000
	ds_read_b128 v[186:189], v144
	ds_read_b128 v[206:209], v144 offset:1024
	ds_read_b128 v[210:213], v144 offset:2048
	ds_read_b128 v[214:217], v144 offset:3072
	ds_read_b128 v[218:221], v144 offset:4096
	ds_read_b128 v[222:225], v144 offset:5120
	ds_read_b128 v[226:229], v144 offset:6144
	ds_read_b128 v[230:233], v144 offset:7168
	global_load_lds_dwordx4 v[190:191], off
	v_lshl_add_u64 v[190:191], s[20:21], 0, v[132:133]
	s_add_i32 m0, s19, 0xe000
	s_nop 0
	global_load_lds_dwordx4 v[190:191], off
	s_waitcnt vmcnt(8)
	s_waitcnt lgkmcnt(0)
	s_barrier
	s_setprio 1
	s_waitcnt lgkmcnt(0)
	v_mfma_f32_16x16x32_f16 v[126:129], v[136:139], v[186:189], v[126:129]
	v_mfma_f32_16x16x32_f16 v[122:125], v[150:153], v[186:189], v[122:125]
	v_mfma_f32_16x16x32_f16 v[110:113], v[136:139], v[210:213], v[110:113]
	v_mfma_f32_16x16x32_f16 v[106:109], v[150:153], v[210:213], v[106:109]
	v_mfma_f32_16x16x32_f16 v[94:97], v[136:139], v[218:221], v[94:97]
	v_mfma_f32_16x16x32_f16 v[90:93], v[150:153], v[218:221], v[90:93]
	v_mfma_f32_16x16x32_f16 v[76:79], v[136:139], v[226:229], v[76:79]
	v_mfma_f32_16x16x32_f16 v[72:75], v[150:153], v[226:229], v[72:75]
	v_mfma_f32_16x16x32_f16 v[126:129], v[146:149], v[206:209], v[126:129]
	v_mfma_f32_16x16x32_f16 v[122:125], v[154:157], v[206:209], v[122:125]
	v_mfma_f32_16x16x32_f16 v[110:113], v[146:149], v[214:217], v[110:113]
	v_mfma_f32_16x16x32_f16 v[106:109], v[154:157], v[214:217], v[106:109]
	v_mfma_f32_16x16x32_f16 v[94:97], v[146:149], v[222:225], v[94:97]
	v_mfma_f32_16x16x32_f16 v[90:93], v[154:157], v[222:225], v[90:93]
	v_mfma_f32_16x16x32_f16 v[76:79], v[146:149], v[230:233], v[76:79]
	v_mfma_f32_16x16x32_f16 v[72:75], v[154:157], v[230:233], v[72:75]
	v_mfma_f32_16x16x32_f16 v[118:121], v[158:161], v[186:189], v[118:121]
	v_mfma_f32_16x16x32_f16 v[114:117], v[178:181], v[186:189], v[114:117]
	v_mfma_f32_16x16x32_f16 v[102:105], v[158:161], v[210:213], v[102:105]
	v_mfma_f32_16x16x32_f16 v[98:101], v[178:181], v[210:213], v[98:101]
	v_mfma_f32_16x16x32_f16 v[86:89], v[158:161], v[218:221], v[86:89]
	v_mfma_f32_16x16x32_f16 v[82:85], v[178:181], v[218:221], v[82:85]
	v_mfma_f32_16x16x32_f16 v[68:71], v[158:161], v[226:229], v[68:71]
	v_mfma_f32_16x16x32_f16 v[64:67], v[178:181], v[226:229], v[64:67]
	v_mfma_f32_16x16x32_f16 v[118:121], v[174:177], v[206:209], v[118:121]
	v_mfma_f32_16x16x32_f16 v[114:117], v[182:185], v[206:209], v[114:117]
	v_mfma_f32_16x16x32_f16 v[102:105], v[174:177], v[214:217], v[102:105]
	v_mfma_f32_16x16x32_f16 v[98:101], v[182:185], v[214:217], v[98:101]
	v_mfma_f32_16x16x32_f16 v[86:89], v[174:177], v[222:225], v[86:89]
	v_mfma_f32_16x16x32_f16 v[82:85], v[182:185], v[222:225], v[82:85]
	v_mfma_f32_16x16x32_f16 v[68:71], v[174:177], v[230:233], v[68:71]
	v_mfma_f32_16x16x32_f16 v[64:67], v[182:185], v[230:233], v[64:67]
	s_setprio 0
	s_barrier
	s_add_i32 s43, s43, s26
	v_lshl_add_u64 v[190:191], s[0:1], 0, v[80:81]
	s_mov_b32 m0, s43
	ds_read_b128 v[186:189], v144 offset:16384
	ds_read_b128 v[206:209], v144 offset:17408
	ds_read_b128 v[210:213], v144 offset:18432
	ds_read_b128 v[214:217], v144 offset:19456
	ds_read_b128 v[218:221], v144 offset:20480
	ds_read_b128 v[222:225], v144 offset:21504
	ds_read_b128 v[226:229], v144 offset:22528
	ds_read_b128 v[230:233], v144 offset:23552
	global_load_lds_dwordx4 v[190:191], off
	s_add_i32 m0, s43, 0x2000
	s_add_u32 s44, s0, 0x40000
	v_lshl_add_u64 v[234:235], s[0:1], 0, v[130:131]
	s_addc_u32 s45, s1, 0
	s_add_i32 s43, s46, s26
	global_load_lds_dwordx4 v[234:235], off
	v_lshl_add_u64 v[236:237], s[44:45], 0, v[80:81]
	s_mov_b32 m0, s43
	v_lshl_add_u64 v[238:239], s[22:23], 0, v[130:131]
	global_load_lds_dwordx4 v[236:237], off
	v_lshl_add_u64 v[236:237], s[44:45], 0, v[130:131]
	s_add_i32 m0, s43, 0x2000
	s_nop 0
	global_load_lds_dwordx4 v[236:237], off
	v_lshl_add_u64 v[236:237], s[22:23], 0, v[80:81]
	s_mov_b32 m0, s19
	s_nop 0
	global_load_lds_dwordx4 v[236:237], off
	s_mov_b32 m0, s29
	s_nop 0
	global_load_lds_dwordx4 v[238:239], off
	s_waitcnt vmcnt(8)
	s_waitcnt lgkmcnt(0)
	s_barrier
; #define PG8_STAGE(bufoff, gbase, voff) do { _Pragma("unroll") for (int _i = 0; _i < 2; ++_i) \
;         __builtin_amdgcn_global_load_lds((const unsigned*)((const char*)(gbase) + (voff)[_i]), (PG8_LAS unsigned*)(lds + (bufoff) + ldsw + _i * 8192), 16, 0, 0); } while (0)
; #define PG8_LDA(dst, b, h) do { if constexpr (FP8) { _Pragma("unroll") for (int m = 0; m < 4; ++m) dst##8[m] = pg8_ld8(lds + PG8_SA(b, h) + aoff + m * 2048); } \
;         else { _Pragma("unroll") for (int m = 0; m < 4; ++m) _Pragma("unroll") for (int k = 0; k < 2; ++k) dst[m][k] = *(const PG8_LAS bf16x8*)(lds + PG8_SA(b, h) + aoff + m * 2048 + k * 1024); } } while (0)
; #define PG8_LDB(dst, b, h) do { if constexpr (FP8) { _Pragma("unroll") for (int n = 0; n < 2; ++n) dst##8[n] = pg8_ld8(lds + PG8_SB(b, h) + boff + n * 2048); } \
;         else { _Pragma("unroll") for (int n = 0; n < 2; ++n) _Pragma("unroll") for (int k = 0; k < 2; ++k) dst[n][k] = *(const PG8_LAS bf16x8*)(lds + PG8_SB(b, h) + boff + n * 2048 + k * 1024); } } while (0)
; #define PG8_WAIT_V(n) asm volatile("s_waitcnt vmcnt(" #n ")" ::: "memory")
; #define PG8_WAIT_L(n) asm volatile("s_waitcnt lgkmcnt(" #n ")" ::: "memory")
; #define PG8_BAR __builtin_amdgcn_s_barrier()
; #define PG8_SCHED __builtin_amdgcn_sched_barrier(0)
;     ...
;             PG8_WAIT_V(8); PG8_WAIT_L(0); PG8_BAR; PG8_MMA(0, 0, At, B0); PG8_MMA(0, 1, At, B1); PG8_BAR; PG8_SCHED;
;             PG8_LDA(At, 0, 1); PG8_STAGE(PG8_SB(0, 0), b2, voffB); PG8_STAGE(PG8_SB(0, 1), b2 + hstep, voffB); PG8_STAGE(PG8_SA(0, 0), a2, voffA);
;             PG8_WAIT_V(8); PG8_WAIT_L(0); PG8_BAR; PG8_MMA(1, 0, At, B0); PG8_MMA(1, 1, At, B1); PG8_BAR; PG8_SCHED;
;             PG8_LDB(B0, 1, 0); PG8_LDB(B1, 1, 1); PG8_SCHED; PG8_LDA(At, 1, 0); PG8_STAGE(PG8_SA(0, 1), a2 + hstep, voffA);
;             PG8_WAIT_V(8); PG8_WAIT_L(0); PG8_BAR; PG8_MMA(0, 0, At, B0); PG8_MMA(0, 1, At, B1); PG8_BAR; PG8_SCHED;
	s_setprio 1
	s_waitcnt lgkmcnt(0)
	v_mfma_f32_16x16x32_f16 v[60:63], v[136:139], v[186:189], v[60:63]
	v_mfma_f32_16x16x32_f16 v[56:59], v[150:153], v[186:189], v[56:59]
	v_mfma_f32_16x16x32_f16 v[44:47], v[136:139], v[210:213], v[44:47]
	v_mfma_f32_16x16x32_f16 v[40:43], v[150:153], v[210:213], v[40:43]
	v_mfma_f32_16x16x32_f16 v[28:31], v[136:139], v[218:221], v[28:31]
	v_mfma_f32_16x16x32_f16 v[24:27], v[150:153], v[218:221], v[24:27]
	v_mfma_f32_16x16x32_f16 v[12:15], v[136:139], v[226:229], v[12:15]
	v_mfma_f32_16x16x32_f16 v[8:11], v[150:153], v[226:229], v[8:11]
	v_mfma_f32_16x16x32_f16 v[60:63], v[146:149], v[206:209], v[60:63]
	v_mfma_f32_16x16x32_f16 v[56:59], v[154:157], v[206:209], v[56:59]
	v_mfma_f32_16x16x32_f16 v[44:47], v[146:149], v[214:217], v[44:47]
	v_mfma_f32_16x16x32_f16 v[40:43], v[154:157], v[214:217], v[40:43]
	v_mfma_f32_16x16x32_f16 v[28:31], v[146:149], v[222:225], v[28:31]
	v_mfma_f32_16x16x32_f16 v[24:27], v[154:157], v[222:225], v[24:27]
	v_mfma_f32_16x16x32_f16 v[12:15], v[146:149], v[230:233], v[12:15]
	v_mfma_f32_16x16x32_f16 v[8:11], v[154:157], v[230:233], v[8:11]
	v_mfma_f32_16x16x32_f16 v[52:55], v[158:161], v[186:189], v[52:55]
	v_mfma_f32_16x16x32_f16 v[48:51], v[178:181], v[186:189], v[48:51]
	v_mfma_f32_16x16x32_f16 v[36:39], v[158:161], v[210:213], v[36:39]
	v_mfma_f32_16x16x32_f16 v[32:35], v[178:181], v[210:213], v[32:35]
	v_mfma_f32_16x16x32_f16 v[20:23], v[158:161], v[218:221], v[20:23]
	v_mfma_f32_16x16x32_f16 v[16:19], v[178:181], v[218:221], v[16:19]
	v_mfma_f32_16x16x32_f16 v[4:7], v[158:161], v[226:229], v[4:7]
	v_mfma_f32_16x16x32_f16 v[0:3], v[178:181], v[226:229], v[0:3]
	v_mfma_f32_16x16x32_f16 v[52:55], v[174:177], v[206:209], v[52:55]
	v_mfma_f32_16x16x32_f16 v[48:51], v[182:185], v[206:209], v[48:51]
	v_mfma_f32_16x16x32_f16 v[36:39], v[174:177], v[214:217], v[36:39]
	v_mfma_f32_16x16x32_f16 v[32:35], v[182:185], v[214:217], v[32:35]
	v_mfma_f32_16x16x32_f16 v[20:23], v[174:177], v[222:225], v[20:23]
	v_mfma_f32_16x16x32_f16 v[16:19], v[182:185], v[222:225], v[16:19]
	v_mfma_f32_16x16x32_f16 v[4:7], v[174:177], v[230:233], v[4:7]
	v_mfma_f32_16x16x32_f16 v[0:3], v[182:185], v[230:233], v[0:3]
	s_setprio 0
	s_barrier
	s_add_i32 s43, 0, 0x18000
	v_add_u32_e32 v145, s43, v141
	s_add_i32 s44, 0, 0x1c000
	ds_read_b128 v[136:139], v145
	ds_read_b128 v[146:149], v145 offset:1024
	ds_read_b128 v[150:153], v145 offset:2048
	ds_read_b128 v[154:157], v145 offset:3072
	v_add_u32_e32 v145, s44, v141
	ds_read_b128 v[158:161], v145
	ds_read_b128 v[174:177], v145 offset:1024
	ds_read_b128 v[178:181], v145 offset:2048
	ds_read_b128 v[182:185], v145 offset:3072
	s_add_u32 s22, s22, 0x40000
	s_addc_u32 s23, s23, 0
	s_mov_b32 m0, s30
	v_lshl_add_u64 v[240:241], s[22:23], 0, v[80:81]
	ds_read_b128 v[186:189], v144 offset:32768
	ds_read_b128 v[206:209], v144 offset:33792
	ds_read_b128 v[210:213], v144 offset:34816
	ds_read_b128 v[214:217], v144 offset:35840
	ds_read_b128 v[218:221], v144 offset:36864
	ds_read_b128 v[222:225], v144 offset:37888
	ds_read_b128 v[226:229], v144 offset:38912
	ds_read_b128 v[230:233], v144 offset:39936
	global_load_lds_dwordx4 v[240:241], off
	v_lshl_add_u64 v[240:241], s[22:23], 0, v[130:131]
	s_mov_b32 m0, s31
	s_nop 0
	global_load_lds_dwordx4 v[240:241], off
	s_waitcnt vmcnt(8)
	s_waitcnt lgkmcnt(0)
	s_barrier
	s_setprio 1
	s_waitcnt lgkmcnt(0)
	v_mfma_f32_16x16x32_f16 v[126:129], v[136:139], v[186:189], v[126:129]
	v_mfma_f32_16x16x32_f16 v[122:125], v[150:153], v[186:189], v[122:125]
	v_mfma_f32_16x16x32_f16 v[110:113], v[136:139], v[210:213], v[110:113]
	v_mfma_f32_16x16x32_f16 v[106:109], v[150:153], v[210:213], v[106:109]
	v_mfma_f32_16x16x32_f16 v[94:97], v[136:139], v[218:221], v[94:97]
	v_mfma_f32_16x16x32_f16 v[90:93], v[150:153], v[218:221], v[90:93]
	v_mfma_f32_16x16x32_f16 v[76:79], v[136:139], v[226:229], v[76:79]
	v_mfma_f32_16x16x32_f16 v[72:75], v[150:153], v[226:229], v[72:75]
	v_mfma_f32_16x16x32_f16 v[126:129], v[146:149], v[206:209], v[126:129]
	v_mfma_f32_16x16x32_f16 v[122:125], v[154:157], v[206:209], v[122:125]
	v_mfma_f32_16x16x32_f16 v[110:113], v[146:149], v[214:217], v[110:113]
	v_mfma_f32_16x16x32_f16 v[106:109], v[154:157], v[214:217], v[106:109]
	v_mfma_f32_16x16x32_f16 v[94:97], v[146:149], v[222:225], v[94:97]
	v_mfma_f32_16x16x32_f16 v[90:93], v[154:157], v[222:225], v[90:93]
	v_mfma_f32_16x16x32_f16 v[76:79], v[146:149], v[230:233], v[76:79]
	v_mfma_f32_16x16x32_f16 v[72:75], v[154:157], v[230:233], v[72:75]
	v_mfma_f32_16x16x32_f16 v[118:121], v[158:161], v[186:189], v[118:121]
	v_mfma_f32_16x16x32_f16 v[114:117], v[178:181], v[186:189], v[114:117]
	v_mfma_f32_16x16x32_f16 v[102:105], v[158:161], v[210:213], v[102:105]
	v_mfma_f32_16x16x32_f16 v[98:101], v[178:181], v[210:213], v[98:101]
	v_mfma_f32_16x16x32_f16 v[86:89], v[158:161], v[218:221], v[86:89]
	v_mfma_f32_16x16x32_f16 v[82:85], v[178:181], v[218:221], v[82:85]
	v_mfma_f32_16x16x32_f16 v[68:71], v[158:161], v[226:229], v[68:71]
	v_mfma_f32_16x16x32_f16 v[64:67], v[178:181], v[226:229], v[64:67]
	v_mfma_f32_16x16x32_f16 v[118:121], v[174:177], v[206:209], v[118:121]
	v_mfma_f32_16x16x32_f16 v[114:117], v[182:185], v[206:209], v[114:117]
	v_mfma_f32_16x16x32_f16 v[102:105], v[174:177], v[214:217], v[102:105]
	v_mfma_f32_16x16x32_f16 v[98:101], v[182:185], v[214:217], v[98:101]
	v_mfma_f32_16x16x32_f16 v[86:89], v[174:177], v[222:225], v[86:89]
	v_mfma_f32_16x16x32_f16 v[82:85], v[182:185], v[222:225], v[82:85]
	v_mfma_f32_16x16x32_f16 v[68:71], v[174:177], v[230:233], v[68:71]
	v_mfma_f32_16x16x32_f16 v[64:67], v[182:185], v[230:233], v[64:67]
	s_setprio 0
	s_barrier
; #define PG8_STAGE(bufoff, gbase, voff) do { _Pragma("unroll") for (int _i = 0; _i < 2; ++_i) \
;         __builtin_amdgcn_global_load_lds((const unsigned*)((const char*)(gbase) + (voff)[_i]), (PG8_LAS unsigned*)(lds + (bufoff) + ldsw + _i * 8192), 16, 0, 0); } while (0)
; #define PG8_LDA(dst, b, h) do { if constexpr (FP8) { _Pragma("unroll") for (int m = 0; m < 4; ++m) dst##8[m] = pg8_ld8(lds + PG8_SA(b, h) + aoff + m * 2048); } \
;         else { _Pragma("unroll") for (int m = 0; m < 4; ++m) _Pragma("unroll") for (int k = 0; k < 2; ++k) dst[m][k] = *(const PG8_LAS bf16x8*)(lds + PG8_SA(b, h) + aoff + m * 2048 + k * 1024); } } while (0)
; #define PG8_WAIT_V(n) asm volatile("s_waitcnt vmcnt(" #n ")" ::: "memory")
; #define PG8_WAIT_L(n) asm volatile("s_waitcnt lgkmcnt(" #n ")" ::: "memory")
; #define PG8_BAR __builtin_amdgcn_s_barrier()
; #define PG8_SCHED __builtin_amdgcn_sched_barrier(0)
;     ...
;             PG8_LDA(At, 1, 1); PG8_STAGE(PG8_SB(1, 0), b3, voffB); PG8_STAGE(PG8_SB(1, 1), b3 + hstep, voffB); PG8_STAGE(PG8_SA(1, 0), a3, voffA);
;             PG8_WAIT_V(8); PG8_WAIT_L(0); PG8_BAR; PG8_MMA(1, 0, At, B0); PG8_MMA(1, 1, At, B1); PG8_BAR; PG8_SCHED;
;     ...
;         if constexpr (ALIGN_EPI) { if (wr == 0) PG8_BAR; }
	s_add_i32 s22, s43, s26
	v_lshl_add_u64 v[190:191], v[190:191], 0, s[86:87]
	s_mov_b32 m0, s22
	ds_read_b128 v[186:189], v144 offset:49152
	ds_read_b128 v[206:209], v144 offset:50176
	ds_read_b128 v[210:213], v144 offset:51200
	ds_read_b128 v[214:217], v144 offset:52224
	ds_read_b128 v[218:221], v144 offset:53248
	ds_read_b128 v[222:225], v144 offset:54272
	ds_read_b128 v[226:229], v144 offset:55296
	ds_read_b128 v[230:233], v144 offset:56320
	global_load_lds_dwordx4 v[190:191], off
	s_add_i32 m0, s22, 0x2000
	s_add_u32 s0, s0, 0x40080
	v_lshl_add_u64 v[190:191], v[234:235], 0, s[86:87]
	s_addc_u32 s1, s1, 0
	s_add_i32 s22, s44, s26
	global_load_lds_dwordx4 v[190:191], off
	v_lshl_add_u64 v[190:191], s[0:1], 0, v[80:81]
	s_mov_b32 m0, s22
	s_nop 0
	global_load_lds_dwordx4 v[190:191], off
	v_lshl_add_u64 v[190:191], s[0:1], 0, v[130:131]
	s_add_i32 m0, s22, 0x2000
	s_nop 0
	global_load_lds_dwordx4 v[190:191], off
	v_lshl_add_u64 v[190:191], v[236:237], 0, s[86:87]
	s_mov_b32 m0, s34
	s_nop 0
	global_load_lds_dwordx4 v[190:191], off
	v_lshl_add_u64 v[190:191], v[238:239], 0, s[86:87]
	s_mov_b32 m0, s35
	s_nop 0
	global_load_lds_dwordx4 v[190:191], off
	s_waitcnt vmcnt(8)
	s_waitcnt lgkmcnt(0)
	s_barrier
	s_setprio 1
	s_waitcnt lgkmcnt(0)
	v_mfma_f32_16x16x32_f16 v[60:63], v[136:139], v[186:189], v[60:63]
	v_mfma_f32_16x16x32_f16 v[56:59], v[150:153], v[186:189], v[56:59]
	v_mfma_f32_16x16x32_f16 v[44:47], v[136:139], v[210:213], v[44:47]
	v_mfma_f32_16x16x32_f16 v[40:43], v[150:153], v[210:213], v[40:43]
	v_mfma_f32_16x16x32_f16 v[28:31], v[136:139], v[218:221], v[28:31]
	v_mfma_f32_16x16x32_f16 v[24:27], v[150:153], v[218:221], v[24:27]
	v_mfma_f32_16x16x32_f16 v[12:15], v[136:139], v[226:229], v[12:15]
	v_mfma_f32_16x16x32_f16 v[8:11], v[150:153], v[226:229], v[8:11]
	v_mfma_f32_16x16x32_f16 v[60:63], v[146:149], v[206:209], v[60:63]
	v_mfma_f32_16x16x32_f16 v[56:59], v[154:157], v[206:209], v[56:59]
	v_mfma_f32_16x16x32_f16 v[44:47], v[146:149], v[214:217], v[44:47]
	v_mfma_f32_16x16x32_f16 v[40:43], v[154:157], v[214:217], v[40:43]
	v_mfma_f32_16x16x32_f16 v[28:31], v[146:149], v[222:225], v[28:31]
	v_mfma_f32_16x16x32_f16 v[24:27], v[154:157], v[222:225], v[24:27]
	v_mfma_f32_16x16x32_f16 v[12:15], v[146:149], v[230:233], v[12:15]
	v_mfma_f32_16x16x32_f16 v[8:11], v[154:157], v[230:233], v[8:11]
	v_mfma_f32_16x16x32_f16 v[52:55], v[158:161], v[186:189], v[52:55]
	v_mfma_f32_16x16x32_f16 v[48:51], v[178:181], v[186:189], v[48:51]
	v_mfma_f32_16x16x32_f16 v[36:39], v[158:161], v[210:213], v[36:39]
	v_mfma_f32_16x16x32_f16 v[32:35], v[178:181], v[210:213], v[32:35]
	v_mfma_f32_16x16x32_f16 v[20:23], v[158:161], v[218:221], v[20:23]
	v_mfma_f32_16x16x32_f16 v[16:19], v[178:181], v[218:221], v[16:19]
	v_mfma_f32_16x16x32_f16 v[4:7], v[158:161], v[226:229], v[4:7]
	v_mfma_f32_16x16x32_f16 v[0:3], v[178:181], v[226:229], v[0:3]
	v_mfma_f32_16x16x32_f16 v[52:55], v[174:177], v[206:209], v[52:55]
	v_mfma_f32_16x16x32_f16 v[48:51], v[182:185], v[206:209], v[48:51]
	v_mfma_f32_16x16x32_f16 v[36:39], v[174:177], v[214:217], v[36:39]
	v_mfma_f32_16x16x32_f16 v[32:35], v[182:185], v[214:217], v[32:35]
	v_mfma_f32_16x16x32_f16 v[20:23], v[174:177], v[222:225], v[20:23]
	v_mfma_f32_16x16x32_f16 v[16:19], v[182:185], v[222:225], v[16:19]
	v_mfma_f32_16x16x32_f16 v[4:7], v[174:177], v[230:233], v[4:7]
	v_mfma_f32_16x16x32_f16 v[0:3], v[182:185], v[230:233], v[0:3]
	s_setprio 0
	s_barrier
	s_add_i32 s42, s42, 2
	s_add_u32 s40, s40, 0x100
	s_addc_u32 s41, s41, 0
	s_add_u32 s20, s20, 0x100
	s_addc_u32 s21, s21, 0
	s_cmp_gt_u32 s42, 13
	s_cbranch_scc0 .LBB0_966
	s_and_b64 vcc, exec, s[8:9]
	s_cbranch_vccz .LBB0_969
	s_barrier

; #define PG8_STAGE(bufoff, gbase, voff) do { _Pragma("unroll") for (int _i = 0; _i < 2; ++_i) \
;         __builtin_amdgcn_global_load_lds((const unsigned*)((const char*)(gbase) + (voff)[_i]), (PG8_LAS unsigned*)(lds + (bufoff) + ldsw + _i * 8192), 16, 0, 0); } while (0)
; #define PG8_LDA(dst, b, h) do { if constexpr (FP8) { _Pragma("unroll") for (int m = 0; m < 4; ++m) dst##8[m] = pg8_ld8(lds + PG8_SA(b, h) + aoff + m * 2048); } \
;         else { _Pragma("unroll") for (int m = 0; m < 4; ++m) _Pragma("unroll") for (int k = 0; k < 2; ++k) dst[m][k] = *(const PG8_LAS bf16x8*)(lds + PG8_SA(b, h) + aoff + m * 2048 + k * 1024); } } while (0)
; #define PG8_LDB(dst, b, h) do { if constexpr (FP8) { _Pragma("unroll") for (int n = 0; n < 2; ++n) dst##8[n] = pg8_ld8(lds + PG8_SB(b, h) + boff + n * 2048); } \
;         else { _Pragma("unroll") for (int n = 0; n < 2; ++n) _Pragma("unroll") for (int k = 0; k < 2; ++k) dst[n][k] = *(const PG8_LAS bf16x8*)(lds + PG8_SB(b, h) + boff + n * 2048 + k * 1024); } } while (0)
; #define PG8_WAIT_V(n) asm volatile("s_waitcnt vmcnt(" #n ")" ::: "memory")
; #define PG8_WAIT_L(n) asm volatile("s_waitcnt lgkmcnt(" #n ")" ::: "memory")
; #define PG8_BAR __builtin_amdgcn_s_barrier()
; #define PG8_SCHED __builtin_amdgcn_sched_barrier(0)
;     ...
;             const bool last = (t == nt - 2);
;             const char* a1 = cA + (size_t)(t + 1) * kstep;
;             const char* a2 = last ? nA : cA + (size_t)(t + 2) * kstep; const char* b2 = last ? nB : cB + (size_t)(t + 2) * kstep;
;             const char* a3 = a2 + kstep; const char* b3 = b2 + kstep;
;             if (last && has_next) S.a_ready(nxt);
;             if constexpr (SP2) {
;             PG8_LDB(B0, 0, 0); PG8_LDB(B1, 0, 1); PG8_SCHED; PG8_LDA(At, 0, 0); PG8_STAGE(PG8_SA(1, 1), a1 + hstep, voffA);
;             PG8_WAIT_V(8); PG8_WAIT_L(0); PG8_BAR; PG8_MMA(0, 0, At, B0); PG8_MMA(0, 1, At, B1); PG8_BAR; PG8_SCHED;
;             PG8_LDA(At, 0, 1); PG8_STAGE(PG8_SB(0, 0), b2, voffB); PG8_STAGE(PG8_SB(0, 1), b2 + hstep, voffB); PG8_STAGE(PG8_SA(0, 0), a2, voffA);
.LBB0_1050:
	s_add_i32 s22, s0, 2
	s_add_u32 s23, s20, 0x80
	s_addc_u32 s1, s21, 0
	s_add_i32 s52, 0, 0x10000
	s_cmp_eq_u32 s44, s0
	s_cselect_b32 s1, s17, s1
	s_cselect_b32 s0, s16, s23
	s_cselect_b32 s51, s19, s49
	s_cselect_b32 s50, s18, s48
	s_add_i32 s23, 0, 0x14000
	v_add_u32_e32 v154, s52, v140
	v_add_u32_e32 v170, s23, v140
	ds_read_b128 v[142:145], v154
	ds_read_b128 v[146:149], v154 offset:1024
	ds_read_b128 v[150:153], v154 offset:2048
	ds_read_b128 v[154:157], v154 offset:3072
	ds_read_b128 v[158:161], v170
	ds_read_b128 v[174:177], v170 offset:1024
	ds_read_b128 v[178:181], v170 offset:2048
	ds_read_b128 v[182:185], v170 offset:3072
	v_lshl_add_u64 v[190:191], s[20:21], 0, v[138:139]
	s_add_i32 m0, s30, 0xc000
	ds_read_b128 v[186:189], v141
	ds_read_b128 v[206:209], v141 offset:1024
	ds_read_b128 v[210:213], v141 offset:2048
	ds_read_b128 v[214:217], v141 offset:3072
	ds_read_b128 v[218:221], v141 offset:4096
	ds_read_b128 v[222:225], v141 offset:5120
	ds_read_b128 v[226:229], v141 offset:6144
	ds_read_b128 v[230:233], v141 offset:7168
	global_load_lds_dwordx4 v[190:191], off
	v_lshl_add_u64 v[190:191], s[20:21], 0, v[136:137]
	s_add_i32 m0, s30, 0xe000
	s_nop 0
	global_load_lds_dwordx4 v[190:191], off
	s_waitcnt vmcnt(8)
	s_waitcnt lgkmcnt(0)
	s_barrier
	s_setprio 1
	s_waitcnt lgkmcnt(0)
	v_mfma_f32_16x16x32_bf16 v[122:125], v[142:145], v[186:189], v[122:125]
	v_mfma_f32_16x16x32_bf16 v[126:129], v[150:153], v[186:189], v[126:129]
	v_mfma_f32_16x16x32_bf16 v[110:113], v[142:145], v[210:213], v[110:113]
	v_mfma_f32_16x16x32_bf16 v[106:109], v[150:153], v[210:213], v[106:109]
	v_mfma_f32_16x16x32_bf16 v[94:97], v[142:145], v[218:221], v[94:97]
	v_mfma_f32_16x16x32_bf16 v[90:93], v[150:153], v[218:221], v[90:93]
	v_mfma_f32_16x16x32_bf16 v[76:79], v[142:145], v[226:229], v[76:79]
	v_mfma_f32_16x16x32_bf16 v[72:75], v[150:153], v[226:229], v[72:75]
	v_mfma_f32_16x16x32_bf16 v[122:125], v[146:149], v[206:209], v[122:125]
	v_mfma_f32_16x16x32_bf16 v[126:129], v[154:157], v[206:209], v[126:129]
	v_mfma_f32_16x16x32_bf16 v[110:113], v[146:149], v[214:217], v[110:113]
	v_mfma_f32_16x16x32_bf16 v[106:109], v[154:157], v[214:217], v[106:109]
	v_mfma_f32_16x16x32_bf16 v[94:97], v[146:149], v[222:225], v[94:97]
	v_mfma_f32_16x16x32_bf16 v[90:93], v[154:157], v[222:225], v[90:93]
	v_mfma_f32_16x16x32_bf16 v[76:79], v[146:149], v[230:233], v[76:79]
	v_mfma_f32_16x16x32_bf16 v[72:75], v[154:157], v[230:233], v[72:75]
	v_mfma_f32_16x16x32_bf16 v[118:121], v[158:161], v[186:189], v[118:121]
	v_mfma_f32_16x16x32_bf16 v[114:117], v[178:181], v[186:189], v[114:117]
	v_mfma_f32_16x16x32_bf16 v[102:105], v[158:161], v[210:213], v[102:105]
	v_mfma_f32_16x16x32_bf16 v[98:101], v[178:181], v[210:213], v[98:101]
	v_mfma_f32_16x16x32_bf16 v[86:89], v[158:161], v[218:221], v[86:89]
	v_mfma_f32_16x16x32_bf16 v[82:85], v[178:181], v[218:221], v[82:85]
	v_mfma_f32_16x16x32_bf16 v[68:71], v[158:161], v[226:229], v[68:71]
	v_mfma_f32_16x16x32_bf16 v[64:67], v[178:181], v[226:229], v[64:67]
	v_mfma_f32_16x16x32_bf16 v[118:121], v[174:177], v[206:209], v[118:121]
	v_mfma_f32_16x16x32_bf16 v[114:117], v[182:185], v[206:209], v[114:117]
	v_mfma_f32_16x16x32_bf16 v[102:105], v[174:177], v[214:217], v[102:105]
	v_mfma_f32_16x16x32_bf16 v[98:101], v[182:185], v[214:217], v[98:101]
	v_mfma_f32_16x16x32_bf16 v[86:89], v[174:177], v[222:225], v[86:89]
	v_mfma_f32_16x16x32_bf16 v[82:85], v[182:185], v[222:225], v[82:85]
	v_mfma_f32_16x16x32_bf16 v[68:71], v[174:177], v[230:233], v[68:71]
	v_mfma_f32_16x16x32_bf16 v[64:67], v[182:185], v[230:233], v[64:67]
	s_setprio 0
	s_barrier
	s_add_i32 s52, s52, s29
	v_lshl_add_u64 v[190:191], s[50:51], 0, v[80:81]
	s_mov_b32 m0, s52
	ds_read_b128 v[186:189], v141 offset:16384
	ds_read_b128 v[206:209], v141 offset:17408
	ds_read_b128 v[210:213], v141 offset:18432
	ds_read_b128 v[214:217], v141 offset:19456
	ds_read_b128 v[218:221], v141 offset:20480
	ds_read_b128 v[222:225], v141 offset:21504
	ds_read_b128 v[226:229], v141 offset:22528
	ds_read_b128 v[230:233], v141 offset:23552
	global_load_lds_dwordx4 v[190:191], off
	s_add_i32 m0, s52, 0x2000
	v_lshl_add_u64 v[234:235], s[50:51], 0, v[130:131]
	s_add_u32 s50, s50, s6
	s_addc_u32 s51, s51, s7
	s_add_i32 s23, s23, s29
	global_load_lds_dwordx4 v[234:235], off
	v_lshl_add_u64 v[236:237], s[50:51], 0, v[80:81]
	s_mov_b32 m0, s23
	v_lshl_add_u64 v[238:239], s[50:51], 0, v[130:131]
	global_load_lds_dwordx4 v[236:237], off
	s_add_i32 m0, s23, 0x2000
	v_lshl_add_u64 v[240:241], s[0:1], 0, v[134:135]
	global_load_lds_dwordx4 v[238:239], off
	s_mov_b32 m0, s30
	v_lshl_add_u64 v[242:243], s[0:1], 0, v[132:133]
	global_load_lds_dwordx4 v[240:241], off
	s_mov_b32 m0, s31
	s_nop 0
	global_load_lds_dwordx4 v[242:243], off
	s_waitcnt vmcnt(8)
	s_waitcnt lgkmcnt(0)
	s_barrier
; #define PG8_STAGE(bufoff, gbase, voff) do { _Pragma("unroll") for (int _i = 0; _i < 2; ++_i) \
;         __builtin_amdgcn_global_load_lds((const unsigned*)((const char*)(gbase) + (voff)[_i]), (PG8_LAS unsigned*)(lds + (bufoff) + ldsw + _i * 8192), 16, 0, 0); } while (0)
; #define PG8_LDA(dst, b, h) do { if constexpr (FP8) { _Pragma("unroll") for (int m = 0; m < 4; ++m) dst##8[m] = pg8_ld8(lds + PG8_SA(b, h) + aoff + m * 2048); } \
;         else { _Pragma("unroll") for (int m = 0; m < 4; ++m) _Pragma("unroll") for (int k = 0; k < 2; ++k) dst[m][k] = *(const PG8_LAS bf16x8*)(lds + PG8_SA(b, h) + aoff + m * 2048 + k * 1024); } } while (0)
; #define PG8_LDB(dst, b, h) do { if constexpr (FP8) { _Pragma("unroll") for (int n = 0; n < 2; ++n) dst##8[n] = pg8_ld8(lds + PG8_SB(b, h) + boff + n * 2048); } \
;         else { _Pragma("unroll") for (int n = 0; n < 2; ++n) _Pragma("unroll") for (int k = 0; k < 2; ++k) dst[n][k] = *(const PG8_LAS bf16x8*)(lds + PG8_SB(b, h) + boff + n * 2048 + k * 1024); } } while (0)
; #define PG8_WAIT_V(n) asm volatile("s_waitcnt vmcnt(" #n ")" ::: "memory")
; #define PG8_WAIT_L(n) asm volatile("s_waitcnt lgkmcnt(" #n ")" ::: "memory")
; #define PG8_BAR __builtin_amdgcn_s_barrier()
; #define PG8_SCHED __builtin_amdgcn_sched_barrier(0)
;     ...
;             PG8_WAIT_V(8); PG8_WAIT_L(0); PG8_BAR; PG8_MMA(0, 0, At, B0); PG8_MMA(0, 1, At, B1); PG8_BAR; PG8_SCHED;
;             PG8_LDA(At, 0, 1); PG8_STAGE(PG8_SB(0, 0), b2, voffB); PG8_STAGE(PG8_SB(0, 1), b2 + hstep, voffB); PG8_STAGE(PG8_SA(0, 0), a2, voffA);
;             PG8_WAIT_V(8); PG8_WAIT_L(0); PG8_BAR; PG8_MMA(1, 0, At, B0); PG8_MMA(1, 1, At, B1); PG8_BAR; PG8_SCHED;
;             PG8_LDB(B0, 1, 0); PG8_LDB(B1, 1, 1); PG8_SCHED; PG8_LDA(At, 1, 0); PG8_STAGE(PG8_SA(0, 1), a2 + hstep, voffA);
;             PG8_WAIT_V(8); PG8_WAIT_L(0); PG8_BAR; PG8_MMA(0, 0, At, B0); PG8_MMA(0, 1, At, B1); PG8_BAR; PG8_SCHED;
	s_setprio 1
	s_waitcnt lgkmcnt(0)
	v_mfma_f32_16x16x32_bf16 v[60:63], v[142:145], v[186:189], v[60:63]
	v_mfma_f32_16x16x32_bf16 v[56:59], v[150:153], v[186:189], v[56:59]
	v_mfma_f32_16x16x32_bf16 v[44:47], v[142:145], v[210:213], v[44:47]
	v_mfma_f32_16x16x32_bf16 v[40:43], v[150:153], v[210:213], v[40:43]
	v_mfma_f32_16x16x32_bf16 v[28:31], v[142:145], v[218:221], v[28:31]
	v_mfma_f32_16x16x32_bf16 v[24:27], v[150:153], v[218:221], v[24:27]
	v_mfma_f32_16x16x32_bf16 v[12:15], v[142:145], v[226:229], v[12:15]
	v_mfma_f32_16x16x32_bf16 v[8:11], v[150:153], v[226:229], v[8:11]
	v_mfma_f32_16x16x32_bf16 v[60:63], v[146:149], v[206:209], v[60:63]
	v_mfma_f32_16x16x32_bf16 v[56:59], v[154:157], v[206:209], v[56:59]
	v_mfma_f32_16x16x32_bf16 v[44:47], v[146:149], v[214:217], v[44:47]
	v_mfma_f32_16x16x32_bf16 v[40:43], v[154:157], v[214:217], v[40:43]
	v_mfma_f32_16x16x32_bf16 v[28:31], v[146:149], v[222:225], v[28:31]
	v_mfma_f32_16x16x32_bf16 v[24:27], v[154:157], v[222:225], v[24:27]
	v_mfma_f32_16x16x32_bf16 v[12:15], v[146:149], v[230:233], v[12:15]
	v_mfma_f32_16x16x32_bf16 v[8:11], v[154:157], v[230:233], v[8:11]
	v_mfma_f32_16x16x32_bf16 v[52:55], v[158:161], v[186:189], v[52:55]
	v_mfma_f32_16x16x32_bf16 v[48:51], v[178:181], v[186:189], v[48:51]
	v_mfma_f32_16x16x32_bf16 v[36:39], v[158:161], v[210:213], v[36:39]
	v_mfma_f32_16x16x32_bf16 v[32:35], v[178:181], v[210:213], v[32:35]
	v_mfma_f32_16x16x32_bf16 v[20:23], v[158:161], v[218:221], v[20:23]
	v_mfma_f32_16x16x32_bf16 v[16:19], v[178:181], v[218:221], v[16:19]
	v_mfma_f32_16x16x32_bf16 v[4:7], v[158:161], v[226:229], v[4:7]
	v_mfma_f32_16x16x32_bf16 v[0:3], v[178:181], v[226:229], v[0:3]
	v_mfma_f32_16x16x32_bf16 v[52:55], v[174:177], v[206:209], v[52:55]
	v_mfma_f32_16x16x32_bf16 v[48:51], v[182:185], v[206:209], v[48:51]
	v_mfma_f32_16x16x32_bf16 v[36:39], v[174:177], v[214:217], v[36:39]
	v_mfma_f32_16x16x32_bf16 v[32:35], v[182:185], v[214:217], v[32:35]
	v_mfma_f32_16x16x32_bf16 v[20:23], v[174:177], v[222:225], v[20:23]
	v_mfma_f32_16x16x32_bf16 v[16:19], v[182:185], v[222:225], v[16:19]
	v_mfma_f32_16x16x32_bf16 v[4:7], v[174:177], v[230:233], v[4:7]
	v_mfma_f32_16x16x32_bf16 v[0:3], v[182:185], v[230:233], v[0:3]
	s_setprio 0
	s_barrier
	s_add_i32 s23, 0, 0x18000
	s_add_i32 s50, 0, 0x1c000
	v_add_u32_e32 v154, s23, v140
	v_add_u32_e32 v170, s50, v140
	ds_read_b128 v[142:145], v154
	ds_read_b128 v[146:149], v154 offset:1024
	ds_read_b128 v[150:153], v154 offset:2048
	ds_read_b128 v[154:157], v154 offset:3072
	ds_read_b128 v[158:161], v170
	ds_read_b128 v[174:177], v170 offset:1024
	ds_read_b128 v[178:181], v170 offset:2048
	ds_read_b128 v[182:185], v170 offset:3072
	s_add_u32 s0, s0, s6
	s_addc_u32 s1, s1, s7
	s_mov_b32 m0, s34
	v_lshl_add_u64 v[244:245], s[0:1], 0, v[134:135]
	ds_read_b128 v[186:189], v141 offset:32768
	ds_read_b128 v[206:209], v141 offset:33792
	ds_read_b128 v[210:213], v141 offset:34816
	ds_read_b128 v[214:217], v141 offset:35840
	ds_read_b128 v[218:221], v141 offset:36864
	ds_read_b128 v[222:225], v141 offset:37888
	ds_read_b128 v[226:229], v141 offset:38912
	ds_read_b128 v[230:233], v141 offset:39936
	global_load_lds_dwordx4 v[244:245], off
	v_lshl_add_u64 v[244:245], s[0:1], 0, v[132:133]
	s_mov_b32 m0, s35
	s_nop 0
	global_load_lds_dwordx4 v[244:245], off
	s_waitcnt vmcnt(8)
	s_waitcnt lgkmcnt(0)
	s_barrier
	s_setprio 1
	s_waitcnt lgkmcnt(0)
	v_mfma_f32_16x16x32_bf16 v[122:125], v[142:145], v[186:189], v[122:125]
	v_mfma_f32_16x16x32_bf16 v[126:129], v[150:153], v[186:189], v[126:129]
	v_mfma_f32_16x16x32_bf16 v[110:113], v[142:145], v[210:213], v[110:113]
	v_mfma_f32_16x16x32_bf16 v[106:109], v[150:153], v[210:213], v[106:109]
	v_mfma_f32_16x16x32_bf16 v[94:97], v[142:145], v[218:221], v[94:97]
	v_mfma_f32_16x16x32_bf16 v[90:93], v[150:153], v[218:221], v[90:93]
	v_mfma_f32_16x16x32_bf16 v[76:79], v[142:145], v[226:229], v[76:79]
	v_mfma_f32_16x16x32_bf16 v[72:75], v[150:153], v[226:229], v[72:75]
	v_mfma_f32_16x16x32_bf16 v[122:125], v[146:149], v[206:209], v[122:125]
	v_mfma_f32_16x16x32_bf16 v[126:129], v[154:157], v[206:209], v[126:129]
	v_mfma_f32_16x16x32_bf16 v[110:113], v[146:149], v[214:217], v[110:113]
	v_mfma_f32_16x16x32_bf16 v[106:109], v[154:157], v[214:217], v[106:109]
	v_mfma_f32_16x16x32_bf16 v[94:97], v[146:149], v[222:225], v[94:97]
	v_mfma_f32_16x16x32_bf16 v[90:93], v[154:157], v[222:225], v[90:93]
	v_mfma_f32_16x16x32_bf16 v[76:79], v[146:149], v[230:233], v[76:79]
	v_mfma_f32_16x16x32_bf16 v[72:75], v[154:157], v[230:233], v[72:75]
	v_mfma_f32_16x16x32_bf16 v[118:121], v[158:161], v[186:189], v[118:121]
	v_mfma_f32_16x16x32_bf16 v[114:117], v[178:181], v[186:189], v[114:117]
	v_mfma_f32_16x16x32_bf16 v[102:105], v[158:161], v[210:213], v[102:105]
	v_mfma_f32_16x16x32_bf16 v[98:101], v[178:181], v[210:213], v[98:101]
	v_mfma_f32_16x16x32_bf16 v[86:89], v[158:161], v[218:221], v[86:89]
	v_mfma_f32_16x16x32_bf16 v[82:85], v[178:181], v[218:221], v[82:85]
	v_mfma_f32_16x16x32_bf16 v[68:71], v[158:161], v[226:229], v[68:71]
	v_mfma_f32_16x16x32_bf16 v[64:67], v[178:181], v[226:229], v[64:67]
	v_mfma_f32_16x16x32_bf16 v[118:121], v[174:177], v[206:209], v[118:121]
	v_mfma_f32_16x16x32_bf16 v[114:117], v[182:185], v[206:209], v[114:117]
	v_mfma_f32_16x16x32_bf16 v[102:105], v[174:177], v[214:217], v[102:105]
	v_mfma_f32_16x16x32_bf16 v[98:101], v[182:185], v[214:217], v[98:101]
	v_mfma_f32_16x16x32_bf16 v[86:89], v[174:177], v[222:225], v[86:89]
	v_mfma_f32_16x16x32_bf16 v[82:85], v[182:185], v[222:225], v[82:85]
	v_mfma_f32_16x16x32_bf16 v[68:71], v[174:177], v[230:233], v[68:71]
	v_mfma_f32_16x16x32_bf16 v[64:67], v[182:185], v[230:233], v[64:67]
	s_setprio 0
	s_barrier
; #define PG8_STAGE(bufoff, gbase, voff) do { _Pragma("unroll") for (int _i = 0; _i < 2; ++_i) \
;         __builtin_amdgcn_global_load_lds((const unsigned*)((const char*)(gbase) + (voff)[_i]), (PG8_LAS unsigned*)(lds + (bufoff) + ldsw + _i * 8192), 16, 0, 0); } while (0)
; #define PG8_LDA(dst, b, h) do { if constexpr (FP8) { _Pragma("unroll") for (int m = 0; m < 4; ++m) dst##8[m] = pg8_ld8(lds + PG8_SA(b, h) + aoff + m * 2048); } \
;         else { _Pragma("unroll") for (int m = 0; m < 4; ++m) _Pragma("unroll") for (int k = 0; k < 2; ++k) dst[m][k] = *(const PG8_LAS bf16x8*)(lds + PG8_SA(b, h) + aoff + m * 2048 + k * 1024); } } while (0)
; #define PG8_WAIT_V(n) asm volatile("s_waitcnt vmcnt(" #n ")" ::: "memory")
; #define PG8_WAIT_L(n) asm volatile("s_waitcnt lgkmcnt(" #n ")" ::: "memory")
; #define PG8_BAR __builtin_amdgcn_s_barrier()
; #define PG8_SCHED __builtin_amdgcn_sched_barrier(0)
;     ...
;         for (int t = 0; t < nt; t += 2) {
;     ...
;             PG8_LDA(At, 1, 1); PG8_STAGE(PG8_SB(1, 0), b3, voffB); PG8_STAGE(PG8_SB(1, 1), b3 + hstep, voffB); PG8_STAGE(PG8_SA(1, 0), a3, voffA);
;             PG8_WAIT_V(8); PG8_WAIT_L(0); PG8_BAR; PG8_MMA(1, 0, At, B0); PG8_MMA(1, 1, At, B1); PG8_BAR; PG8_SCHED;
	s_add_i32 s0, s23, s29
	v_lshl_add_u64 v[190:191], v[190:191], 0, s[86:87]
	s_mov_b32 m0, s0
	ds_read_b128 v[186:189], v141 offset:49152
	ds_read_b128 v[206:209], v141 offset:50176
	ds_read_b128 v[210:213], v141 offset:51200
	ds_read_b128 v[214:217], v141 offset:52224
	ds_read_b128 v[218:221], v141 offset:53248
	ds_read_b128 v[222:225], v141 offset:54272
	ds_read_b128 v[226:229], v141 offset:55296
	ds_read_b128 v[230:233], v141 offset:56320
	global_load_lds_dwordx4 v[190:191], off
	v_lshl_add_u64 v[190:191], v[234:235], 0, s[86:87]
	s_add_i32 m0, s0, 0x2000
	s_add_i32 s0, s50, s29
	global_load_lds_dwordx4 v[190:191], off
	v_lshl_add_u64 v[190:191], v[236:237], 0, s[86:87]
	s_mov_b32 m0, s0
	s_nop 0
	global_load_lds_dwordx4 v[190:191], off
	v_lshl_add_u64 v[190:191], v[238:239], 0, s[86:87]
	s_add_i32 m0, s0, 0x2000
	s_nop 0
	global_load_lds_dwordx4 v[190:191], off
	v_lshl_add_u64 v[190:191], v[240:241], 0, s[86:87]
	s_mov_b32 m0, s42
	s_nop 0
	global_load_lds_dwordx4 v[190:191], off
	v_lshl_add_u64 v[190:191], v[242:243], 0, s[86:87]
	s_mov_b32 m0, s43
	s_nop 0
	global_load_lds_dwordx4 v[190:191], off
	s_waitcnt vmcnt(8)
	s_waitcnt lgkmcnt(0)
	s_barrier
	s_setprio 1
	s_waitcnt lgkmcnt(0)
	v_mfma_f32_16x16x32_bf16 v[60:63], v[142:145], v[186:189], v[60:63]
	v_mfma_f32_16x16x32_bf16 v[56:59], v[150:153], v[186:189], v[56:59]
	v_mfma_f32_16x16x32_bf16 v[44:47], v[142:145], v[210:213], v[44:47]
	v_mfma_f32_16x16x32_bf16 v[40:43], v[150:153], v[210:213], v[40:43]
	v_mfma_f32_16x16x32_bf16 v[28:31], v[142:145], v[218:221], v[28:31]
	v_mfma_f32_16x16x32_bf16 v[24:27], v[150:153], v[218:221], v[24:27]
	v_mfma_f32_16x16x32_bf16 v[12:15], v[142:145], v[226:229], v[12:15]
	v_mfma_f32_16x16x32_bf16 v[8:11], v[150:153], v[226:229], v[8:11]
	v_mfma_f32_16x16x32_bf16 v[60:63], v[146:149], v[206:209], v[60:63]
	v_mfma_f32_16x16x32_bf16 v[56:59], v[154:157], v[206:209], v[56:59]
	v_mfma_f32_16x16x32_bf16 v[44:47], v[146:149], v[214:217], v[44:47]
	v_mfma_f32_16x16x32_bf16 v[40:43], v[154:157], v[214:217], v[40:43]
	v_mfma_f32_16x16x32_bf16 v[28:31], v[146:149], v[222:225], v[28:31]
	v_mfma_f32_16x16x32_bf16 v[24:27], v[154:157], v[222:225], v[24:27]
	v_mfma_f32_16x16x32_bf16 v[12:15], v[146:149], v[230:233], v[12:15]
	v_mfma_f32_16x16x32_bf16 v[8:11], v[154:157], v[230:233], v[8:11]
	v_mfma_f32_16x16x32_bf16 v[52:55], v[158:161], v[186:189], v[52:55]
	v_mfma_f32_16x16x32_bf16 v[48:51], v[178:181], v[186:189], v[48:51]
	v_mfma_f32_16x16x32_bf16 v[36:39], v[158:161], v[210:213], v[36:39]
	v_mfma_f32_16x16x32_bf16 v[32:35], v[178:181], v[210:213], v[32:35]
	v_mfma_f32_16x16x32_bf16 v[20:23], v[158:161], v[218:221], v[20:23]
	v_mfma_f32_16x16x32_bf16 v[16:19], v[178:181], v[218:221], v[16:19]
	v_mfma_f32_16x16x32_bf16 v[4:7], v[158:161], v[226:229], v[4:7]
	v_mfma_f32_16x16x32_bf16 v[0:3], v[178:181], v[226:229], v[0:3]
	v_mfma_f32_16x16x32_bf16 v[52:55], v[174:177], v[206:209], v[52:55]
	v_mfma_f32_16x16x32_bf16 v[48:51], v[182:185], v[206:209], v[48:51]
	v_mfma_f32_16x16x32_bf16 v[36:39], v[174:177], v[214:217], v[36:39]
	v_mfma_f32_16x16x32_bf16 v[32:35], v[182:185], v[214:217], v[32:35]
	v_mfma_f32_16x16x32_bf16 v[20:23], v[174:177], v[222:225], v[20:23]
	v_mfma_f32_16x16x32_bf16 v[16:19], v[182:185], v[222:225], v[16:19]
	v_mfma_f32_16x16x32_bf16 v[4:7], v[174:177], v[230:233], v[4:7]
	v_mfma_f32_16x16x32_bf16 v[0:3], v[182:185], v[230:233], v[0:3]
	s_setprio 0
	s_barrier
	s_add_u32 s48, s48, 0x100
	s_addc_u32 s49, s49, 0
	s_add_u32 s20, s20, 0x100
	s_addc_u32 s21, s21, 0
	s_cmp_ge_i32 s22, s37
	s_mov_b32 s0, s22
	s_cbranch_scc0 .LBB0_1050

; #define PG8_STAGE(bufoff, gbase, voff) do { _Pragma("unroll") for (int _i = 0; _i < 2; ++_i) \
;         __builtin_amdgcn_global_load_lds((const unsigned*)((const char*)(gbase) + (voff)[_i]), (PG8_LAS unsigned*)(lds + (bufoff) + ldsw + _i * 8192), 16, 0, 0); } while (0)
; #define PG8_LDA(dst, b, h) do { if constexpr (FP8) { _Pragma("unroll") for (int m = 0; m < 4; ++m) dst##8[m] = pg8_ld8(lds + PG8_SA(b, h) + aoff + m * 2048); } \
;         else { _Pragma("unroll") for (int m = 0; m < 4; ++m) _Pragma("unroll") for (int k = 0; k < 2; ++k) dst[m][k] = *(const PG8_LAS bf16x8*)(lds + PG8_SA(b, h) + aoff + m * 2048 + k * 1024); } } while (0)
; #define PG8_LDB(dst, b, h) do { if constexpr (FP8) { _Pragma("unroll") for (int n = 0; n < 2; ++n) dst##8[n] = pg8_ld8(lds + PG8_SB(b, h) + boff + n * 2048); } \
;         else { _Pragma("unroll") for (int n = 0; n < 2; ++n) _Pragma("unroll") for (int k = 0; k < 2; ++k) dst[n][k] = *(const PG8_LAS bf16x8*)(lds + PG8_SB(b, h) + boff + n * 2048 + k * 1024); } } while (0)
; #define PG8_WAIT_V(n) asm volatile("s_waitcnt vmcnt(" #n ")" ::: "memory")
; #define PG8_WAIT_L(n) asm volatile("s_waitcnt lgkmcnt(" #n ")" ::: "memory")
; #define PG8_BAR __builtin_amdgcn_s_barrier()
; #define PG8_SCHED __builtin_amdgcn_sched_barrier(0)
;     ...
;             const bool last = (t == nt - 2);
;             const char* a1 = cA + (size_t)(t + 1) * kstep;
;             const char* a2 = last ? nA : cA + (size_t)(t + 2) * kstep; const char* b2 = last ? nB : cB + (size_t)(t + 2) * kstep;
;             const char* a3 = a2 + kstep; const char* b3 = b2 + kstep;
;             if (last && has_next) S.a_ready(nxt);
;             if constexpr (SP2) {
;             PG8_LDB(B0, 0, 0); PG8_LDB(B1, 0, 1); PG8_SCHED; PG8_LDA(At, 0, 0); PG8_STAGE(PG8_SA(1, 1), a1 + hstep, voffA);
;             PG8_WAIT_V(8); PG8_WAIT_L(0); PG8_BAR; PG8_MMA(0, 0, At, B0); PG8_MMA(0, 1, At, B1); PG8_BAR; PG8_SCHED;
;             PG8_LDA(At, 0, 1); PG8_STAGE(PG8_SB(0, 0), b2, voffB); PG8_STAGE(PG8_SB(0, 1), b2 + hstep, voffB); PG8_STAGE(PG8_SA(0, 0), a2, voffA);
;             PG8_WAIT_V(8); PG8_WAIT_L(0); PG8_BAR; PG8_MMA(1, 0, At, B0); PG8_MMA(1, 1, At, B1); PG8_BAR; PG8_SCHED;
.LBB0_1077:
	s_add_u32 s20, s18, 0x100
	s_addc_u32 s21, s19, 0
	s_add_i32 s43, 0, 0x10000
	s_cmp_eq_u32 s42, 24
	s_cselect_b32 s23, s5, s21
	s_cselect_b32 s22, s4, s20
	s_cselect_b32 s1, s17, s41
	s_cselect_b32 s0, s16, s40
	s_add_i32 s44, 0, 0x14000
	v_add_u32_e32 v0, s43, v207
	v_add_u32_e32 v12, s44, v207
	ds_read_b128 v[16:19], v0
	ds_read_b128 v[20:23], v0 offset:1024
	ds_read_b128 v[24:27], v0 offset:2048
	ds_read_b128 v[28:31], v0 offset:3072
	ds_read_b128 v[0:3], v12
	ds_read_b128 v[4:7], v12 offset:1024
	ds_read_b128 v[8:11], v12 offset:2048
	ds_read_b128 v[12:15], v12 offset:3072
	v_lshl_add_u64 v[234:235], s[18:19], 0, v[182:183]
	s_add_i32 m0, s27, 0xc000
	ds_read_b128 v[184:187], v209
	ds_read_b128 v[188:191], v209 offset:1024
	ds_read_b128 v[210:213], v209 offset:2048
	ds_read_b128 v[214:217], v209 offset:3072
	ds_read_b128 v[218:221], v209 offset:4096
	ds_read_b128 v[222:225], v209 offset:5120
	ds_read_b128 v[226:229], v209 offset:6144
	ds_read_b128 v[230:233], v209 offset:7168
	global_load_lds_dwordx4 v[234:235], off
	v_lshl_add_u64 v[234:235], s[18:19], 0, v[180:181]
	s_add_i32 m0, s27, 0xe000
	s_nop 0
	global_load_lds_dwordx4 v[234:235], off
	s_waitcnt vmcnt(8)
	s_waitcnt lgkmcnt(0)
	s_barrier
	s_setprio 1
	s_waitcnt lgkmcnt(0)
	v_mfma_scale_f32_16x16x128_f8f6f4 v[158:161], v[16:23], v[184:191], v[158:161], v205, v205 op_sel_hi:[0,0,0]
	v_mfma_scale_f32_16x16x128_f8f6f4 v[154:157], v[24:31], v[184:191], v[154:157], v205, v205 op_sel_hi:[0,0,0]
	v_mfma_scale_f32_16x16x128_f8f6f4 v[142:145], v[16:23], v[210:217], v[142:145], v205, v205 op_sel_hi:[0,0,0]
	v_mfma_scale_f32_16x16x128_f8f6f4 v[138:141], v[24:31], v[210:217], v[138:141], v205, v205 op_sel_hi:[0,0,0]
	v_mfma_scale_f32_16x16x128_f8f6f4 v[126:129], v[16:23], v[218:225], v[126:129], v205, v205 op_sel_hi:[0,0,0]
	v_mfma_scale_f32_16x16x128_f8f6f4 v[122:125], v[24:31], v[218:225], v[122:125], v205, v205 op_sel_hi:[0,0,0]
	v_mfma_scale_f32_16x16x128_f8f6f4 v[110:113], v[16:23], v[226:233], v[110:113], v205, v205 op_sel_hi:[0,0,0]
	v_mfma_scale_f32_16x16x128_f8f6f4 v[106:109], v[24:31], v[226:233], v[106:109], v205, v205 op_sel_hi:[0,0,0]
	v_mfma_scale_f32_16x16x128_f8f6f4 v[150:153], v[0:7], v[184:191], v[150:153], v205, v205 op_sel_hi:[0,0,0]
	v_mfma_scale_f32_16x16x128_f8f6f4 v[146:149], v[8:15], v[184:191], v[146:149], v205, v205 op_sel_hi:[0,0,0]
	v_mfma_scale_f32_16x16x128_f8f6f4 v[134:137], v[0:7], v[210:217], v[134:137], v205, v205 op_sel_hi:[0,0,0]
	v_mfma_scale_f32_16x16x128_f8f6f4 v[130:133], v[8:15], v[210:217], v[130:133], v205, v205 op_sel_hi:[0,0,0]
	v_mfma_scale_f32_16x16x128_f8f6f4 v[118:121], v[0:7], v[218:225], v[118:121], v205, v205 op_sel_hi:[0,0,0]
	v_mfma_scale_f32_16x16x128_f8f6f4 v[114:117], v[8:15], v[218:225], v[114:117], v205, v205 op_sel_hi:[0,0,0]
	v_mfma_scale_f32_16x16x128_f8f6f4 v[102:105], v[0:7], v[226:233], v[102:105], v205, v205 op_sel_hi:[0,0,0]
	v_mfma_scale_f32_16x16x128_f8f6f4 v[98:101], v[8:15], v[226:233], v[98:101], v205, v205 op_sel_hi:[0,0,0]
	s_setprio 0
	s_barrier
	s_add_i32 s18, s43, s24
	v_lshl_add_u64 v[184:185], s[0:1], 0, v[80:81]
	s_mov_b32 m0, s18
	ds_read_b128 v[210:213], v209 offset:16384
	ds_read_b128 v[214:217], v209 offset:17408
	ds_read_b128 v[218:221], v209 offset:18432
	ds_read_b128 v[222:225], v209 offset:19456
	ds_read_b128 v[226:229], v209 offset:20480
	ds_read_b128 v[230:233], v209 offset:21504
	ds_read_b128 v[234:237], v209 offset:22528
	ds_read_b128 v[238:241], v209 offset:23552
	global_load_lds_dwordx4 v[184:185], off
	s_add_i32 m0, s18, 0x2000
	s_add_u32 s18, s0, 0x70000
	v_lshl_add_u64 v[186:187], s[0:1], 0, v[174:175]
	s_addc_u32 s19, s1, 0
	s_add_i32 s43, s44, s24
	global_load_lds_dwordx4 v[186:187], off
	v_lshl_add_u64 v[188:189], s[18:19], 0, v[80:81]
	s_mov_b32 m0, s43
	v_lshl_add_u64 v[190:191], s[22:23], 0, v[176:177]
	global_load_lds_dwordx4 v[188:189], off
	v_lshl_add_u64 v[188:189], s[18:19], 0, v[174:175]
	s_add_i32 m0, s43, 0x2000
	s_nop 0
	global_load_lds_dwordx4 v[188:189], off
	v_lshl_add_u64 v[188:189], s[22:23], 0, v[178:179]
	s_mov_b32 m0, s27
	s_nop 0
	global_load_lds_dwordx4 v[188:189], off
	s_mov_b32 m0, s28
	s_nop 0
	global_load_lds_dwordx4 v[190:191], off
	s_waitcnt vmcnt(8)
	s_waitcnt lgkmcnt(0)
	s_barrier
	s_setprio 1
	s_waitcnt lgkmcnt(0)
	v_mfma_scale_f32_16x16x128_f8f6f4 v[94:97], v[16:23], v[210:217], v[94:97], v205, v205 op_sel_hi:[0,0,0]
	v_mfma_scale_f32_16x16x128_f8f6f4 v[90:93], v[24:31], v[210:217], v[90:93], v205, v205 op_sel_hi:[0,0,0]
	v_mfma_scale_f32_16x16x128_f8f6f4 v[76:79], v[16:23], v[218:225], v[76:79], v205, v205 op_sel_hi:[0,0,0]
	v_mfma_scale_f32_16x16x128_f8f6f4 v[72:75], v[24:31], v[218:225], v[72:75], v205, v205 op_sel_hi:[0,0,0]
	v_mfma_scale_f32_16x16x128_f8f6f4 v[60:63], v[16:23], v[226:233], v[60:63], v205, v205 op_sel_hi:[0,0,0]
	v_mfma_scale_f32_16x16x128_f8f6f4 v[56:59], v[24:31], v[226:233], v[56:59], v205, v205 op_sel_hi:[0,0,0]
	v_mfma_scale_f32_16x16x128_f8f6f4 v[44:47], v[16:23], v[234:241], v[44:47], v205, v205 op_sel_hi:[0,0,0]
	v_mfma_scale_f32_16x16x128_f8f6f4 v[40:43], v[24:31], v[234:241], v[40:43], v205, v205 op_sel_hi:[0,0,0]
	v_mfma_scale_f32_16x16x128_f8f6f4 v[86:89], v[0:7], v[210:217], v[86:89], v205, v205 op_sel_hi:[0,0,0]
	v_mfma_scale_f32_16x16x128_f8f6f4 v[82:85], v[8:15], v[210:217], v[82:85], v205, v205 op_sel_hi:[0,0,0]
	v_mfma_scale_f32_16x16x128_f8f6f4 v[68:71], v[0:7], v[218:225], v[68:71], v205, v205 op_sel_hi:[0,0,0]
	v_mfma_scale_f32_16x16x128_f8f6f4 v[64:67], v[8:15], v[218:225], v[64:67], v205, v205 op_sel_hi:[0,0,0]
	v_mfma_scale_f32_16x16x128_f8f6f4 v[52:55], v[0:7], v[226:233], v[52:55], v205, v205 op_sel_hi:[0,0,0]
	v_mfma_scale_f32_16x16x128_f8f6f4 v[48:51], v[8:15], v[226:233], v[48:51], v205, v205 op_sel_hi:[0,0,0]
	v_mfma_scale_f32_16x16x128_f8f6f4 v[36:39], v[0:7], v[234:241], v[36:39], v205, v205 op_sel_hi:[0,0,0]
	v_mfma_scale_f32_16x16x128_f8f6f4 v[32:35], v[8:15], v[234:241], v[32:35], v205, v205 op_sel_hi:[0,0,0]
	s_setprio 0
	s_barrier
; #define PG8_STAGE(bufoff, gbase, voff) do { _Pragma("unroll") for (int _i = 0; _i < 2; ++_i) \
;         __builtin_amdgcn_global_load_lds((const unsigned*)((const char*)(gbase) + (voff)[_i]), (PG8_LAS unsigned*)(lds + (bufoff) + ldsw + _i * 8192), 16, 0, 0); } while (0)
; #define PG8_LDA(dst, b, h) do { if constexpr (FP8) { _Pragma("unroll") for (int m = 0; m < 4; ++m) dst##8[m] = pg8_ld8(lds + PG8_SA(b, h) + aoff + m * 2048); } \
;         else { _Pragma("unroll") for (int m = 0; m < 4; ++m) _Pragma("unroll") for (int k = 0; k < 2; ++k) dst[m][k] = *(const PG8_LAS bf16x8*)(lds + PG8_SA(b, h) + aoff + m * 2048 + k * 1024); } } while (0)
; #define PG8_LDB(dst, b, h) do { if constexpr (FP8) { _Pragma("unroll") for (int n = 0; n < 2; ++n) dst##8[n] = pg8_ld8(lds + PG8_SB(b, h) + boff + n * 2048); } \
;         else { _Pragma("unroll") for (int n = 0; n < 2; ++n) _Pragma("unroll") for (int k = 0; k < 2; ++k) dst[n][k] = *(const PG8_LAS bf16x8*)(lds + PG8_SB(b, h) + boff + n * 2048 + k * 1024); } } while (0)
; #define PG8_WAIT_V(n) asm volatile("s_waitcnt vmcnt(" #n ")" ::: "memory")
; #define PG8_WAIT_L(n) asm volatile("s_waitcnt lgkmcnt(" #n ")" ::: "memory")
; #define PG8_BAR __builtin_amdgcn_s_barrier()
; #define PG8_SCHED __builtin_amdgcn_sched_barrier(0)
;     ...
;             PG8_LDB(B0, 1, 0); PG8_LDB(B1, 1, 1); PG8_SCHED; PG8_LDA(At, 1, 0); PG8_STAGE(PG8_SA(0, 1), a2 + hstep, voffA);
;             PG8_WAIT_V(8); PG8_WAIT_L(0); PG8_BAR; PG8_MMA(0, 0, At, B0); PG8_MMA(0, 1, At, B1); PG8_BAR; PG8_SCHED;
;             PG8_LDA(At, 1, 1); PG8_STAGE(PG8_SB(1, 0), b3, voffB); PG8_STAGE(PG8_SB(1, 1), b3 + hstep, voffB); PG8_STAGE(PG8_SA(1, 0), a3, voffA);
;             PG8_WAIT_V(8); PG8_WAIT_L(0); PG8_BAR; PG8_MMA(1, 0, At, B0); PG8_MMA(1, 1, At, B1); PG8_BAR; PG8_SCHED;
;     ...
;         if constexpr (FP8) asm volatile("s_nop 15\n\ts_nop 15" ::: "memory");
;         if constexpr (ALIGN_EPI) { if (wr == 0) PG8_BAR; }
	s_add_i32 s43, 0, 0x18000
	s_add_i32 s44, 0, 0x1c000
	v_add_u32_e32 v12, s43, v207
	v_add_u32_e32 v28, s44, v207
	ds_read_b128 v[0:3], v12
	ds_read_b128 v[4:7], v12 offset:1024
	ds_read_b128 v[8:11], v12 offset:2048
	ds_read_b128 v[12:15], v12 offset:3072
	ds_read_b128 v[16:19], v28
	ds_read_b128 v[20:23], v28 offset:1024
	ds_read_b128 v[24:27], v28 offset:2048
	ds_read_b128 v[28:31], v28 offset:3072
	s_add_u32 s18, s22, 0x70000
	s_addc_u32 s19, s23, 0
	s_mov_b32 m0, s29
	v_lshl_add_u64 v[242:243], s[18:19], 0, v[178:179]
	ds_read_b128 v[210:213], v209 offset:32768
	ds_read_b128 v[214:217], v209 offset:33792
	ds_read_b128 v[218:221], v209 offset:34816
	ds_read_b128 v[222:225], v209 offset:35840
	ds_read_b128 v[226:229], v209 offset:36864
	ds_read_b128 v[230:233], v209 offset:37888
	ds_read_b128 v[234:237], v209 offset:38912
	ds_read_b128 v[238:241], v209 offset:39936
	global_load_lds_dwordx4 v[242:243], off
	v_lshl_add_u64 v[242:243], s[18:19], 0, v[176:177]
	s_mov_b32 m0, s30
	s_nop 0
	global_load_lds_dwordx4 v[242:243], off
	s_waitcnt vmcnt(8)
	s_waitcnt lgkmcnt(0)
	s_barrier
	s_setprio 1
	s_waitcnt lgkmcnt(0)
	v_mfma_scale_f32_16x16x128_f8f6f4 v[158:161], v[0:7], v[210:217], v[158:161], v205, v205 op_sel_hi:[0,0,0]
	v_mfma_scale_f32_16x16x128_f8f6f4 v[154:157], v[8:15], v[210:217], v[154:157], v205, v205 op_sel_hi:[0,0,0]
	v_mfma_scale_f32_16x16x128_f8f6f4 v[142:145], v[0:7], v[218:225], v[142:145], v205, v205 op_sel_hi:[0,0,0]
	v_mfma_scale_f32_16x16x128_f8f6f4 v[138:141], v[8:15], v[218:225], v[138:141], v205, v205 op_sel_hi:[0,0,0]
	v_mfma_scale_f32_16x16x128_f8f6f4 v[126:129], v[0:7], v[226:233], v[126:129], v205, v205 op_sel_hi:[0,0,0]
	v_mfma_scale_f32_16x16x128_f8f6f4 v[122:125], v[8:15], v[226:233], v[122:125], v205, v205 op_sel_hi:[0,0,0]
	v_mfma_scale_f32_16x16x128_f8f6f4 v[110:113], v[0:7], v[234:241], v[110:113], v205, v205 op_sel_hi:[0,0,0]
	v_mfma_scale_f32_16x16x128_f8f6f4 v[106:109], v[8:15], v[234:241], v[106:109], v205, v205 op_sel_hi:[0,0,0]
	v_mfma_scale_f32_16x16x128_f8f6f4 v[150:153], v[16:23], v[210:217], v[150:153], v205, v205 op_sel_hi:[0,0,0]
	v_mfma_scale_f32_16x16x128_f8f6f4 v[146:149], v[24:31], v[210:217], v[146:149], v205, v205 op_sel_hi:[0,0,0]
	v_mfma_scale_f32_16x16x128_f8f6f4 v[134:137], v[16:23], v[218:225], v[134:137], v205, v205 op_sel_hi:[0,0,0]
	v_mfma_scale_f32_16x16x128_f8f6f4 v[130:133], v[24:31], v[218:225], v[130:133], v205, v205 op_sel_hi:[0,0,0]
	v_mfma_scale_f32_16x16x128_f8f6f4 v[118:121], v[16:23], v[226:233], v[118:121], v205, v205 op_sel_hi:[0,0,0]
	v_mfma_scale_f32_16x16x128_f8f6f4 v[114:117], v[24:31], v[226:233], v[114:117], v205, v205 op_sel_hi:[0,0,0]
	v_mfma_scale_f32_16x16x128_f8f6f4 v[102:105], v[16:23], v[234:241], v[102:105], v205, v205 op_sel_hi:[0,0,0]
	v_mfma_scale_f32_16x16x128_f8f6f4 v[98:101], v[24:31], v[234:241], v[98:101], v205, v205 op_sel_hi:[0,0,0]
	s_setprio 0
	s_barrier
	s_add_i32 s18, s43, s24
	v_lshl_add_u64 v[184:185], v[184:185], 0, s[86:87]
	s_mov_b32 m0, s18
	ds_read_b128 v[210:213], v209 offset:49152
	ds_read_b128 v[214:217], v209 offset:50176
	ds_read_b128 v[218:221], v209 offset:51200
	ds_read_b128 v[222:225], v209 offset:52224
	ds_read_b128 v[226:229], v209 offset:53248
	ds_read_b128 v[230:233], v209 offset:54272
	ds_read_b128 v[234:237], v209 offset:55296
	ds_read_b128 v[238:241], v209 offset:56320
	global_load_lds_dwordx4 v[184:185], off
	s_add_i32 m0, s18, 0x2000
	s_add_u32 s0, s0, 0x70080
	v_lshl_add_u64 v[184:185], v[186:187], 0, s[86:87]
	s_addc_u32 s1, s1, 0
	s_add_i32 s18, s44, s24
	global_load_lds_dwordx4 v[184:185], off
	v_lshl_add_u64 v[184:185], s[0:1], 0, v[80:81]
	s_mov_b32 m0, s18
	s_nop 0
	global_load_lds_dwordx4 v[184:185], off
	v_lshl_add_u64 v[184:185], s[0:1], 0, v[174:175]
	s_add_i32 m0, s18, 0x2000
	s_nop 0
	global_load_lds_dwordx4 v[184:185], off
	v_lshl_add_u64 v[184:185], v[188:189], 0, s[86:87]
	s_mov_b32 m0, s31
	s_nop 0
	global_load_lds_dwordx4 v[184:185], off
	v_lshl_add_u64 v[184:185], v[190:191], 0, s[86:87]
	s_mov_b32 m0, s34
	s_nop 0
	global_load_lds_dwordx4 v[184:185], off
	s_waitcnt vmcnt(8)
	s_waitcnt lgkmcnt(0)
	s_barrier
	s_setprio 1
	s_waitcnt lgkmcnt(0)
	v_mfma_scale_f32_16x16x128_f8f6f4 v[94:97], v[0:7], v[210:217], v[94:97], v205, v205 op_sel_hi:[0,0,0]
	v_mfma_scale_f32_16x16x128_f8f6f4 v[90:93], v[8:15], v[210:217], v[90:93], v205, v205 op_sel_hi:[0,0,0]
	v_mfma_scale_f32_16x16x128_f8f6f4 v[76:79], v[0:7], v[218:225], v[76:79], v205, v205 op_sel_hi:[0,0,0]
	v_mfma_scale_f32_16x16x128_f8f6f4 v[72:75], v[8:15], v[218:225], v[72:75], v205, v205 op_sel_hi:[0,0,0]
	v_mfma_scale_f32_16x16x128_f8f6f4 v[60:63], v[0:7], v[226:233], v[60:63], v205, v205 op_sel_hi:[0,0,0]
	v_mfma_scale_f32_16x16x128_f8f6f4 v[56:59], v[8:15], v[226:233], v[56:59], v205, v205 op_sel_hi:[0,0,0]
	v_mfma_scale_f32_16x16x128_f8f6f4 v[44:47], v[0:7], v[234:241], v[44:47], v205, v205 op_sel_hi:[0,0,0]
	v_mfma_scale_f32_16x16x128_f8f6f4 v[40:43], v[8:15], v[234:241], v[40:43], v205, v205 op_sel_hi:[0,0,0]
	v_mfma_scale_f32_16x16x128_f8f6f4 v[86:89], v[16:23], v[210:217], v[86:89], v205, v205 op_sel_hi:[0,0,0]
	v_mfma_scale_f32_16x16x128_f8f6f4 v[82:85], v[24:31], v[210:217], v[82:85], v205, v205 op_sel_hi:[0,0,0]
	v_mfma_scale_f32_16x16x128_f8f6f4 v[68:71], v[16:23], v[218:225], v[68:71], v205, v205 op_sel_hi:[0,0,0]
	v_mfma_scale_f32_16x16x128_f8f6f4 v[64:67], v[24:31], v[218:225], v[64:67], v205, v205 op_sel_hi:[0,0,0]
	v_mfma_scale_f32_16x16x128_f8f6f4 v[52:55], v[16:23], v[226:233], v[52:55], v205, v205 op_sel_hi:[0,0,0]
	v_mfma_scale_f32_16x16x128_f8f6f4 v[48:51], v[24:31], v[226:233], v[48:51], v205, v205 op_sel_hi:[0,0,0]
	v_mfma_scale_f32_16x16x128_f8f6f4 v[36:39], v[16:23], v[234:241], v[36:39], v205, v205 op_sel_hi:[0,0,0]
	v_mfma_scale_f32_16x16x128_f8f6f4 v[32:35], v[24:31], v[234:241], v[32:35], v205, v205 op_sel_hi:[0,0,0]
	s_setprio 0
	s_barrier
	s_add_i32 s42, s42, 2
	s_add_u32 s40, s40, 0x100
	s_addc_u32 s41, s41, 0
	s_cmp_gt_u32 s42, 25
	s_mov_b64 s[18:19], s[20:21]
	s_cbranch_scc0 .LBB0_1077
	s_nop 15
	s_nop 15
	s_and_b64 vcc, exec, s[12:13]
	s_cbranch_vccz .LBB0_1080
	s_barrier

; #define PG8_STAGE(bufoff, gbase, voff) do { _Pragma("unroll") for (int _i = 0; _i < 2; ++_i) \
;         __builtin_amdgcn_global_load_lds((const unsigned*)((const char*)(gbase) + (voff)[_i]), (PG8_LAS unsigned*)(lds + (bufoff) + ldsw + _i * 8192), 16, 0, 0); } while (0)
; #define PG8_LDA(dst, b, h) do { if constexpr (FP8) { _Pragma("unroll") for (int m = 0; m < 4; ++m) dst##8[m] = pg8_ld8(lds + PG8_SA(b, h) + aoff + m * 2048); } \
;         else { _Pragma("unroll") for (int m = 0; m < 4; ++m) _Pragma("unroll") for (int k = 0; k < 2; ++k) dst[m][k] = *(const PG8_LAS bf16x8*)(lds + PG8_SA(b, h) + aoff + m * 2048 + k * 1024); } } while (0)
; #define PG8_LDB(dst, b, h) do { if constexpr (FP8) { _Pragma("unroll") for (int n = 0; n < 2; ++n) dst##8[n] = pg8_ld8(lds + PG8_SB(b, h) + boff + n * 2048); } \
;         else { _Pragma("unroll") for (int n = 0; n < 2; ++n) _Pragma("unroll") for (int k = 0; k < 2; ++k) dst[n][k] = *(const PG8_LAS bf16x8*)(lds + PG8_SB(b, h) + boff + n * 2048 + k * 1024); } } while (0)
; #define PG8_WAIT_V(n) asm volatile("s_waitcnt vmcnt(" #n ")" ::: "memory")
; #define PG8_WAIT_L(n) asm volatile("s_waitcnt lgkmcnt(" #n ")" ::: "memory")
; #define PG8_BAR __builtin_amdgcn_s_barrier()
; #define PG8_SCHED __builtin_amdgcn_sched_barrier(0)
;     ...
;             const bool last = (t == nt - 2);
;             const char* a1 = cA + (size_t)(t + 1) * kstep;
;             const char* a2 = last ? nA : cA + (size_t)(t + 2) * kstep; const char* b2 = last ? nB : cB + (size_t)(t + 2) * kstep;
;             const char* a3 = a2 + kstep; const char* b3 = b2 + kstep;
;             if (last && has_next) S.a_ready(nxt);
;             if constexpr (SP2) {
;             PG8_LDB(B0, 0, 0); PG8_LDB(B1, 0, 1); PG8_SCHED; PG8_LDA(At, 0, 0); PG8_STAGE(PG8_SA(1, 1), a1 + hstep, voffA);
;             PG8_WAIT_V(8); PG8_WAIT_L(0); PG8_BAR; PG8_MMA(0, 0, At, B0); PG8_MMA(0, 1, At, B1); PG8_BAR; PG8_SCHED;
;             PG8_LDA(At, 0, 1); PG8_STAGE(PG8_SB(0, 0), b2, voffB); PG8_STAGE(PG8_SB(0, 1), b2 + hstep, voffB); PG8_STAGE(PG8_SA(0, 0), a2, voffA);
.LBB0_1109:
	s_add_u32 s0, s14, 0x100
	s_addc_u32 s1, s15, 0
	s_add_i32 s44, 0, 0x10000
	s_cmp_eq_u32 s43, 40
	s_cselect_b32 s19, s5, s1
	s_cselect_b32 s18, s4, s0
	s_cselect_b32 s17, s13, s42
	s_cselect_b32 s16, s12, s41
	s_add_i32 s45, 0, 0x14000
	v_add_u32_e32 v152, s44, v156
	v_add_u32_e32 v170, s45, v156
	ds_read_b128 v[130:133], v152
	ds_read_b128 v[134:137], v152 offset:1024
	ds_read_b128 v[148:151], v152 offset:2048
	ds_read_b128 v[152:155], v152 offset:3072
	ds_read_b128 v[158:161], v170
	ds_read_b128 v[174:177], v170 offset:1024
	ds_read_b128 v[178:181], v170 offset:2048
	ds_read_b128 v[182:185], v170 offset:3072
	v_lshl_add_u64 v[190:191], s[14:15], 0, v[146:147]
	s_add_i32 m0, s24, 0xc000
	ds_read_b128 v[186:189], v157
	ds_read_b128 v[206:209], v157 offset:1024
	ds_read_b128 v[210:213], v157 offset:2048
	ds_read_b128 v[214:217], v157 offset:3072
	ds_read_b128 v[218:221], v157 offset:4096
	ds_read_b128 v[222:225], v157 offset:5120
	ds_read_b128 v[226:229], v157 offset:6144
	ds_read_b128 v[230:233], v157 offset:7168
	global_load_lds_dwordx4 v[190:191], off
	v_lshl_add_u64 v[190:191], s[14:15], 0, v[144:145]
	s_add_i32 m0, s24, 0xe000
	s_nop 0
	global_load_lds_dwordx4 v[190:191], off
	s_waitcnt vmcnt(8)
	s_waitcnt lgkmcnt(0)
	s_barrier
	s_setprio 1
	s_waitcnt lgkmcnt(0)
	v_mfma_f32_16x16x32_bf16 v[126:129], v[130:133], v[186:189], v[126:129]
	v_mfma_f32_16x16x32_bf16 v[122:125], v[148:151], v[186:189], v[122:125]
	v_mfma_f32_16x16x32_bf16 v[110:113], v[130:133], v[210:213], v[110:113]
	v_mfma_f32_16x16x32_bf16 v[106:109], v[148:151], v[210:213], v[106:109]
	v_mfma_f32_16x16x32_bf16 v[94:97], v[130:133], v[218:221], v[94:97]
	v_mfma_f32_16x16x32_bf16 v[90:93], v[148:151], v[218:221], v[90:93]
	v_mfma_f32_16x16x32_bf16 v[76:79], v[130:133], v[226:229], v[76:79]
	v_mfma_f32_16x16x32_bf16 v[72:75], v[148:151], v[226:229], v[72:75]
	v_mfma_f32_16x16x32_bf16 v[126:129], v[134:137], v[206:209], v[126:129]
	v_mfma_f32_16x16x32_bf16 v[122:125], v[152:155], v[206:209], v[122:125]
	v_mfma_f32_16x16x32_bf16 v[110:113], v[134:137], v[214:217], v[110:113]
	v_mfma_f32_16x16x32_bf16 v[106:109], v[152:155], v[214:217], v[106:109]
	v_mfma_f32_16x16x32_bf16 v[94:97], v[134:137], v[222:225], v[94:97]
	v_mfma_f32_16x16x32_bf16 v[90:93], v[152:155], v[222:225], v[90:93]
	v_mfma_f32_16x16x32_bf16 v[76:79], v[134:137], v[230:233], v[76:79]
	v_mfma_f32_16x16x32_bf16 v[72:75], v[152:155], v[230:233], v[72:75]
	v_mfma_f32_16x16x32_bf16 v[118:121], v[158:161], v[186:189], v[118:121]
	v_mfma_f32_16x16x32_bf16 v[114:117], v[178:181], v[186:189], v[114:117]
	v_mfma_f32_16x16x32_bf16 v[102:105], v[158:161], v[210:213], v[102:105]
	v_mfma_f32_16x16x32_bf16 v[98:101], v[178:181], v[210:213], v[98:101]
	v_mfma_f32_16x16x32_bf16 v[86:89], v[158:161], v[218:221], v[86:89]
	v_mfma_f32_16x16x32_bf16 v[82:85], v[178:181], v[218:221], v[82:85]
	v_mfma_f32_16x16x32_bf16 v[68:71], v[158:161], v[226:229], v[68:71]
	v_mfma_f32_16x16x32_bf16 v[64:67], v[178:181], v[226:229], v[64:67]
	v_mfma_f32_16x16x32_bf16 v[118:121], v[174:177], v[206:209], v[118:121]
	v_mfma_f32_16x16x32_bf16 v[114:117], v[182:185], v[206:209], v[114:117]
	v_mfma_f32_16x16x32_bf16 v[102:105], v[174:177], v[214:217], v[102:105]
	v_mfma_f32_16x16x32_bf16 v[98:101], v[182:185], v[214:217], v[98:101]
	v_mfma_f32_16x16x32_bf16 v[86:89], v[174:177], v[222:225], v[86:89]
	v_mfma_f32_16x16x32_bf16 v[82:85], v[182:185], v[222:225], v[82:85]
	v_mfma_f32_16x16x32_bf16 v[68:71], v[174:177], v[230:233], v[68:71]
	v_mfma_f32_16x16x32_bf16 v[64:67], v[182:185], v[230:233], v[64:67]
	s_setprio 0
	s_barrier
	s_add_i32 s14, s44, s23
	v_lshl_add_u64 v[190:191], s[16:17], 0, v[80:81]
	s_mov_b32 m0, s14
	ds_read_b128 v[186:189], v157 offset:16384
	ds_read_b128 v[206:209], v157 offset:17408
	ds_read_b128 v[210:213], v157 offset:18432
	ds_read_b128 v[214:217], v157 offset:19456
	ds_read_b128 v[218:221], v157 offset:20480
	ds_read_b128 v[222:225], v157 offset:21504
	ds_read_b128 v[226:229], v157 offset:22528
	ds_read_b128 v[230:233], v157 offset:23552
	global_load_lds_dwordx4 v[190:191], off
	s_add_i32 m0, s14, 0x2000
	s_add_u32 s14, s16, 0xb0000
	v_lshl_add_u64 v[234:235], s[16:17], 0, v[142:143]
	s_addc_u32 s15, s17, 0
	s_add_i32 s44, s45, s23
	global_load_lds_dwordx4 v[234:235], off
	v_lshl_add_u64 v[236:237], s[14:15], 0, v[80:81]
	s_mov_b32 m0, s44
	v_lshl_add_u64 v[238:239], s[18:19], 0, v[140:141]
	global_load_lds_dwordx4 v[236:237], off
	v_lshl_add_u64 v[236:237], s[14:15], 0, v[142:143]
	s_add_i32 m0, s44, 0x2000
	s_nop 0
	global_load_lds_dwordx4 v[236:237], off
	v_lshl_add_u64 v[236:237], s[18:19], 0, v[138:139]
	s_mov_b32 m0, s24
	s_nop 0
	global_load_lds_dwordx4 v[236:237], off
	s_mov_b32 m0, s25
	s_nop 0
	global_load_lds_dwordx4 v[238:239], off
	s_waitcnt vmcnt(8)
	s_waitcnt lgkmcnt(0)
	s_barrier
; #define PG8_STAGE(bufoff, gbase, voff) do { _Pragma("unroll") for (int _i = 0; _i < 2; ++_i) \
;         __builtin_amdgcn_global_load_lds((const unsigned*)((const char*)(gbase) + (voff)[_i]), (PG8_LAS unsigned*)(lds + (bufoff) + ldsw + _i * 8192), 16, 0, 0); } while (0)
; #define PG8_LDA(dst, b, h) do { if constexpr (FP8) { _Pragma("unroll") for (int m = 0; m < 4; ++m) dst##8[m] = pg8_ld8(lds + PG8_SA(b, h) + aoff + m * 2048); } \
;         else { _Pragma("unroll") for (int m = 0; m < 4; ++m) _Pragma("unroll") for (int k = 0; k < 2; ++k) dst[m][k] = *(const PG8_LAS bf16x8*)(lds + PG8_SA(b, h) + aoff + m * 2048 + k * 1024); } } while (0)
; #define PG8_LDB(dst, b, h) do { if constexpr (FP8) { _Pragma("unroll") for (int n = 0; n < 2; ++n) dst##8[n] = pg8_ld8(lds + PG8_SB(b, h) + boff + n * 2048); } \
;         else { _Pragma("unroll") for (int n = 0; n < 2; ++n) _Pragma("unroll") for (int k = 0; k < 2; ++k) dst[n][k] = *(const PG8_LAS bf16x8*)(lds + PG8_SB(b, h) + boff + n * 2048 + k * 1024); } } while (0)
; #define PG8_WAIT_V(n) asm volatile("s_waitcnt vmcnt(" #n ")" ::: "memory")
; #define PG8_WAIT_L(n) asm volatile("s_waitcnt lgkmcnt(" #n ")" ::: "memory")
; #define PG8_BAR __builtin_amdgcn_s_barrier()
; #define PG8_SCHED __builtin_amdgcn_sched_barrier(0)
;     ...
;             PG8_WAIT_V(8); PG8_WAIT_L(0); PG8_BAR; PG8_MMA(0, 0, At, B0); PG8_MMA(0, 1, At, B1); PG8_BAR; PG8_SCHED;
;             PG8_LDA(At, 0, 1); PG8_STAGE(PG8_SB(0, 0), b2, voffB); PG8_STAGE(PG8_SB(0, 1), b2 + hstep, voffB); PG8_STAGE(PG8_SA(0, 0), a2, voffA);
;             PG8_WAIT_V(8); PG8_WAIT_L(0); PG8_BAR; PG8_MMA(1, 0, At, B0); PG8_MMA(1, 1, At, B1); PG8_BAR; PG8_SCHED;
;             PG8_LDB(B0, 1, 0); PG8_LDB(B1, 1, 1); PG8_SCHED; PG8_LDA(At, 1, 0); PG8_STAGE(PG8_SA(0, 1), a2 + hstep, voffA);
;             PG8_WAIT_V(8); PG8_WAIT_L(0); PG8_BAR; PG8_MMA(0, 0, At, B0); PG8_MMA(0, 1, At, B1); PG8_BAR; PG8_SCHED;
	s_setprio 1
	s_waitcnt lgkmcnt(0)
	v_mfma_f32_16x16x32_bf16 v[60:63], v[130:133], v[186:189], v[60:63]
	v_mfma_f32_16x16x32_bf16 v[56:59], v[148:151], v[186:189], v[56:59]
	v_mfma_f32_16x16x32_bf16 v[44:47], v[130:133], v[210:213], v[44:47]
	v_mfma_f32_16x16x32_bf16 v[40:43], v[148:151], v[210:213], v[40:43]
	v_mfma_f32_16x16x32_bf16 v[28:31], v[130:133], v[218:221], v[28:31]
	v_mfma_f32_16x16x32_bf16 v[24:27], v[148:151], v[218:221], v[24:27]
	v_mfma_f32_16x16x32_bf16 v[12:15], v[130:133], v[226:229], v[12:15]
	v_mfma_f32_16x16x32_bf16 v[8:11], v[148:151], v[226:229], v[8:11]
	v_mfma_f32_16x16x32_bf16 v[60:63], v[134:137], v[206:209], v[60:63]
	v_mfma_f32_16x16x32_bf16 v[56:59], v[152:155], v[206:209], v[56:59]
	v_mfma_f32_16x16x32_bf16 v[44:47], v[134:137], v[214:217], v[44:47]
	v_mfma_f32_16x16x32_bf16 v[40:43], v[152:155], v[214:217], v[40:43]
	v_mfma_f32_16x16x32_bf16 v[28:31], v[134:137], v[222:225], v[28:31]
	v_mfma_f32_16x16x32_bf16 v[24:27], v[152:155], v[222:225], v[24:27]
	v_mfma_f32_16x16x32_bf16 v[12:15], v[134:137], v[230:233], v[12:15]
	v_mfma_f32_16x16x32_bf16 v[8:11], v[152:155], v[230:233], v[8:11]
	v_mfma_f32_16x16x32_bf16 v[52:55], v[158:161], v[186:189], v[52:55]
	v_mfma_f32_16x16x32_bf16 v[48:51], v[178:181], v[186:189], v[48:51]
	v_mfma_f32_16x16x32_bf16 v[36:39], v[158:161], v[210:213], v[36:39]
	v_mfma_f32_16x16x32_bf16 v[32:35], v[178:181], v[210:213], v[32:35]
	v_mfma_f32_16x16x32_bf16 v[20:23], v[158:161], v[218:221], v[20:23]
	v_mfma_f32_16x16x32_bf16 v[16:19], v[178:181], v[218:221], v[16:19]
	v_mfma_f32_16x16x32_bf16 v[4:7], v[158:161], v[226:229], v[4:7]
	v_mfma_f32_16x16x32_bf16 v[0:3], v[178:181], v[226:229], v[0:3]
	v_mfma_f32_16x16x32_bf16 v[52:55], v[174:177], v[206:209], v[52:55]
	v_mfma_f32_16x16x32_bf16 v[48:51], v[182:185], v[206:209], v[48:51]
	v_mfma_f32_16x16x32_bf16 v[36:39], v[174:177], v[214:217], v[36:39]
	v_mfma_f32_16x16x32_bf16 v[32:35], v[182:185], v[214:217], v[32:35]
	v_mfma_f32_16x16x32_bf16 v[20:23], v[174:177], v[222:225], v[20:23]
	v_mfma_f32_16x16x32_bf16 v[16:19], v[182:185], v[222:225], v[16:19]
	v_mfma_f32_16x16x32_bf16 v[4:7], v[174:177], v[230:233], v[4:7]
	v_mfma_f32_16x16x32_bf16 v[0:3], v[182:185], v[230:233], v[0:3]
	s_setprio 0
	s_barrier
	s_add_i32 s44, 0, 0x18000
	s_add_i32 s45, 0, 0x1c000
	v_add_u32_e32 v152, s44, v156
	v_add_u32_e32 v170, s45, v156
	ds_read_b128 v[130:133], v152
	ds_read_b128 v[134:137], v152 offset:1024
	ds_read_b128 v[148:151], v152 offset:2048
	ds_read_b128 v[152:155], v152 offset:3072
	ds_read_b128 v[158:161], v170
	ds_read_b128 v[174:177], v170 offset:1024
	ds_read_b128 v[178:181], v170 offset:2048
	ds_read_b128 v[182:185], v170 offset:3072
	s_add_u32 s14, s18, 0xb0000
	s_addc_u32 s15, s19, 0
	s_mov_b32 m0, s26
	v_lshl_add_u64 v[240:241], s[14:15], 0, v[138:139]
	ds_read_b128 v[186:189], v157 offset:32768
	ds_read_b128 v[206:209], v157 offset:33792
	ds_read_b128 v[210:213], v157 offset:34816
	ds_read_b128 v[214:217], v157 offset:35840
	ds_read_b128 v[218:221], v157 offset:36864
	ds_read_b128 v[222:225], v157 offset:37888
	ds_read_b128 v[226:229], v157 offset:38912
	ds_read_b128 v[230:233], v157 offset:39936
	global_load_lds_dwordx4 v[240:241], off
	v_lshl_add_u64 v[240:241], s[14:15], 0, v[140:141]
	s_mov_b32 m0, s27
	s_nop 0
	global_load_lds_dwordx4 v[240:241], off
	s_waitcnt vmcnt(8)
	s_waitcnt lgkmcnt(0)
	s_barrier
	s_setprio 1
	s_waitcnt lgkmcnt(0)
	v_mfma_f32_16x16x32_bf16 v[126:129], v[130:133], v[186:189], v[126:129]
	v_mfma_f32_16x16x32_bf16 v[122:125], v[148:151], v[186:189], v[122:125]
	v_mfma_f32_16x16x32_bf16 v[110:113], v[130:133], v[210:213], v[110:113]
	v_mfma_f32_16x16x32_bf16 v[106:109], v[148:151], v[210:213], v[106:109]
	v_mfma_f32_16x16x32_bf16 v[94:97], v[130:133], v[218:221], v[94:97]
	v_mfma_f32_16x16x32_bf16 v[90:93], v[148:151], v[218:221], v[90:93]
	v_mfma_f32_16x16x32_bf16 v[76:79], v[130:133], v[226:229], v[76:79]
	v_mfma_f32_16x16x32_bf16 v[72:75], v[148:151], v[226:229], v[72:75]
	v_mfma_f32_16x16x32_bf16 v[126:129], v[134:137], v[206:209], v[126:129]
	v_mfma_f32_16x16x32_bf16 v[122:125], v[152:155], v[206:209], v[122:125]
	v_mfma_f32_16x16x32_bf16 v[110:113], v[134:137], v[214:217], v[110:113]
	v_mfma_f32_16x16x32_bf16 v[106:109], v[152:155], v[214:217], v[106:109]
	v_mfma_f32_16x16x32_bf16 v[94:97], v[134:137], v[222:225], v[94:97]
	v_mfma_f32_16x16x32_bf16 v[90:93], v[152:155], v[222:225], v[90:93]
	v_mfma_f32_16x16x32_bf16 v[76:79], v[134:137], v[230:233], v[76:79]
	v_mfma_f32_16x16x32_bf16 v[72:75], v[152:155], v[230:233], v[72:75]
	v_mfma_f32_16x16x32_bf16 v[118:121], v[158:161], v[186:189], v[118:121]
	v_mfma_f32_16x16x32_bf16 v[114:117], v[178:181], v[186:189], v[114:117]
	v_mfma_f32_16x16x32_bf16 v[102:105], v[158:161], v[210:213], v[102:105]
	v_mfma_f32_16x16x32_bf16 v[98:101], v[178:181], v[210:213], v[98:101]
	v_mfma_f32_16x16x32_bf16 v[86:89], v[158:161], v[218:221], v[86:89]
	v_mfma_f32_16x16x32_bf16 v[82:85], v[178:181], v[218:221], v[82:85]
	v_mfma_f32_16x16x32_bf16 v[68:71], v[158:161], v[226:229], v[68:71]
	v_mfma_f32_16x16x32_bf16 v[64:67], v[178:181], v[226:229], v[64:67]
	v_mfma_f32_16x16x32_bf16 v[118:121], v[174:177], v[206:209], v[118:121]
	v_mfma_f32_16x16x32_bf16 v[114:117], v[182:185], v[206:209], v[114:117]
	v_mfma_f32_16x16x32_bf16 v[102:105], v[174:177], v[214:217], v[102:105]
	v_mfma_f32_16x16x32_bf16 v[98:101], v[182:185], v[214:217], v[98:101]
	v_mfma_f32_16x16x32_bf16 v[86:89], v[174:177], v[222:225], v[86:89]
	v_mfma_f32_16x16x32_bf16 v[82:85], v[182:185], v[222:225], v[82:85]
	v_mfma_f32_16x16x32_bf16 v[68:71], v[174:177], v[230:233], v[68:71]
	v_mfma_f32_16x16x32_bf16 v[64:67], v[182:185], v[230:233], v[64:67]
	s_setprio 0
	s_barrier
; #define PG8_STAGE(bufoff, gbase, voff) do { _Pragma("unroll") for (int _i = 0; _i < 2; ++_i) \
;         __builtin_amdgcn_global_load_lds((const unsigned*)((const char*)(gbase) + (voff)[_i]), (PG8_LAS unsigned*)(lds + (bufoff) + ldsw + _i * 8192), 16, 0, 0); } while (0)
; #define PG8_LDA(dst, b, h) do { if constexpr (FP8) { _Pragma("unroll") for (int m = 0; m < 4; ++m) dst##8[m] = pg8_ld8(lds + PG8_SA(b, h) + aoff + m * 2048); } \
;         else { _Pragma("unroll") for (int m = 0; m < 4; ++m) _Pragma("unroll") for (int k = 0; k < 2; ++k) dst[m][k] = *(const PG8_LAS bf16x8*)(lds + PG8_SA(b, h) + aoff + m * 2048 + k * 1024); } } while (0)
; #define PG8_WAIT_V(n) asm volatile("s_waitcnt vmcnt(" #n ")" ::: "memory")
; #define PG8_WAIT_L(n) asm volatile("s_waitcnt lgkmcnt(" #n ")" ::: "memory")
; #define PG8_BAR __builtin_amdgcn_s_barrier()
; #define PG8_SCHED __builtin_amdgcn_sched_barrier(0)
;     ...
;             PG8_LDA(At, 1, 1); PG8_STAGE(PG8_SB(1, 0), b3, voffB); PG8_STAGE(PG8_SB(1, 1), b3 + hstep, voffB); PG8_STAGE(PG8_SA(1, 0), a3, voffA);
;             PG8_WAIT_V(8); PG8_WAIT_L(0); PG8_BAR; PG8_MMA(1, 0, At, B0); PG8_MMA(1, 1, At, B1); PG8_BAR; PG8_SCHED;
;     ...
;         if constexpr (ALIGN_EPI) { if (wr == 0) PG8_BAR; }
	s_add_i32 s14, s44, s23
	v_lshl_add_u64 v[190:191], v[190:191], 0, s[86:87]
	s_mov_b32 m0, s14
	ds_read_b128 v[186:189], v157 offset:49152
	ds_read_b128 v[206:209], v157 offset:50176
	ds_read_b128 v[210:213], v157 offset:51200
	ds_read_b128 v[214:217], v157 offset:52224
	ds_read_b128 v[218:221], v157 offset:53248
	ds_read_b128 v[222:225], v157 offset:54272
	ds_read_b128 v[226:229], v157 offset:55296
	ds_read_b128 v[230:233], v157 offset:56320
	global_load_lds_dwordx4 v[190:191], off
	s_add_i32 m0, s14, 0x2000
	s_add_u32 s14, s16, 0xb0080
	v_lshl_add_u64 v[190:191], v[234:235], 0, s[86:87]
	s_addc_u32 s15, s17, 0
	s_add_i32 s16, s45, s23
	global_load_lds_dwordx4 v[190:191], off
	v_lshl_add_u64 v[190:191], s[14:15], 0, v[80:81]
	s_mov_b32 m0, s16
	s_nop 0
	global_load_lds_dwordx4 v[190:191], off
	v_lshl_add_u64 v[190:191], s[14:15], 0, v[142:143]
	s_add_i32 m0, s16, 0x2000
	s_nop 0
	global_load_lds_dwordx4 v[190:191], off
	v_lshl_add_u64 v[190:191], v[236:237], 0, s[86:87]
	s_mov_b32 m0, s31
	s_nop 0
	global_load_lds_dwordx4 v[190:191], off
	v_lshl_add_u64 v[190:191], v[238:239], 0, s[86:87]
	s_mov_b32 m0, s34
	s_nop 0
	global_load_lds_dwordx4 v[190:191], off
	s_waitcnt vmcnt(8)
	s_waitcnt lgkmcnt(0)
	s_barrier
	s_setprio 1
	s_waitcnt lgkmcnt(0)
	v_mfma_f32_16x16x32_bf16 v[60:63], v[130:133], v[186:189], v[60:63]
	v_mfma_f32_16x16x32_bf16 v[56:59], v[148:151], v[186:189], v[56:59]
	v_mfma_f32_16x16x32_bf16 v[44:47], v[130:133], v[210:213], v[44:47]
	v_mfma_f32_16x16x32_bf16 v[40:43], v[148:151], v[210:213], v[40:43]
	v_mfma_f32_16x16x32_bf16 v[28:31], v[130:133], v[218:221], v[28:31]
	v_mfma_f32_16x16x32_bf16 v[24:27], v[148:151], v[218:221], v[24:27]
	v_mfma_f32_16x16x32_bf16 v[12:15], v[130:133], v[226:229], v[12:15]
	v_mfma_f32_16x16x32_bf16 v[8:11], v[148:151], v[226:229], v[8:11]
	v_mfma_f32_16x16x32_bf16 v[60:63], v[134:137], v[206:209], v[60:63]
	v_mfma_f32_16x16x32_bf16 v[56:59], v[152:155], v[206:209], v[56:59]
	v_mfma_f32_16x16x32_bf16 v[44:47], v[134:137], v[214:217], v[44:47]
	v_mfma_f32_16x16x32_bf16 v[40:43], v[152:155], v[214:217], v[40:43]
	v_mfma_f32_16x16x32_bf16 v[28:31], v[134:137], v[222:225], v[28:31]
	v_mfma_f32_16x16x32_bf16 v[24:27], v[152:155], v[222:225], v[24:27]
	v_mfma_f32_16x16x32_bf16 v[12:15], v[134:137], v[230:233], v[12:15]
	v_mfma_f32_16x16x32_bf16 v[8:11], v[152:155], v[230:233], v[8:11]
	v_mfma_f32_16x16x32_bf16 v[52:55], v[158:161], v[186:189], v[52:55]
	v_mfma_f32_16x16x32_bf16 v[48:51], v[178:181], v[186:189], v[48:51]
	v_mfma_f32_16x16x32_bf16 v[36:39], v[158:161], v[210:213], v[36:39]
	v_mfma_f32_16x16x32_bf16 v[32:35], v[178:181], v[210:213], v[32:35]
	v_mfma_f32_16x16x32_bf16 v[20:23], v[158:161], v[218:221], v[20:23]
	v_mfma_f32_16x16x32_bf16 v[16:19], v[178:181], v[218:221], v[16:19]
	v_mfma_f32_16x16x32_bf16 v[4:7], v[158:161], v[226:229], v[4:7]
	v_mfma_f32_16x16x32_bf16 v[0:3], v[178:181], v[226:229], v[0:3]
	v_mfma_f32_16x16x32_bf16 v[52:55], v[174:177], v[206:209], v[52:55]
	v_mfma_f32_16x16x32_bf16 v[48:51], v[182:185], v[206:209], v[48:51]
	v_mfma_f32_16x16x32_bf16 v[36:39], v[174:177], v[214:217], v[36:39]
	v_mfma_f32_16x16x32_bf16 v[32:35], v[182:185], v[214:217], v[32:35]
	v_mfma_f32_16x16x32_bf16 v[20:23], v[174:177], v[222:225], v[20:23]
	v_mfma_f32_16x16x32_bf16 v[16:19], v[182:185], v[222:225], v[16:19]
	v_mfma_f32_16x16x32_bf16 v[4:7], v[174:177], v[230:233], v[4:7]
	v_mfma_f32_16x16x32_bf16 v[0:3], v[182:185], v[230:233], v[0:3]
	s_setprio 0
	s_barrier
	s_add_i32 s43, s43, 2
	s_add_u32 s41, s41, 0x100
	s_addc_u32 s42, s42, 0
	s_cmp_gt_u32 s43, 41
	s_mov_b64 s[14:15], s[0:1]
	s_cbranch_scc0 .LBB0_1109
	s_and_b64 vcc, exec, s[10:11]
	s_cbranch_vccz .LBB0_1112
	s_barrier

; #define PG8_STAGE(bufoff, gbase, voff) do { _Pragma("unroll") for (int _i = 0; _i < 2; ++_i) \
;         __builtin_amdgcn_global_load_lds((const unsigned*)((const char*)(gbase) + (voff)[_i]), (PG8_LAS unsigned*)(lds + (bufoff) + ldsw + _i * 8192), 16, 0, 0); } while (0)
; #define PG8_LDA(dst, b, h) do { if constexpr (FP8) { _Pragma("unroll") for (int m = 0; m < 4; ++m) dst##8[m] = pg8_ld8(lds + PG8_SA(b, h) + aoff + m * 2048); } \
;         else { _Pragma("unroll") for (int m = 0; m < 4; ++m) _Pragma("unroll") for (int k = 0; k < 2; ++k) dst[m][k] = *(const PG8_LAS bf16x8*)(lds + PG8_SA(b, h) + aoff + m * 2048 + k * 1024); } } while (0)
; #define PG8_LDB(dst, b, h) do { if constexpr (FP8) { _Pragma("unroll") for (int n = 0; n < 2; ++n) dst##8[n] = pg8_ld8(lds + PG8_SB(b, h) + boff + n * 2048); } \
;         else { _Pragma("unroll") for (int n = 0; n < 2; ++n) _Pragma("unroll") for (int k = 0; k < 2; ++k) dst[n][k] = *(const PG8_LAS bf16x8*)(lds + PG8_SB(b, h) + boff + n * 2048 + k * 1024); } } while (0)
; #define PG8_WAIT_V(n) asm volatile("s_waitcnt vmcnt(" #n ")" ::: "memory")
; #define PG8_WAIT_L(n) asm volatile("s_waitcnt lgkmcnt(" #n ")" ::: "memory")
; #define PG8_BAR __builtin_amdgcn_s_barrier()
; #define PG8_SCHED __builtin_amdgcn_sched_barrier(0)
;     ...
;             const bool last = (t == nt - 2);
;             const char* a1 = cA + (size_t)(t + 1) * kstep;
;             const char* a2 = last ? nA : cA + (size_t)(t + 2) * kstep; const char* b2 = last ? nB : cB + (size_t)(t + 2) * kstep;
;             const char* a3 = a2 + kstep; const char* b3 = b2 + kstep;
;             if (last && has_next) S.a_ready(nxt);
;             if constexpr (SP2) {
;             PG8_LDB(B0, 0, 0); PG8_LDB(B1, 0, 1); PG8_SCHED; PG8_LDA(At, 0, 0); PG8_STAGE(PG8_SA(1, 1), a1 + hstep, voffA);
;             PG8_WAIT_V(8); PG8_WAIT_L(0); PG8_BAR; PG8_MMA(0, 0, At, B0); PG8_MMA(0, 1, At, B1); PG8_BAR; PG8_SCHED;
;             PG8_LDA(At, 0, 1); PG8_STAGE(PG8_SB(0, 0), b2, voffB); PG8_STAGE(PG8_SB(0, 1), b2 + hstep, voffB); PG8_STAGE(PG8_SA(0, 0), a2, voffA);
.LBB0_1280:
	s_add_u32 s0, s22, 0xfffc0080
	s_addc_u32 s1, s23, -1
	s_add_i32 s47, 0, 0x10000
	s_cmp_eq_u32 s46, 12
	s_cselect_b32 s25, s13, s1
	s_cselect_b32 s24, s42, s0
	s_cselect_b32 s1, s11, s45
	s_cselect_b32 s0, s43, s44
	s_add_i32 s50, 0, 0x14000
	v_add_u32_e32 v152, s47, v156
	v_add_u32_e32 v170, s50, v156
	ds_read_b128 v[130:133], v152
	ds_read_b128 v[134:137], v152 offset:1024
	ds_read_b128 v[148:151], v152 offset:2048
	ds_read_b128 v[152:155], v152 offset:3072
	ds_read_b128 v[158:161], v170
	ds_read_b128 v[174:177], v170 offset:1024
	ds_read_b128 v[178:181], v170 offset:2048
	ds_read_b128 v[182:185], v170 offset:3072
	v_lshl_add_u64 v[190:191], s[22:23], 0, v[146:147]
	s_add_i32 m0, s19, 0xc000
	ds_read_b128 v[186:189], v157
	ds_read_b128 v[206:209], v157 offset:1024
	ds_read_b128 v[210:213], v157 offset:2048
	ds_read_b128 v[214:217], v157 offset:3072
	ds_read_b128 v[218:221], v157 offset:4096
	ds_read_b128 v[222:225], v157 offset:5120
	ds_read_b128 v[226:229], v157 offset:6144
	ds_read_b128 v[230:233], v157 offset:7168
	global_load_lds_dwordx4 v[190:191], off
	v_lshl_add_u64 v[190:191], s[22:23], 0, v[144:145]
	s_add_i32 m0, s19, 0xe000
	s_nop 0
	global_load_lds_dwordx4 v[190:191], off
	s_waitcnt vmcnt(8)
	s_waitcnt lgkmcnt(0)
	s_barrier
	s_setprio 1
	s_waitcnt lgkmcnt(0)
	v_mfma_f32_16x16x32_f16 v[126:129], v[130:133], v[186:189], v[126:129]
	v_mfma_f32_16x16x32_f16 v[122:125], v[148:151], v[186:189], v[122:125]
	v_mfma_f32_16x16x32_f16 v[110:113], v[130:133], v[210:213], v[110:113]
	v_mfma_f32_16x16x32_f16 v[106:109], v[148:151], v[210:213], v[106:109]
	v_mfma_f32_16x16x32_f16 v[94:97], v[130:133], v[218:221], v[94:97]
	v_mfma_f32_16x16x32_f16 v[90:93], v[148:151], v[218:221], v[90:93]
	v_mfma_f32_16x16x32_f16 v[76:79], v[130:133], v[226:229], v[76:79]
	v_mfma_f32_16x16x32_f16 v[72:75], v[148:151], v[226:229], v[72:75]
	v_mfma_f32_16x16x32_f16 v[126:129], v[134:137], v[206:209], v[126:129]
	v_mfma_f32_16x16x32_f16 v[122:125], v[152:155], v[206:209], v[122:125]
	v_mfma_f32_16x16x32_f16 v[110:113], v[134:137], v[214:217], v[110:113]
	v_mfma_f32_16x16x32_f16 v[106:109], v[152:155], v[214:217], v[106:109]
	v_mfma_f32_16x16x32_f16 v[94:97], v[134:137], v[222:225], v[94:97]
	v_mfma_f32_16x16x32_f16 v[90:93], v[152:155], v[222:225], v[90:93]
	v_mfma_f32_16x16x32_f16 v[76:79], v[134:137], v[230:233], v[76:79]
	v_mfma_f32_16x16x32_f16 v[72:75], v[152:155], v[230:233], v[72:75]
	v_mfma_f32_16x16x32_f16 v[118:121], v[158:161], v[186:189], v[118:121]
	v_mfma_f32_16x16x32_f16 v[114:117], v[178:181], v[186:189], v[114:117]
	v_mfma_f32_16x16x32_f16 v[102:105], v[158:161], v[210:213], v[102:105]
	v_mfma_f32_16x16x32_f16 v[98:101], v[178:181], v[210:213], v[98:101]
	v_mfma_f32_16x16x32_f16 v[86:89], v[158:161], v[218:221], v[86:89]
	v_mfma_f32_16x16x32_f16 v[82:85], v[178:181], v[218:221], v[82:85]
	v_mfma_f32_16x16x32_f16 v[68:71], v[158:161], v[226:229], v[68:71]
	v_mfma_f32_16x16x32_f16 v[64:67], v[178:181], v[226:229], v[64:67]
	v_mfma_f32_16x16x32_f16 v[118:121], v[174:177], v[206:209], v[118:121]
	v_mfma_f32_16x16x32_f16 v[114:117], v[182:185], v[206:209], v[114:117]
	v_mfma_f32_16x16x32_f16 v[102:105], v[174:177], v[214:217], v[102:105]
	v_mfma_f32_16x16x32_f16 v[98:101], v[182:185], v[214:217], v[98:101]
	v_mfma_f32_16x16x32_f16 v[86:89], v[174:177], v[222:225], v[86:89]
	v_mfma_f32_16x16x32_f16 v[82:85], v[182:185], v[222:225], v[82:85]
	v_mfma_f32_16x16x32_f16 v[68:71], v[174:177], v[230:233], v[68:71]
	v_mfma_f32_16x16x32_f16 v[64:67], v[182:185], v[230:233], v[64:67]
	s_setprio 0
	s_barrier
	s_add_i32 s47, s47, s28
	v_lshl_add_u64 v[190:191], s[0:1], 0, v[80:81]
	s_mov_b32 m0, s47
	ds_read_b128 v[186:189], v157 offset:16384
	ds_read_b128 v[206:209], v157 offset:17408
	ds_read_b128 v[210:213], v157 offset:18432
	ds_read_b128 v[214:217], v157 offset:19456
	ds_read_b128 v[218:221], v157 offset:20480
	ds_read_b128 v[222:225], v157 offset:21504
	ds_read_b128 v[226:229], v157 offset:22528
	ds_read_b128 v[230:233], v157 offset:23552
	global_load_lds_dwordx4 v[190:191], off
	s_add_i32 m0, s47, 0x2000
	s_add_u32 s48, s0, 0x40000
	v_lshl_add_u64 v[234:235], s[0:1], 0, v[142:143]
	s_addc_u32 s49, s1, 0
	s_add_i32 s47, s50, s28
	global_load_lds_dwordx4 v[234:235], off
	v_lshl_add_u64 v[236:237], s[48:49], 0, v[80:81]
	s_mov_b32 m0, s47
	v_lshl_add_u64 v[238:239], s[24:25], 0, v[140:141]
	global_load_lds_dwordx4 v[236:237], off
	v_lshl_add_u64 v[236:237], s[48:49], 0, v[142:143]
	s_add_i32 m0, s47, 0x2000
	s_nop 0
	global_load_lds_dwordx4 v[236:237], off
	v_lshl_add_u64 v[236:237], s[24:25], 0, v[138:139]
	s_mov_b32 m0, s19
	s_nop 0
	global_load_lds_dwordx4 v[236:237], off
	s_mov_b32 m0, s21
	s_nop 0
	global_load_lds_dwordx4 v[238:239], off
	s_waitcnt vmcnt(8)
	s_waitcnt lgkmcnt(0)
	s_barrier
; #define PG8_STAGE(bufoff, gbase, voff) do { _Pragma("unroll") for (int _i = 0; _i < 2; ++_i) \
;         __builtin_amdgcn_global_load_lds((const unsigned*)((const char*)(gbase) + (voff)[_i]), (PG8_LAS unsigned*)(lds + (bufoff) + ldsw + _i * 8192), 16, 0, 0); } while (0)
; #define PG8_LDA(dst, b, h) do { if constexpr (FP8) { _Pragma("unroll") for (int m = 0; m < 4; ++m) dst##8[m] = pg8_ld8(lds + PG8_SA(b, h) + aoff + m * 2048); } \
;         else { _Pragma("unroll") for (int m = 0; m < 4; ++m) _Pragma("unroll") for (int k = 0; k < 2; ++k) dst[m][k] = *(const PG8_LAS bf16x8*)(lds + PG8_SA(b, h) + aoff + m * 2048 + k * 1024); } } while (0)
; #define PG8_LDB(dst, b, h) do { if constexpr (FP8) { _Pragma("unroll") for (int n = 0; n < 2; ++n) dst##8[n] = pg8_ld8(lds + PG8_SB(b, h) + boff + n * 2048); } \
;         else { _Pragma("unroll") for (int n = 0; n < 2; ++n) _Pragma("unroll") for (int k = 0; k < 2; ++k) dst[n][k] = *(const PG8_LAS bf16x8*)(lds + PG8_SB(b, h) + boff + n * 2048 + k * 1024); } } while (0)
; #define PG8_WAIT_V(n) asm volatile("s_waitcnt vmcnt(" #n ")" ::: "memory")
; #define PG8_WAIT_L(n) asm volatile("s_waitcnt lgkmcnt(" #n ")" ::: "memory")
; #define PG8_BAR __builtin_amdgcn_s_barrier()
; #define PG8_SCHED __builtin_amdgcn_sched_barrier(0)
;     ...
;             PG8_WAIT_V(8); PG8_WAIT_L(0); PG8_BAR; PG8_MMA(1, 0, At, B0); PG8_MMA(1, 1, At, B1); PG8_BAR; PG8_SCHED;
;             PG8_LDB(B0, 1, 0); PG8_LDB(B1, 1, 1); PG8_SCHED; PG8_LDA(At, 1, 0); PG8_STAGE(PG8_SA(0, 1), a2 + hstep, voffA);
;             PG8_WAIT_V(8); PG8_WAIT_L(0); PG8_BAR; PG8_MMA(0, 0, At, B0); PG8_MMA(0, 1, At, B1); PG8_BAR; PG8_SCHED;
	s_setprio 1
	s_waitcnt lgkmcnt(0)
	v_mfma_f32_16x16x32_f16 v[60:63], v[130:133], v[186:189], v[60:63]
	v_mfma_f32_16x16x32_f16 v[56:59], v[148:151], v[186:189], v[56:59]
	v_mfma_f32_16x16x32_f16 v[44:47], v[130:133], v[210:213], v[44:47]
	v_mfma_f32_16x16x32_f16 v[40:43], v[148:151], v[210:213], v[40:43]
	v_mfma_f32_16x16x32_f16 v[28:31], v[130:133], v[218:221], v[28:31]
	v_mfma_f32_16x16x32_f16 v[24:27], v[148:151], v[218:221], v[24:27]
	v_mfma_f32_16x16x32_f16 v[12:15], v[130:133], v[226:229], v[12:15]
	v_mfma_f32_16x16x32_f16 v[8:11], v[148:151], v[226:229], v[8:11]
	v_mfma_f32_16x16x32_f16 v[60:63], v[134:137], v[206:209], v[60:63]
	v_mfma_f32_16x16x32_f16 v[56:59], v[152:155], v[206:209], v[56:59]
	v_mfma_f32_16x16x32_f16 v[44:47], v[134:137], v[214:217], v[44:47]
	v_mfma_f32_16x16x32_f16 v[40:43], v[152:155], v[214:217], v[40:43]
	v_mfma_f32_16x16x32_f16 v[28:31], v[134:137], v[222:225], v[28:31]
	v_mfma_f32_16x16x32_f16 v[24:27], v[152:155], v[222:225], v[24:27]
	v_mfma_f32_16x16x32_f16 v[12:15], v[134:137], v[230:233], v[12:15]
	v_mfma_f32_16x16x32_f16 v[8:11], v[152:155], v[230:233], v[8:11]
	v_mfma_f32_16x16x32_f16 v[52:55], v[158:161], v[186:189], v[52:55]
	v_mfma_f32_16x16x32_f16 v[48:51], v[178:181], v[186:189], v[48:51]
	v_mfma_f32_16x16x32_f16 v[36:39], v[158:161], v[210:213], v[36:39]
	v_mfma_f32_16x16x32_f16 v[32:35], v[178:181], v[210:213], v[32:35]
	v_mfma_f32_16x16x32_f16 v[20:23], v[158:161], v[218:221], v[20:23]
	v_mfma_f32_16x16x32_f16 v[16:19], v[178:181], v[218:221], v[16:19]
	v_mfma_f32_16x16x32_f16 v[4:7], v[158:161], v[226:229], v[4:7]
	v_mfma_f32_16x16x32_f16 v[0:3], v[178:181], v[226:229], v[0:3]
	v_mfma_f32_16x16x32_f16 v[52:55], v[174:177], v[206:209], v[52:55]
	v_mfma_f32_16x16x32_f16 v[48:51], v[182:185], v[206:209], v[48:51]
	v_mfma_f32_16x16x32_f16 v[36:39], v[174:177], v[214:217], v[36:39]
	v_mfma_f32_16x16x32_f16 v[32:35], v[182:185], v[214:217], v[32:35]
	v_mfma_f32_16x16x32_f16 v[20:23], v[174:177], v[222:225], v[20:23]
	v_mfma_f32_16x16x32_f16 v[16:19], v[182:185], v[222:225], v[16:19]
	v_mfma_f32_16x16x32_f16 v[4:7], v[174:177], v[230:233], v[4:7]
	v_mfma_f32_16x16x32_f16 v[0:3], v[182:185], v[230:233], v[0:3]
	s_setprio 0
	s_barrier
	s_add_i32 s47, 0, 0x18000
	s_add_i32 s48, 0, 0x1c000
	v_add_u32_e32 v152, s47, v156
	v_add_u32_e32 v170, s48, v156
	ds_read_b128 v[130:133], v152
	ds_read_b128 v[134:137], v152 offset:1024
	ds_read_b128 v[148:151], v152 offset:2048
	ds_read_b128 v[152:155], v152 offset:3072
	ds_read_b128 v[158:161], v170
	ds_read_b128 v[174:177], v170 offset:1024
	ds_read_b128 v[178:181], v170 offset:2048
	ds_read_b128 v[182:185], v170 offset:3072
	s_add_u32 s24, s24, 0x40000
	s_addc_u32 s25, s25, 0
	s_mov_b32 m0, s31
	v_lshl_add_u64 v[240:241], s[24:25], 0, v[138:139]
	ds_read_b128 v[186:189], v157 offset:32768
	ds_read_b128 v[206:209], v157 offset:33792
	ds_read_b128 v[210:213], v157 offset:34816
	ds_read_b128 v[214:217], v157 offset:35840
	ds_read_b128 v[218:221], v157 offset:36864
	ds_read_b128 v[222:225], v157 offset:37888
	ds_read_b128 v[226:229], v157 offset:38912
	ds_read_b128 v[230:233], v157 offset:39936
	global_load_lds_dwordx4 v[240:241], off
	v_lshl_add_u64 v[240:241], s[24:25], 0, v[140:141]
	s_mov_b32 m0, s34
	s_nop 0
	global_load_lds_dwordx4 v[240:241], off
	s_waitcnt vmcnt(8)
	s_waitcnt lgkmcnt(0)
	s_barrier
	s_setprio 1
	s_waitcnt lgkmcnt(0)
	v_mfma_f32_16x16x32_f16 v[126:129], v[130:133], v[186:189], v[126:129]
	v_mfma_f32_16x16x32_f16 v[122:125], v[148:151], v[186:189], v[122:125]
	v_mfma_f32_16x16x32_f16 v[110:113], v[130:133], v[210:213], v[110:113]
	v_mfma_f32_16x16x32_f16 v[106:109], v[148:151], v[210:213], v[106:109]
	v_mfma_f32_16x16x32_f16 v[94:97], v[130:133], v[218:221], v[94:97]
	v_mfma_f32_16x16x32_f16 v[90:93], v[148:151], v[218:221], v[90:93]
	v_mfma_f32_16x16x32_f16 v[76:79], v[130:133], v[226:229], v[76:79]
	v_mfma_f32_16x16x32_f16 v[72:75], v[148:151], v[226:229], v[72:75]
	v_mfma_f32_16x16x32_f16 v[126:129], v[134:137], v[206:209], v[126:129]
	v_mfma_f32_16x16x32_f16 v[122:125], v[152:155], v[206:209], v[122:125]
	v_mfma_f32_16x16x32_f16 v[110:113], v[134:137], v[214:217], v[110:113]
	v_mfma_f32_16x16x32_f16 v[106:109], v[152:155], v[214:217], v[106:109]
	v_mfma_f32_16x16x32_f16 v[94:97], v[134:137], v[222:225], v[94:97]
	v_mfma_f32_16x16x32_f16 v[90:93], v[152:155], v[222:225], v[90:93]
	v_mfma_f32_16x16x32_f16 v[76:79], v[134:137], v[230:233], v[76:79]
	v_mfma_f32_16x16x32_f16 v[72:75], v[152:155], v[230:233], v[72:75]
	v_mfma_f32_16x16x32_f16 v[118:121], v[158:161], v[186:189], v[118:121]
	v_mfma_f32_16x16x32_f16 v[114:117], v[178:181], v[186:189], v[114:117]
	v_mfma_f32_16x16x32_f16 v[102:105], v[158:161], v[210:213], v[102:105]
	v_mfma_f32_16x16x32_f16 v[98:101], v[178:181], v[210:213], v[98:101]
	v_mfma_f32_16x16x32_f16 v[86:89], v[158:161], v[218:221], v[86:89]
	v_mfma_f32_16x16x32_f16 v[82:85], v[178:181], v[218:221], v[82:85]
	v_mfma_f32_16x16x32_f16 v[68:71], v[158:161], v[226:229], v[68:71]
	v_mfma_f32_16x16x32_f16 v[64:67], v[178:181], v[226:229], v[64:67]
	v_mfma_f32_16x16x32_f16 v[118:121], v[174:177], v[206:209], v[118:121]
	v_mfma_f32_16x16x32_f16 v[114:117], v[182:185], v[206:209], v[114:117]
	v_mfma_f32_16x16x32_f16 v[102:105], v[174:177], v[214:217], v[102:105]
	v_mfma_f32_16x16x32_f16 v[98:101], v[182:185], v[214:217], v[98:101]
	v_mfma_f32_16x16x32_f16 v[86:89], v[174:177], v[222:225], v[86:89]
	v_mfma_f32_16x16x32_f16 v[82:85], v[182:185], v[222:225], v[82:85]
	v_mfma_f32_16x16x32_f16 v[68:71], v[174:177], v[230:233], v[68:71]
	v_mfma_f32_16x16x32_f16 v[64:67], v[182:185], v[230:233], v[64:67]
	s_setprio 0
	s_barrier
; #define PG8_STAGE(bufoff, gbase, voff) do { _Pragma("unroll") for (int _i = 0; _i < 2; ++_i) \
;         __builtin_amdgcn_global_load_lds((const unsigned*)((const char*)(gbase) + (voff)[_i]), (PG8_LAS unsigned*)(lds + (bufoff) + ldsw + _i * 8192), 16, 0, 0); } while (0)
; #define PG8_LDA(dst, b, h) do { if constexpr (FP8) { _Pragma("unroll") for (int m = 0; m < 4; ++m) dst##8[m] = pg8_ld8(lds + PG8_SA(b, h) + aoff + m * 2048); } \
;         else { _Pragma("unroll") for (int m = 0; m < 4; ++m) _Pragma("unroll") for (int k = 0; k < 2; ++k) dst[m][k] = *(const PG8_LAS bf16x8*)(lds + PG8_SA(b, h) + aoff + m * 2048 + k * 1024); } } while (0)
; #define PG8_WAIT_V(n) asm volatile("s_waitcnt vmcnt(" #n ")" ::: "memory")
; #define PG8_WAIT_L(n) asm volatile("s_waitcnt lgkmcnt(" #n ")" ::: "memory")
; #define PG8_BAR __builtin_amdgcn_s_barrier()
; #define PG8_SCHED __builtin_amdgcn_sched_barrier(0)
;     ...
;         for (int t = 0; t < nt; t += 2) {
;             if constexpr (MID) { if (t == (nt >> 1)) E.mid(acc, cur, wr, wc); }
;             const bool last = (t == nt - 2);
;             const char* a1 = cA + (size_t)(t + 1) * kstep;
;             const char* a2 = last ? nA : cA + (size_t)(t + 2) * kstep; const char* b2 = last ? nB : cB + (size_t)(t + 2) * kstep;
;     ...
;             PG8_LDA(At, 1, 1); PG8_STAGE(PG8_SB(1, 0), b3, voffB); PG8_STAGE(PG8_SB(1, 1), b3 + hstep, voffB); PG8_STAGE(PG8_SA(1, 0), a3, voffA);
;             PG8_WAIT_V(8); PG8_WAIT_L(0); PG8_BAR; PG8_MMA(1, 0, At, B0); PG8_MMA(1, 1, At, B1); PG8_BAR; PG8_SCHED;
	s_add_i32 s24, s47, s28
	v_lshl_add_u64 v[190:191], v[190:191], 0, s[86:87]
	s_mov_b32 m0, s24
	ds_read_b128 v[186:189], v157 offset:49152
	ds_read_b128 v[206:209], v157 offset:50176
	ds_read_b128 v[210:213], v157 offset:51200
	ds_read_b128 v[214:217], v157 offset:52224
	ds_read_b128 v[218:221], v157 offset:53248
	ds_read_b128 v[222:225], v157 offset:54272
	ds_read_b128 v[226:229], v157 offset:55296
	ds_read_b128 v[230:233], v157 offset:56320
	global_load_lds_dwordx4 v[190:191], off
	s_add_i32 m0, s24, 0x2000
	s_add_u32 s0, s0, 0x40080
	v_lshl_add_u64 v[190:191], v[234:235], 0, s[86:87]
	s_addc_u32 s1, s1, 0
	s_add_i32 s24, s48, s28
	global_load_lds_dwordx4 v[190:191], off
	v_lshl_add_u64 v[190:191], s[0:1], 0, v[80:81]
	s_mov_b32 m0, s24
	s_nop 0
	global_load_lds_dwordx4 v[190:191], off
	v_lshl_add_u64 v[190:191], s[0:1], 0, v[142:143]
	s_add_i32 m0, s24, 0x2000
	s_nop 0
	global_load_lds_dwordx4 v[190:191], off
	v_lshl_add_u64 v[190:191], v[236:237], 0, s[86:87]
	s_mov_b32 m0, s38
	s_nop 0
	global_load_lds_dwordx4 v[190:191], off
	v_lshl_add_u64 v[190:191], v[238:239], 0, s[86:87]
	s_mov_b32 m0, s39
	s_nop 0
	global_load_lds_dwordx4 v[190:191], off
	s_waitcnt vmcnt(8)
	s_waitcnt lgkmcnt(0)
	s_barrier
	s_setprio 1
	s_waitcnt lgkmcnt(0)
	v_mfma_f32_16x16x32_f16 v[60:63], v[130:133], v[186:189], v[60:63]
	v_mfma_f32_16x16x32_f16 v[56:59], v[148:151], v[186:189], v[56:59]
	v_mfma_f32_16x16x32_f16 v[44:47], v[130:133], v[210:213], v[44:47]
	v_mfma_f32_16x16x32_f16 v[40:43], v[148:151], v[210:213], v[40:43]
	v_mfma_f32_16x16x32_f16 v[28:31], v[130:133], v[218:221], v[28:31]
	v_mfma_f32_16x16x32_f16 v[24:27], v[148:151], v[218:221], v[24:27]
	v_mfma_f32_16x16x32_f16 v[12:15], v[130:133], v[226:229], v[12:15]
	v_mfma_f32_16x16x32_f16 v[8:11], v[148:151], v[226:229], v[8:11]
	v_mfma_f32_16x16x32_f16 v[60:63], v[134:137], v[206:209], v[60:63]
	v_mfma_f32_16x16x32_f16 v[56:59], v[152:155], v[206:209], v[56:59]
	v_mfma_f32_16x16x32_f16 v[44:47], v[134:137], v[214:217], v[44:47]
	v_mfma_f32_16x16x32_f16 v[40:43], v[152:155], v[214:217], v[40:43]
	v_mfma_f32_16x16x32_f16 v[28:31], v[134:137], v[222:225], v[28:31]
	v_mfma_f32_16x16x32_f16 v[24:27], v[152:155], v[222:225], v[24:27]
	v_mfma_f32_16x16x32_f16 v[12:15], v[134:137], v[230:233], v[12:15]
	v_mfma_f32_16x16x32_f16 v[8:11], v[152:155], v[230:233], v[8:11]
	v_mfma_f32_16x16x32_f16 v[52:55], v[158:161], v[186:189], v[52:55]
	v_mfma_f32_16x16x32_f16 v[48:51], v[178:181], v[186:189], v[48:51]
	v_mfma_f32_16x16x32_f16 v[36:39], v[158:161], v[210:213], v[36:39]
	v_mfma_f32_16x16x32_f16 v[32:35], v[178:181], v[210:213], v[32:35]
	v_mfma_f32_16x16x32_f16 v[20:23], v[158:161], v[218:221], v[20:23]
	v_mfma_f32_16x16x32_f16 v[16:19], v[178:181], v[218:221], v[16:19]
	v_mfma_f32_16x16x32_f16 v[4:7], v[158:161], v[226:229], v[4:7]
	v_mfma_f32_16x16x32_f16 v[0:3], v[178:181], v[226:229], v[0:3]
	v_mfma_f32_16x16x32_f16 v[52:55], v[174:177], v[206:209], v[52:55]
	v_mfma_f32_16x16x32_f16 v[48:51], v[182:185], v[206:209], v[48:51]
	v_mfma_f32_16x16x32_f16 v[36:39], v[174:177], v[214:217], v[36:39]
	v_mfma_f32_16x16x32_f16 v[32:35], v[182:185], v[214:217], v[32:35]
	v_mfma_f32_16x16x32_f16 v[20:23], v[174:177], v[222:225], v[20:23]
	v_mfma_f32_16x16x32_f16 v[16:19], v[182:185], v[222:225], v[16:19]
	v_mfma_f32_16x16x32_f16 v[4:7], v[174:177], v[230:233], v[4:7]
	v_mfma_f32_16x16x32_f16 v[0:3], v[182:185], v[230:233], v[0:3]
	s_setprio 0
	s_barrier
	s_add_i32 s46, s46, 2
	s_add_u32 s44, s44, 0x100
	s_addc_u32 s45, s45, 0
	s_add_u32 s22, s22, 0x100
	s_addc_u32 s23, s23, 0
	s_cmp_gt_u32 s46, 13
	s_cbranch_scc0 .LBB0_1280
	s_and_b64 vcc, exec, s[8:9]
	s_cbranch_vccz .LBB0_1283
	s_barrier
